# expert conversion rewrite plus attention P-fragment permlane swaps removed by permuting V tr-read addressing
# baseline (speedup 1.0000x reference)
.LBB0_912:
	s_load_dwordx2 s[26:27], s[2:3], 0x78
	s_ashr_i32 s2, s54, 4
	s_mul_hi_i32 s3, s2, 0x2aaaaaab
	s_lshr_b32 s4, s3, 31
	s_add_i32 s3, s3, s4
	s_mul_i32 s3, s3, 6
	s_sub_i32 s2, s2, s3
	s_mul_hi_i32 s3, s54, 0x2aaaaaab
	s_lshr_b32 s4, s3, 31
	s_ashr_i32 s3, s3, 4
	s_add_i32 s28, s3, s4
	s_mul_i32 s3, s2, 0x56
	s_lshr_b32 s4, s3, 8
	s_bfe_u32 s3, s3, 0x1000f
	s_add_i32 s4, s4, s3
	s_ashr_i32 s29, s28, 31
	s_lshl_b32 s3, s54, 8
	s_lshl_b64 s[30:31], s[28:29], 12
	s_and_b32 s3, s3, 0xf00
	s_or_b32 s30, s30, s3
	s_sext_i32_i8 s34, s4
	s_mul_i32 s3, s31, 0x600
	s_mul_hi_u32 s4, s30, 0x600
	s_add_i32 s4, s4, s3
	s_mul_i32 s3, s30, 0x600
	s_add_u32 s5, s24, s3
	s_addc_u32 s4, s25, s4
	s_lshl_b32 s22, s2, 7
	s_ashr_i32 s23, s22, 31
	s_lshl_b64 s[2:3], s[22:23], 1
	s_add_u32 s2, s5, s2
	s_addc_u32 s3, s4, s3
	s_add_u32 s38, s2, 0x48560200
	s_addc_u32 s39, s3, 0
	s_lshl_b64 s[4:5], s[28:29], 21
	s_add_u32 s37, s24, s4
	s_addc_u32 s40, s25, s5
	s_lshl_b32 s2, s34, 7
	s_ashr_i32 s3, s2, 31
	s_lshl_b64 s[34:35], s[2:3], 1
	s_add_u32 s2, s37, s34
	s_addc_u32 s3, s40, s35
	s_add_u32 s2, s2, 0x49d60200
	s_addc_u32 s3, s3, 0
	s_lshl_b64 s[28:29], s[28:29], 25
	s_add_u32 s37, s24, s28
	s_addc_u32 s40, s25, s29
	s_add_u32 s37, s37, s34
	s_waitcnt lgkmcnt(0)
	s_addc_u32 s40, s40, s35
	s_add_u32 s52, s37, 0x40560a00
	v_ashrrev_i32_e32 v54, 4, v0
	v_lshlrev_b32_e32 v1, 3, v0
	v_ashrrev_i32_e32 v55, 31, v54
	s_addc_u32 s53, s40, 0
	v_and_b32_e32 v2, 0x78, v1
	v_lshlrev_b64 v[48:49], 13, v[54:55]
	v_lshlrev_b32_e32 v52, 1, v2
	v_add_u32_e32 v18, 32, v54
	v_lshl_add_u64 v[2:3], s[52:53], 0, v[48:49]
	v_mov_b32_e32 v53, v177
	v_lshl_add_u64 v[2:3], v[2:3], 0, v[52:53]
	v_ashrrev_i32_e32 v19, 31, v18
	global_load_dwordx4 v[2:5], v[2:3], off
	v_lshlrev_b64 v[6:7], 13, v[18:19]
	v_lshlrev_b64 v[50:51], 9, v[54:55]
	v_lshl_add_u64 v[6:7], s[52:53], 0, v[6:7]
	v_lshl_add_u64 v[10:11], s[2:3], 0, v[50:51]
	v_lshl_add_u64 v[6:7], v[6:7], 0, v[52:53]
	v_lshl_add_u64 v[10:11], v[10:11], 0, v[52:53]
	global_load_dwordx4 v[6:9], v[6:7], off
	v_lshlrev_b64 v[14:15], 9, v[18:19]
	global_load_dwordx4 v[10:13], v[10:11], off
	v_lshl_add_u64 v[14:15], s[2:3], 0, v[14:15]
	v_lshl_add_u64 v[14:15], v[14:15], 0, v[52:53]
	v_readfirstlane_b32 s37, v0
	global_load_dwordx4 v[14:17], v[14:15], off
	s_ashr_i32 s40, s37, 1
	v_mov_b32_e32 v19, s40
	v_bfe_u32 v22, v0, 5, 1
	v_bfi_b32 v19, s1, v19, v0
	v_mov_b64_e32 v[20:21], s[38:39]
	v_mad_i64_i32 v[20:21], s[38:39], v19, s0, v[20:21]
	v_lshlrev_b32_e32 v176, 4, v22
	v_lshl_add_u64 v[20:21], v[20:21], 0, v[176:177]
	global_load_dwordx4 v[124:127], v[20:21], off
	global_load_dwordx4 v[120:123], v[20:21], off offset:32
	global_load_dwordx4 v[116:119], v[20:21], off offset:64
	global_load_dwordx4 v[112:115], v[20:21], off offset:96
	global_load_dwordx4 v[108:111], v[20:21], off offset:128
	global_load_dwordx4 v[104:107], v[20:21], off offset:160
	global_load_dwordx4 v[100:103], v[20:21], off offset:192
	global_load_dwordx4 v[96:99], v[20:21], off offset:224
	v_and_b32_e32 v19, 0xfffff0, v54
	v_lshlrev_b32_e32 v20, 1, v54
	v_mov_b32_e32 v216, v22
	v_and_or_b32 v19, v20, 8, v19
	v_and_b32_e32 v22, 0xfffff0, v18
	v_lshlrev_b32_e32 v23, 1, v18
	v_lshrrev_b32_e32 v20, 1, v54
	v_lshrrev_b32_e32 v19, 1, v19
	v_bfe_u32 v1, v1, 5, 2
	v_and_b32_e32 v21, 3, v54
	v_and_or_b32 v22, v23, 8, v22
	v_or_b32_e32 v19, v19, v1
	v_and_or_b32 v20, v20, 4, v21
	v_lshrrev_b32_e32 v22, 1, v22
	v_lshlrev_b32_e32 v19, 9, v19
	v_lshlrev_b32_e32 v20, 6, v20
	v_and_b32_e32 v21, 48, v52
	v_or_b32_e32 v1, v22, v1
	v_or3_b32 v19, v19, v20, v21
	v_lshlrev_b32_e32 v1, 9, v1
	v_or3_b32 v1, v1, v20, v21
	v_add_u32_e32 v193, 0, v19
	s_waitcnt vmcnt(0)
	v_add_u32_e32 v194, 0, v1
	v_lshlrev_b32_e32 v1, 8, v54
	v_and_b32_e32 v178, 31, v0
	v_lshlrev_b32_e32 v78, 4, v0
	v_and_b32_e32 v79, 63, v0
	v_add_u32_e32 v64, 64, v54
	v_add_u32_e32 v66, 0x60, v54
	v_ashrrev_i32_e32 v65, 31, v64
	v_ashrrev_i32_e32 v67, 31, v66
	v_add_u32_e32 v72, 0xa0, v54
	v_ashrrev_i32_e32 v73, 31, v72
	v_add_u32_e32 v54, 0x80, v54
	v_lshlrev_b64 v[74:75], 9, v[72:73]
	v_lshlrev_b64 v[72:73], 13, v[72:73]
	v_lshl_add_u64 v[74:75], s[2:3], 0, v[74:75]
	v_lshl_add_u64 v[72:73], s[52:53], 0, v[72:73]
	v_lshl_add_u64 v[74:75], v[74:75], 0, v[52:53]
	v_lshl_add_u64 v[72:73], v[72:73], 0, v[52:53]
	s_and_b32 s37, s37, 0x3fffffc0
	s_lshl_b32 s37, s37, 2
	s_add_i32 s56, s37, 0
	s_add_i32 s56, s56, 0x10000
	s_and_b32 s55, s40, 0xffffffe0
	s_cmp_lg_u32 0, -1
	s_cselect_b32 s58, 0, 0
	s_mov_b32 s37, s36
	s_mov_b32 s38, s36
	s_mov_b32 s39, s36
	s_mov_b32 s40, s36
	s_mov_b32 s41, s36
	s_mov_b32 s42, s36
	s_mov_b32 s43, s36
	s_waitcnt vmcnt(11)
	ds_write_b128 v193, v[2:5]
	v_and_b32_e32 v2, 0x70, v0
	v_bitop3_b32 v1, v52, v1, v2 bitop3:0xde
	v_add_u32_e32 v195, 0, v1
	v_lshlrev_b32_e32 v1, 8, v18
	v_bitop3_b32 v1, v52, v1, v2 bitop3:0xde
	v_add_u32_e32 v196, 0, v1
	s_waitcnt vmcnt(10)
	ds_write_b128 v194, v[6:9]
	s_mov_b32 s44, s36
	s_waitcnt vmcnt(9)
	ds_write_b128 v195, v[10:13] offset:32768
	v_lshlrev_b32_e32 v10, 8, v178
	v_and_b32_e32 v11, 0x70, v78
	v_bitop3_b32 v1, v176, v10, v11 bitop3:0xde
	v_add_u32_e32 v197, 0, v1
	s_waitcnt vmcnt(8)
	ds_write_b128 v196, v[14:17] offset:32768
	s_waitcnt lgkmcnt(0)
	s_barrier
	ds_read_b128 v[2:5], v197 offset:32768
	ds_read_b128 v[6:9], v197 offset:40960
	s_waitcnt vmcnt(7) lgkmcnt(1)
	v_mfma_f32_32x32x16_bf16 v[32:47], v[2:5], v[124:127], 0
	v_or_b32_e32 v1, 32, v176
	v_bitop3_b32 v1, v1, v10, v11 bitop3:0xde
	v_add_u32_e32 v198, 0, v1
	v_or_b32_e32 v1, 64, v176
	v_bitop3_b32 v1, v1, v10, v11 bitop3:0xde
	v_add_u32_e32 v199, 0, v1
	v_or_b32_e32 v1, 0x60, v176
	s_waitcnt lgkmcnt(0)
	v_mfma_f32_32x32x16_bf16 v[16:31], v[6:9], v[124:127], 0
	ds_read_b128 v[2:5], v198 offset:32768
	ds_read_b128 v[6:9], v198 offset:40960
	v_bitop3_b32 v1, v1, v10, v11 bitop3:0xde
	v_add_u32_e32 v200, 0, v1
	v_or_b32_e32 v1, 0x80, v176
	v_bitop3_b32 v1, v1, v10, v11 bitop3:0xde
	v_add_u32_e32 v201, 0, v1
	v_or_b32_e32 v1, 0xa0, v176
	s_waitcnt vmcnt(6) lgkmcnt(1)
	v_mfma_f32_32x32x16_bf16 v[32:47], v[2:5], v[120:123], v[32:47]
	v_bitop3_b32 v1, v1, v10, v11 bitop3:0xde
	v_add_u32_e32 v202, 0, v1
	v_lshlrev_b32_e32 v12, 3, v79
	v_and_b32_e32 v1, 0xc0, v78
	s_mov_b32 s45, s36
	s_mov_b32 s46, s36
	s_mov_b32 s47, s36
	s_waitcnt lgkmcnt(0)
	v_mfma_f32_32x32x16_bf16 v[16:31], v[6:9], v[120:123], v[16:31]
	ds_read_b128 v[2:5], v199 offset:32768
	ds_read_b128 v[6:9], v199 offset:40960
	s_mov_b32 s48, s36
	s_mov_b32 s49, s36
	s_mov_b32 s50, s36
	s_mov_b32 s51, s36
	s_mov_b32 s57, 1
	v_lshl_add_u32 v179, v178, 2, s56
	s_waitcnt vmcnt(5) lgkmcnt(1)
	v_mfma_f32_32x32x16_bf16 v[32:47], v[2:5], v[116:119], v[32:47]
	v_mov_b32_e32 v190, 0
	s_waitcnt lgkmcnt(0)
	v_mfma_f32_32x32x16_bf16 v[16:31], v[6:9], v[116:119], v[16:31]
	ds_read_b128 v[2:5], v200 offset:32768
	ds_read_b128 v[6:9], v200 offset:40960
	s_waitcnt vmcnt(4) lgkmcnt(1)
	v_mfma_f32_32x32x16_bf16 v[32:47], v[2:5], v[112:115], v[32:47]
	s_waitcnt lgkmcnt(0)
	v_mfma_f32_32x32x16_bf16 v[16:31], v[6:9], v[112:115], v[16:31]
	ds_read_b128 v[2:5], v201 offset:32768
	ds_read_b128 v[6:9], v201 offset:40960
	s_waitcnt vmcnt(3) lgkmcnt(1)
	v_mfma_f32_32x32x16_bf16 v[32:47], v[2:5], v[108:111], v[32:47]
	ds_read_b128 v[2:5], v202 offset:32768
	s_waitcnt lgkmcnt(1)
	v_mfma_f32_32x32x16_bf16 v[16:31], v[6:9], v[108:111], v[16:31]
	ds_read_b128 v[6:9], v202 offset:40960
	s_waitcnt vmcnt(2) lgkmcnt(1)
	v_mfma_f32_32x32x16_bf16 v[32:47], v[2:5], v[104:107], v[32:47]
	v_lshlrev_b32_e32 v5, 1, v0
	v_or_b32_e32 v0, 0xc0, v176
	v_bitop3_b32 v0, v0, v10, v11 bitop3:0xde
	v_add_u32_e32 v203, 0, v0
	v_and_or_b32 v4, v12, 24, v1
	ds_read_b128 v[0:3], v203 offset:32768
	v_and_b32_e32 v5, 32, v5
	s_waitcnt lgkmcnt(1)
	v_mfma_f32_32x32x16_bf16 v[16:31], v[6:9], v[104:107], v[16:31]
	v_lshlrev_b32_e32 v6, 3, v12
	v_and_b32_e32 v6, 0x800, v6
	v_or3_b32 v80, v4, v5, v6
	ds_read_b128 v[4:7], v203 offset:40960
	v_add_u32_e32 v192, s58, v80
	s_waitcnt vmcnt(1) lgkmcnt(1)
	v_mfma_f32_32x32x16_bf16 v[32:47], v[0:3], v[100:103], v[32:47]
	v_or_b32_e32 v0, 0xe0, v176
	v_bitop3_b32 v0, v0, v10, v11 bitop3:0xde
	v_add_u32_e32 v204, 0, v0
	ds_read_b128 v[0:3], v204 offset:32768
	ds_read_b128 v[56:59], v204 offset:40960
	s_waitcnt lgkmcnt(2)
	v_mfma_f32_32x32x16_bf16 v[16:31], v[4:7], v[100:103], v[16:31]
	s_waitcnt vmcnt(0) lgkmcnt(1)
	v_mfma_f32_32x32x16_bf16 v[32:47], v[0:3], v[96:99], v[32:47]
	v_mov_b64_e32 v[0:1], s[36:37]
	v_mov_b64_e32 v[14:15], s[50:51]
	v_mov_b64_e32 v[2:3], s[38:39]
	v_mov_b64_e32 v[4:5], s[40:41]
	v_mov_b64_e32 v[6:7], s[42:43]
	v_mov_b64_e32 v[8:9], s[44:45]
	v_mov_b64_e32 v[10:11], s[46:47]
	s_waitcnt lgkmcnt(0)
	v_mfma_f32_32x32x16_bf16 v[16:31], v[56:59], v[96:99], v[16:31]
	s_nop 2
	v_max_f32_e32 v55, v33, v33
	v_max_f32_e32 v56, v32, v32
	v_max_f32_e32 v55, v56, v55
	v_max3_f32 v55, v55, v34, v35
	v_max3_f32 v55, v55, v36, v37
	v_max3_f32 v55, v55, v38, v39
	v_max3_f32 v55, v55, v40, v41
	v_max3_f32 v55, v55, v42, v43
	v_max3_f32 v55, v55, v44, v45
	v_max3_f32 v55, v55, v46, v47
	v_max3_f32 v55, v55, v16, v17
	v_max3_f32 v55, v55, v18, v19
	v_max3_f32 v55, v55, v20, v21
	v_max3_f32 v55, v55, v22, v23
	v_max3_f32 v55, v55, v24, v25
	v_max3_f32 v55, v55, v26, v27
	v_lshlrev_b64 v[56:57], 13, v[64:65]
	v_lshlrev_b64 v[58:59], 13, v[66:67]
	v_lshlrev_b64 v[64:65], 9, v[64:65]
	v_lshlrev_b64 v[66:67], 9, v[66:67]
	v_max3_f32 v55, v55, v28, v29
	v_lshl_add_u64 v[56:57], s[52:53], 0, v[56:57]
	v_lshl_add_u64 v[58:59], s[52:53], 0, v[58:59]
	v_lshl_add_u64 v[64:65], s[2:3], 0, v[64:65]
	v_lshl_add_u64 v[66:67], s[2:3], 0, v[66:67]
	v_max3_f32 v81, v55, v30, v31
	v_lshl_add_u64 v[56:57], v[56:57], 0, v[52:53]
	v_lshl_add_u64 v[60:61], v[58:59], 0, v[52:53]
	v_lshl_add_u64 v[64:65], v[64:65], 0, v[52:53]
	v_lshl_add_u64 v[68:69], v[66:67], 0, v[52:53]
	v_ashrrev_i32_e32 v55, 31, v54
	global_load_dwordx4 v[56:59], v[56:57], off
	s_nop 0
	global_load_dwordx4 v[60:63], v[60:61], off
	s_nop 0
	global_load_dwordx4 v[64:67], v[64:65], off
	s_nop 0
	global_load_dwordx4 v[68:71], v[68:69], off
	v_lshlrev_b64 v[76:77], 9, v[54:55]
	v_lshlrev_b64 v[54:55], 13, v[54:55]
	v_lshl_add_u64 v[76:77], s[2:3], 0, v[76:77]
	v_lshl_add_u64 v[54:55], s[52:53], 0, v[54:55]
	v_lshl_add_u64 v[76:77], v[76:77], 0, v[52:53]
	global_load_dwordx4 v[140:143], v[74:75], off
	global_load_dwordx4 v[136:139], v[76:77], off
	v_lshl_add_u64 v[52:53], v[54:55], 0, v[52:53]
	global_load_dwordx4 v[132:135], v[72:73], off
	global_load_dwordx4 v[128:131], v[52:53], off
	v_mov_b32_e32 v82, v81
	s_nop 1
	v_permlane32_swap_b32_e32 v81, v82
	v_max_f32_e32 v52, v82, v82
	v_max_f32_e32 v53, v81, v81
	v_max_f32_e32 v52, v53, v52
	v_add_f32_e32 v53, 0x7149f2ca, v52
	v_max_f32_e32 v52, 0xf149f2ca, v52
	v_cmp_ge_f32_e32 vcc, s9, v53
	v_sub_f32_e32 v53, 0xf149f2ca, v52
	v_mul_f32_e32 v53, 0x3e0293ee, v53
	v_exp_f32_e32 v53, v53
	s_cmp_eq_u64 vcc, exec
	s_cselect_b64 vcc, -1, 0
	v_mov_b32_e32 v54, 0xf149f2ca
	v_cndmask_b32_e32 v160, v52, v54, vcc
	v_mul_f32_e32 v52, 0xbe0293ee, v160
	v_cndmask_b32_e64 v205, v53, 1.0, vcc
	v_mov_b32_e32 v53, v52
	v_fmac_f32_e32 v53, 0x3e0293ee, v47
	v_pk_fma_f32 v[150:151], v[18:19], s[8:9], v[52:53] op_sel_hi:[1,0,0]
	v_pk_fma_f32 v[152:153], v[16:17], s[8:9], v[52:53] op_sel_hi:[1,0,0]
	v_lshl_add_u64 v[16:17], s[4:5], 0, v[50:51]
	v_and_b32_e32 v18, 0xf0, v78
	v_fmamk_f32 v32, v32, 0x3e0293ee, v52
	v_fmamk_f32 v33, v33, 0x3e0293ee, v52
	v_fmamk_f32 v34, v34, 0x3e0293ee, v52
	v_fmamk_f32 v35, v35, 0x3e0293ee, v52
	v_fmamk_f32 v36, v36, 0x3e0293ee, v52
	v_fmamk_f32 v37, v37, 0x3e0293ee, v52
	v_fmamk_f32 v38, v38, 0x3e0293ee, v52
	v_fmamk_f32 v39, v39, 0x3e0293ee, v52
	v_fmamk_f32 v40, v40, 0x3e0293ee, v52
	v_fmamk_f32 v41, v41, 0x3e0293ee, v52
	v_fmamk_f32 v42, v42, 0x3e0293ee, v52
	v_fmamk_f32 v43, v43, 0x3e0293ee, v52
	v_fmamk_f32 v44, v44, 0x3e0293ee, v52
	v_fmamk_f32 v45, v45, 0x3e0293ee, v52
	v_fmamk_f32 v46, v46, 0x3e0293ee, v52
	v_or_b32_e32 v16, v16, v18
	v_exp_f32_e32 v170, v32
	v_exp_f32_e32 v171, v33
	v_exp_f32_e32 v172, v34
	v_exp_f32_e32 v173, v35
	v_exp_f32_e32 v174, v36
	v_exp_f32_e32 v184, v37
	v_exp_f32_e32 v175, v38
	v_exp_f32_e32 v185, v39
	v_exp_f32_e32 v162, v40
	v_exp_f32_e32 v163, v41
	v_exp_f32_e32 v164, v42
	v_exp_f32_e32 v166, v43
	v_exp_f32_e32 v165, v44
	v_exp_f32_e32 v167, v45
	v_exp_f32_e32 v168, v46
	v_exp_f32_e32 v169, v53
	v_lshl_add_u64 v[180:181], s[24:25], 0, v[16:17]
	v_lshl_add_u64 v[16:17], s[28:29], 0, v[48:49]
	s_waitcnt vmcnt(4)
	v_or_b32_e32 v16, v16, v18
	v_mov_b64_e32 v[12:13], s[48:49]
	v_pk_fma_f32 v[154:155], v[30:31], s[8:9], v[52:53] op_sel_hi:[1,0,0]
	v_pk_fma_f32 v[156:157], v[28:29], s[8:9], v[52:53] op_sel_hi:[1,0,0]
	v_pk_fma_f32 v[158:159], v[26:27], s[8:9], v[52:53] op_sel_hi:[1,0,0]
	v_pk_fma_f32 v[144:145], v[24:25], s[8:9], v[52:53] op_sel_hi:[1,0,0]
	v_pk_fma_f32 v[146:147], v[22:23], s[8:9], v[52:53] op_sel_hi:[1,0,0]
	v_pk_fma_f32 v[148:149], v[20:21], s[8:9], v[52:53] op_sel_hi:[1,0,0]
	s_waitcnt vmcnt(7)
	ds_write_b128 v193, v[56:59] offset:16384
	s_waitcnt vmcnt(6)
	ds_write_b128 v194, v[60:63] offset:16384
	s_waitcnt vmcnt(5)
	ds_write_b128 v195, v[64:67] offset:49152
	s_waitcnt vmcnt(4)
	ds_write_b128 v196, v[68:71] offset:49152
	s_addk_i32 s58, 0x4000
	v_lshl_add_u64 v[182:183], s[24:25], 0, v[16:17]
	v_mov_b64_e32 v[62:63], v[14:15]
	v_mov_b64_e32 v[30:31], v[14:15]
	v_mov_b64_e32 v[46:47], v[14:15]
	v_cmp_gt_u32_e64 s[2:3], 32, v79
	v_add_u32_e32 v191, s58, v80
	v_mov_b64_e32 v[60:61], v[12:13]
	v_mov_b64_e32 v[58:59], v[10:11]
	v_mov_b64_e32 v[56:57], v[8:9]
	v_mov_b64_e32 v[54:55], v[6:7]
	v_mov_b64_e32 v[52:53], v[4:5]
	v_mov_b64_e32 v[50:51], v[2:3]
	v_mov_b64_e32 v[48:49], v[0:1]
	v_mov_b64_e32 v[28:29], v[12:13]
	v_mov_b64_e32 v[26:27], v[10:11]
	v_mov_b64_e32 v[24:25], v[8:9]
	v_mov_b64_e32 v[22:23], v[6:7]
	v_mov_b64_e32 v[20:21], v[4:5]
	v_mov_b64_e32 v[18:19], v[2:3]
	v_mov_b64_e32 v[16:17], v[0:1]
	v_mov_b64_e32 v[44:45], v[12:13]
	v_mov_b64_e32 v[42:43], v[10:11]
	v_mov_b64_e32 v[40:41], v[8:9]
	v_mov_b64_e32 v[38:39], v[6:7]
	v_mov_b64_e32 v[36:37], v[4:5]
	v_mov_b64_e32 v[34:35], v[2:3]
	v_mov_b64_e32 v[32:33], v[0:1]
	s_waitcnt lgkmcnt(0)
	s_barrier
.LBB0_913:
	ds_read_b128 v[64:67], v197 offset:49152
	ds_read_b128 v[68:71], v197 offset:57344
	ds_read_b128 v[206:209], v198 offset:49152
	ds_read_b128 v[210:213], v198 offset:57344
	ds_read_b128 v[218:221], v199 offset:49152
	ds_read_b128 v[222:225], v199 offset:57344
	v_add_f32_e32 v161, 0, v170
	v_add_f32_e32 v161, v171, v161
	s_waitcnt lgkmcnt(5)
	v_mfma_f32_32x32x16_bf16 v[80:95], v[64:67], v[124:127], 0
	v_add_f32_e32 v161, v172, v161
	v_add_f32_e32 v161, v173, v161
	v_add_f32_e32 v161, v174, v161
	v_add_f32_e32 v161, v184, v161
	v_add_f32_e32 v161, v175, v161
	v_add_f32_e32 v161, v185, v161
	v_add_f32_e32 v161, v162, v161
	s_waitcnt lgkmcnt(4)
	v_mfma_f32_32x32x16_bf16 v[64:79], v[68:71], v[124:127], 0
	v_add_f32_e32 v161, v163, v161
	v_add_f32_e32 v161, v164, v161
	v_add_f32_e32 v161, v166, v161
	v_exp_f32_e32 v152, v152
	v_add_f32_e32 v161, v165, v161
	v_exp_f32_e32 v153, v153
	v_add_f32_e32 v161, v167, v161
	s_waitcnt lgkmcnt(3)
	v_mfma_f32_32x32x16_bf16 v[80:95], v[206:209], v[120:123], v[80:95]
	ds_read_b128 v[206:209], v200 offset:49152
	ds_read_b128 v[226:229], v200 offset:57344
	ds_read_b128 v[230:233], v201 offset:49152
	ds_read_b128 v[234:237], v201 offset:57344
	ds_read_b128 v[238:241], v202 offset:49152
	ds_read_b128 v[242:245], v202 offset:57344
	ds_read_b128 v[246:249], v203 offset:49152
	ds_read_b128 v[250:253], v203 offset:57344
	v_exp_f32_e32 v150, v150
	v_add_f32_e32 v161, v168, v161
	v_exp_f32_e32 v151, v151
	v_add_f32_e32 v161, v169, v161
	v_exp_f32_e32 v148, v148
	v_add_f32_e32 v161, v152, v161
	s_waitcnt lgkmcnt(10)
	v_mfma_f32_32x32x16_bf16 v[64:79], v[210:213], v[120:123], v[64:79]
	v_exp_f32_e32 v149, v149
	v_add_f32_e32 v161, v153, v161
	v_exp_f32_e32 v146, v146
	v_add_f32_e32 v161, v150, v161
	v_exp_f32_e32 v147, v147
	v_add_f32_e32 v161, v151, v161
	v_exp_f32_e32 v144, v144
	s_waitcnt lgkmcnt(9)
	v_mfma_f32_32x32x16_bf16 v[80:95], v[218:221], v[116:119], v[80:95]
	v_add_f32_e32 v161, v148, v161
	ds_read_b128 v[210:213], v204 offset:49152
	ds_read_b128 v[186:189], v204 offset:57344
	v_exp_f32_e32 v145, v145
	v_add_f32_e32 v161, v149, v161
	v_exp_f32_e32 v158, v158
	v_add_f32_e32 v161, v146, v161
	v_exp_f32_e32 v159, v159
	s_waitcnt lgkmcnt(10)
	v_mfma_f32_32x32x16_bf16 v[64:79], v[222:225], v[116:119], v[64:79]
	v_add_f32_e32 v161, v147, v161
	v_exp_f32_e32 v156, v156
	v_add_f32_e32 v161, v144, v161
	v_exp_f32_e32 v157, v157
	v_add_f32_e32 v161, v145, v161
	v_exp_f32_e32 v154, v154
	v_add_f32_e32 v161, v158, v161
	s_waitcnt lgkmcnt(9)
	v_mfma_f32_32x32x16_bf16 v[80:95], v[206:209], v[112:115], v[80:95]
	v_exp_f32_e32 v155, v155
	v_add_f32_e32 v161, v159, v161
	v_add_f32_e32 v161, v156, v161
	v_add_f32_e32 v161, v157, v161
	v_add_f32_e32 v161, v154, v161
	v_add_f32_e32 v206, v155, v161
	v_mov_b32_e32 v207, v206
	s_waitcnt lgkmcnt(8)
	v_mfma_f32_32x32x16_bf16 v[64:79], v[226:229], v[112:115], v[64:79]
	v_cvt_pk_bf16_f32 v208, v144, v145
	v_permlane32_swap_b32_e32 v206, v207
	v_cvt_pk_bf16_f32 v170, v170, v171
	v_cvt_pk_bf16_f32 v171, v172, v173
	v_cvt_pk_bf16_f32 v172, v174, v184
	v_cvt_pk_bf16_f32 v173, v175, v185
	s_waitcnt lgkmcnt(7)
	v_mfma_f32_32x32x16_bf16 v[80:95], v[230:233], v[108:111], v[80:95]
	v_cvt_pk_bf16_f32 v162, v162, v163
	v_cvt_pk_bf16_f32 v163, v164, v166
	v_cvt_pk_bf16_f32 v164, v165, v167
	v_cvt_pk_bf16_f32 v165, v168, v169
	v_cvt_pk_bf16_f32 v166, v152, v153
	v_cvt_pk_bf16_f32 v167, v150, v151
	v_cvt_pk_bf16_f32 v168, v148, v149
	s_waitcnt lgkmcnt(6)
	v_mfma_f32_32x32x16_bf16 v[64:79], v[234:237], v[108:111], v[64:79]
	v_cvt_pk_bf16_f32 v169, v146, v147
	v_cvt_pk_bf16_f32 v209, v158, v159
	s_waitcnt lgkmcnt(5)
	v_mfma_f32_32x32x16_bf16 v[80:95], v[238:241], v[104:107], v[80:95]
	s_waitcnt lgkmcnt(4)
	v_mfma_f32_32x32x16_bf16 v[64:79], v[242:245], v[104:107], v[64:79]
	s_waitcnt lgkmcnt(3)
	v_mfma_f32_32x32x16_bf16 v[80:95], v[246:249], v[100:103], v[80:95]
	s_waitcnt lgkmcnt(2)
	v_mfma_f32_32x32x16_bf16 v[64:79], v[250:253], v[100:103], v[64:79]
	s_waitcnt lgkmcnt(1)
	v_mfma_f32_32x32x16_bf16 v[80:95], v[210:213], v[96:99], v[80:95]
	v_cvt_pk_bf16_f32 v210, v156, v157
	v_cvt_pk_bf16_f32 v211, v154, v155
	s_waitcnt lgkmcnt(0)
	v_mfma_f32_32x32x16_bf16 v[64:79], v[186:189], v[96:99], v[64:79]
	v_lshl_add_u64 v[186:187], v[182:183], 0, s[34:35]
	v_add_co_u32_e32 v144, vcc, s16, v186
	v_lshl_add_u64 v[184:185], v[180:181], 0, s[34:35]
	s_nop 0
	v_addc_co_u32_e32 v145, vcc, 0, v187, vcc
	v_add_co_u32_e32 v148, vcc, s17, v186
	s_nop 1
	v_addc_co_u32_e32 v149, vcc, 0, v187, vcc
	v_add_co_u32_e32 v152, vcc, s19, v184
	global_load_dwordx4 v[144:147], v[144:145], off offset:2560
	s_nop 0
	global_load_dwordx4 v[148:151], v[148:149], off offset:2560
	v_addc_co_u32_e32 v153, vcc, 0, v185, vcc
	v_add_co_u32_e32 v156, vcc, s21, v184
	s_nop 1
	v_addc_co_u32_e32 v157, vcc, 0, v185, vcc
	global_load_dwordx4 v[152:155], v[152:153], off offset:512
	s_nop 0
	global_load_dwordx4 v[156:159], v[156:157], off offset:512
	ds_read_b64_tr_b16 v[212:213], v192 offset:0x0
	ds_read_b64_tr_b16 v[214:215], v192 offset:0x100
	ds_read_b64_tr_b16 v[218:219], v192 offset:0x1000
	ds_read_b64_tr_b16 v[220:221], v192 offset:0x1100
	ds_read_b64_tr_b16 v[222:223], v192 offset:0x2000
	ds_read_b64_tr_b16 v[224:225], v192 offset:0x2100
	ds_read_b64_tr_b16 v[226:227], v192 offset:0x3000
	ds_read_b64_tr_b16 v[228:229], v192 offset:0x3100
	s_waitcnt lgkmcnt(0)
	s_nop 0
	v_mfma_f32_32x32x16_bf16 v[0:15], v[170:173], v[212:215], v[0:15]
	ds_read_b64_tr_b16 v[212:213], v192 offset:0x200
	ds_read_b64_tr_b16 v[214:215], v192 offset:0x300
	v_mfma_f32_32x32x16_bf16 v[0:15], v[162:165], v[218:221], v[0:15]
	ds_read_b64_tr_b16 v[218:219], v192 offset:0x1200
	ds_read_b64_tr_b16 v[220:221], v192 offset:0x1300
	v_mfma_f32_32x32x16_bf16 v[0:15], v[166:169], v[222:225], v[0:15]
	ds_read_b64_tr_b16 v[222:223], v192 offset:0x2200
	ds_read_b64_tr_b16 v[224:225], v192 offset:0x2300
	ds_read_b64_tr_b16 v[230:231], v192 offset:0x3200
	ds_read_b64_tr_b16 v[232:233], v192 offset:0x3300
	s_waitcnt lgkmcnt(0)
	v_mfma_f32_32x32x16_bf16 v[0:15], v[208:211], v[226:229], v[0:15]
	v_mfma_f32_32x32x16_bf16 v[48:63], v[170:173], v[212:215], v[48:63]
	ds_read_b64_tr_b16 v[212:213], v192 offset:0x400
	ds_read_b64_tr_b16 v[214:215], v192 offset:0x500
	v_mfma_f32_32x32x16_bf16 v[48:63], v[162:165], v[218:221], v[48:63]
	ds_read_b64_tr_b16 v[218:219], v192 offset:0x1400
	ds_read_b64_tr_b16 v[220:221], v192 offset:0x1500
	v_mfma_f32_32x32x16_bf16 v[48:63], v[166:169], v[222:225], v[48:63]
	ds_read_b64_tr_b16 v[222:223], v192 offset:0x2400
	ds_read_b64_tr_b16 v[224:225], v192 offset:0x2500
	ds_read_b64_tr_b16 v[226:227], v192 offset:0x3400
	ds_read_b64_tr_b16 v[228:229], v192 offset:0x3500
	s_waitcnt lgkmcnt(0)
	v_mfma_f32_32x32x16_bf16 v[48:63], v[208:211], v[230:233], v[48:63]
	v_mfma_f32_32x32x16_bf16 v[16:31], v[170:173], v[212:215], v[16:31]
	ds_read_b64_tr_b16 v[212:213], v192 offset:0x600
	ds_read_b64_tr_b16 v[214:215], v192 offset:0x700
	v_mfma_f32_32x32x16_bf16 v[16:31], v[162:165], v[218:221], v[16:31]
	ds_read_b64_tr_b16 v[218:219], v192 offset:0x1600
	ds_read_b64_tr_b16 v[220:221], v192 offset:0x1700
	v_mfma_f32_32x32x16_bf16 v[16:31], v[166:169], v[222:225], v[16:31]
	ds_read_b64_tr_b16 v[222:223], v192 offset:0x2600
	ds_read_b64_tr_b16 v[224:225], v192 offset:0x2700
	ds_read_b64_tr_b16 v[230:231], v192 offset:0x3600
	ds_read_b64_tr_b16 v[232:233], v192 offset:0x3700
	s_waitcnt lgkmcnt(0)
	v_mfma_f32_32x32x16_bf16 v[16:31], v[208:211], v[226:229], v[16:31]
	v_mfma_f32_32x32x16_bf16 v[32:47], v[170:173], v[212:215], v[32:47]
	v_max_f32_e32 v161, v81, v81
	v_max_f32_e32 v174, v80, v80
	v_max_f32_e32 v161, v174, v161
	v_max3_f32 v161, v161, v82, v83
	v_max3_f32 v161, v161, v84, v85
	v_max3_f32 v161, v161, v86, v87
	v_max3_f32 v161, v161, v88, v89
	v_max3_f32 v161, v161, v90, v91
	v_mfma_f32_32x32x16_bf16 v[32:47], v[162:165], v[218:221], v[32:47]
	v_max3_f32 v161, v161, v92, v93
	v_max3_f32 v161, v161, v94, v95
	v_max3_f32 v161, v161, v64, v65
	v_max3_f32 v161, v161, v66, v67
	v_max3_f32 v161, v161, v68, v69
	v_max3_f32 v161, v161, v70, v71
	v_max3_f32 v161, v161, v72, v73
	v_max3_f32 v161, v161, v74, v75
	v_mfma_f32_32x32x16_bf16 v[32:47], v[166:169], v[222:225], v[32:47]
	v_max3_f32 v161, v161, v76, v77
	v_max3_f32 v161, v161, v78, v79
	v_mov_b32_e32 v162, v161
	s_nop 1
	v_permlane32_swap_b32_e32 v161, v162
	v_max_f32_e32 v162, v162, v162
	v_max_f32_e32 v161, v161, v161
	v_max_f32_e32 v161, v161, v162
	v_max_f32_e32 v163, v160, v160
	v_sub_f32_e32 v162, v161, v160
	v_max_f32_e32 v161, v163, v161
	v_mfma_f32_32x32x16_bf16 v[32:47], v[208:211], v[230:233], v[32:47]
	v_sub_f32_e32 v163, v160, v161
	v_mul_f32_e32 v163, 0x3e0293ee, v163
	v_exp_f32_e32 v163, v163
	v_cmp_ge_f32_e32 vcc, s9, v162
	s_cmp_eq_u64 vcc, exec
	s_cselect_b64 s[4:5], -1, 0
	s_barrier
	s_waitcnt vmcnt(4)
	v_cndmask_b32_e64 v208, v163, 1.0, s[4:5]
	v_cmp_gt_f32_e32 vcc, 1.0, v208
	s_waitcnt vmcnt(4)
	ds_write_b128 v193, v[128:131]
	ds_write_b128 v194, v[132:135]
	ds_write_b128 v195, v[136:139] offset:32768
	ds_write_b128 v196, v[140:143] offset:32768
	s_cbranch_vccz .LBB0_917
	s_and_saveexec_b64 s[28:29], s[2:3]
	ds_write_b32 v179, v208 offset:128
	s_or_b64 exec, exec, s[28:29]
	s_waitcnt lgkmcnt(0)
	v_add_u32_e32 v174, s56, v176
	ds_read_b128 v[162:165], v174 offset:224
	ds_read_b128 v[166:169], v174 offset:192
	ds_read_b128 v[170:173], v174 offset:160
	ds_read_b128 v[210:213], v174 offset:128
	s_waitcnt lgkmcnt(3)
	v_pk_mul_f32 v[12:13], v[12:13], v[162:163]
	s_waitcnt lgkmcnt(2)
	v_pk_mul_f32 v[8:9], v[8:9], v[166:167]
	s_waitcnt lgkmcnt(1)
	v_pk_mul_f32 v[4:5], v[4:5], v[170:171]
	v_pk_mul_f32 v[14:15], v[14:15], v[164:165]
	v_pk_mul_f32 v[10:11], v[10:11], v[168:169]
	v_pk_mul_f32 v[6:7], v[6:7], v[172:173]
	s_waitcnt lgkmcnt(0)
	v_pk_mul_f32 v[2:3], v[2:3], v[212:213]
	v_pk_mul_f32 v[0:1], v[0:1], v[210:211]
	v_pk_mul_f32 v[60:61], v[60:61], v[162:163]
	v_pk_mul_f32 v[56:57], v[56:57], v[166:167]
	v_pk_mul_f32 v[52:53], v[52:53], v[170:171]
	v_pk_mul_f32 v[62:63], v[62:63], v[164:165]
	v_pk_mul_f32 v[58:59], v[58:59], v[168:169]
	v_pk_mul_f32 v[54:55], v[54:55], v[172:173]
	v_pk_mul_f32 v[50:51], v[50:51], v[212:213]
	v_pk_mul_f32 v[48:49], v[48:49], v[210:211]
	v_pk_mul_f32 v[28:29], v[28:29], v[162:163]
	v_pk_mul_f32 v[24:25], v[24:25], v[166:167]
	v_pk_mul_f32 v[20:21], v[20:21], v[170:171]
	v_pk_mul_f32 v[30:31], v[30:31], v[164:165]
	v_pk_mul_f32 v[26:27], v[26:27], v[168:169]
	v_pk_mul_f32 v[22:23], v[22:23], v[172:173]
	v_pk_mul_f32 v[18:19], v[18:19], v[212:213]
	v_pk_mul_f32 v[16:17], v[16:17], v[210:211]
	v_pk_mul_f32 v[44:45], v[44:45], v[162:163]
	v_pk_mul_f32 v[40:41], v[40:41], v[166:167]
	v_pk_mul_f32 v[36:37], v[36:37], v[170:171]
	v_pk_mul_f32 v[46:47], v[46:47], v[164:165]
	v_pk_mul_f32 v[42:43], v[42:43], v[168:169]
	v_pk_mul_f32 v[38:39], v[38:39], v[172:173]
	v_pk_mul_f32 v[34:35], v[34:35], v[212:213]
	v_pk_mul_f32 v[32:33], v[32:33], v[210:211]
.LBB0_917:
	v_cndmask_b32_e64 v209, v161, v160, s[4:5]
	v_mul_f32_e32 v210, 0xbe0293ee, v209
	v_fmamk_f32 v80, v80, 0x3e0293ee, v210
	v_fmamk_f32 v81, v81, 0x3e0293ee, v210
	v_fmamk_f32 v82, v82, 0x3e0293ee, v210
	v_fmamk_f32 v83, v83, 0x3e0293ee, v210
	v_fmamk_f32 v84, v84, 0x3e0293ee, v210
	v_fmamk_f32 v85, v85, 0x3e0293ee, v210
	v_fmamk_f32 v86, v86, 0x3e0293ee, v210
	v_fmamk_f32 v87, v87, 0x3e0293ee, v210
	v_fmamk_f32 v88, v88, 0x3e0293ee, v210
	v_fmamk_f32 v89, v89, 0x3e0293ee, v210
	v_fmamk_f32 v90, v90, 0x3e0293ee, v210
	v_fmamk_f32 v91, v91, 0x3e0293ee, v210
	v_fmamk_f32 v92, v92, 0x3e0293ee, v210
	v_fmamk_f32 v93, v93, 0x3e0293ee, v210
	v_fmamk_f32 v94, v94, 0x3e0293ee, v210
	v_fmamk_f32 v95, v95, 0x3e0293ee, v210
	v_exp_f32_e32 v160, v80
	v_exp_f32_e32 v161, v81
	v_exp_f32_e32 v162, v82
	v_exp_f32_e32 v173, v83
	v_exp_f32_e32 v174, v84
	v_exp_f32_e32 v175, v85
	v_exp_f32_e32 v163, v86
	v_exp_f32_e32 v172, v87
	v_exp_f32_e32 v164, v88
	v_exp_f32_e32 v165, v89
	v_exp_f32_e32 v169, v90
	v_exp_f32_e32 v171, v91
	v_exp_f32_e32 v166, v92
	v_exp_f32_e32 v167, v93
	v_exp_f32_e32 v168, v94
	v_exp_f32_e32 v170, v95
	v_fmamk_f32 v220, v64, 0x3e0293ee, v210
	v_fmamk_f32 v221, v65, 0x3e0293ee, v210
	v_fmamk_f32 v222, v66, 0x3e0293ee, v210
	v_fmamk_f32 v223, v67, 0x3e0293ee, v210
	v_fmamk_f32 v224, v68, 0x3e0293ee, v210
	v_fmamk_f32 v212, v69, 0x3e0293ee, v210
	v_fmamk_f32 v213, v70, 0x3e0293ee, v210
	v_fmamk_f32 v214, v71, 0x3e0293ee, v210
	v_fmamk_f32 v215, v72, 0x3e0293ee, v210
	v_fmamk_f32 v217, v73, 0x3e0293ee, v210
	v_fmamk_f32 v218, v74, 0x3e0293ee, v210
	v_fmamk_f32 v219, v75, 0x3e0293ee, v210
	v_fmamk_f32 v211, v76, 0x3e0293ee, v210
	v_fmamk_f32 v225, v77, 0x3e0293ee, v210
	v_fmamk_f32 v226, v78, 0x3e0293ee, v210
	v_fmac_f32_e32 v210, 0x3e0293ee, v79
	s_waitcnt lgkmcnt(0)
	s_barrier
	ds_read_b128 v[64:67], v197 offset:32768
	ds_read_b128 v[68:71], v197 offset:40960
	ds_read_b128 v[228:231], v198 offset:32768
	ds_read_b128 v[232:235], v198 offset:40960
	v_exp_f32_e32 v188, v220
	v_exp_f32_e32 v220, v222
	s_waitcnt lgkmcnt(3)
	v_mfma_f32_32x32x16_bf16 v[80:95], v[64:67], v[124:127], 0
	v_exp_f32_e32 v222, v224
	v_exp_f32_e32 v224, v225
	v_exp_f32_e32 v225, v226
	v_exp_f32_e32 v226, v210
	v_add_f32_e32 v210, 0, v160
	v_add_f32_e32 v210, v161, v210
	v_add_f32_e32 v210, v162, v210
	s_waitcnt lgkmcnt(2)
	v_mfma_f32_32x32x16_bf16 v[64:79], v[68:71], v[124:127], 0
	v_add_f32_e32 v210, v173, v210
	v_add_f32_e32 v210, v174, v210
	v_add_f32_e32 v210, v175, v210
	v_add_f32_e32 v210, v163, v210
	v_add_f32_e32 v210, v172, v210
	v_add_f32_e32 v210, v164, v210
	v_add_f32_e32 v210, v165, v210
	s_waitcnt lgkmcnt(1)
	v_mfma_f32_32x32x16_bf16 v[80:95], v[228:231], v[120:123], v[80:95]
	v_add_f32_e32 v210, v169, v210
	v_add_f32_e32 v210, v171, v210
	v_add_f32_e32 v210, v166, v210
	v_exp_f32_e32 v189, v221
	v_add_f32_e32 v210, v167, v210
	v_add_f32_e32 v210, v168, v210
	v_exp_f32_e32 v221, v223
	s_waitcnt lgkmcnt(0)
	v_mfma_f32_32x32x16_bf16 v[64:79], v[232:235], v[120:123], v[64:79]
	ds_read_b128 v[228:231], v199 offset:32768
	ds_read_b128 v[232:235], v199 offset:40960
	v_add_f32_e32 v210, v170, v210
	v_add_f32_e32 v210, v188, v210
	v_exp_f32_e32 v212, v212
	v_add_f32_e32 v210, v189, v210
	v_exp_f32_e32 v213, v213
	v_add_f32_e32 v210, v220, v210
	s_waitcnt lgkmcnt(1)
	v_mfma_f32_32x32x16_bf16 v[80:95], v[228:231], v[116:119], v[80:95]
	v_exp_f32_e32 v214, v214
	v_add_f32_e32 v210, v221, v210
	v_exp_f32_e32 v215, v215
	v_add_f32_e32 v210, v222, v210
	v_exp_f32_e32 v217, v217
	v_add_f32_e32 v210, v212, v210
	v_exp_f32_e32 v218, v218
	s_waitcnt lgkmcnt(0)
	v_mfma_f32_32x32x16_bf16 v[64:79], v[232:235], v[116:119], v[64:79]
	ds_read_b128 v[228:231], v200 offset:32768
	ds_read_b128 v[232:235], v200 offset:40960
	v_add_f32_e32 v210, v213, v210
	v_exp_f32_e32 v219, v219
	v_add_f32_e32 v210, v214, v210
	v_exp_f32_e32 v223, v211
	v_add_f32_e32 v210, v215, v210
	v_add_f32_e32 v210, v217, v210
	s_waitcnt lgkmcnt(1)
	v_mfma_f32_32x32x16_bf16 v[80:95], v[228:231], v[112:115], v[80:95]
	v_add_f32_e32 v210, v218, v210
	v_add_f32_e32 v210, v219, v210
	v_add_f32_e32 v210, v223, v210
	v_add_f32_e32 v210, v224, v210
	v_add_f32_e32 v210, v225, v210
	v_add_f32_e32 v210, v226, v210
	v_mov_b32_e32 v211, v210
	s_waitcnt lgkmcnt(0)
	v_mfma_f32_32x32x16_bf16 v[64:79], v[232:235], v[112:115], v[64:79]
	ds_read_b128 v[228:231], v201 offset:32768
	ds_read_b128 v[232:235], v201 offset:40960
	v_cvt_pk_bf16_f32 v160, v160, v161
	v_cvt_pk_bf16_f32 v161, v162, v173
	v_cvt_pk_bf16_f32 v162, v174, v175
	v_cvt_pk_bf16_f32 v163, v163, v172
	v_cvt_pk_bf16_f32 v164, v164, v165
	v_cvt_pk_bf16_f32 v165, v169, v171
	s_waitcnt lgkmcnt(1)
	v_mfma_f32_32x32x16_bf16 v[80:95], v[228:231], v[108:111], v[80:95]
	v_cvt_pk_bf16_f32 v166, v166, v167
	v_cvt_pk_bf16_f32 v167, v168, v170
	v_cvt_pk_bf16_f32 v168, v188, v189
	v_cvt_pk_bf16_f32 v169, v220, v221
	v_cvt_pk_bf16_f32 v170, v222, v212
	v_cvt_pk_bf16_f32 v171, v213, v214
	v_cvt_pk_bf16_f32 v172, v215, v217
	s_waitcnt lgkmcnt(0)
	v_mfma_f32_32x32x16_bf16 v[64:79], v[232:235], v[108:111], v[64:79]
	ds_read_b128 v[228:231], v202 offset:32768
	ds_read_b128 v[232:235], v202 offset:40960
	v_cvt_pk_bf16_f32 v173, v218, v219
	v_cvt_pk_bf16_f32 v174, v223, v224
	v_cvt_pk_bf16_f32 v175, v225, v226
	v_permlane32_swap_b32_e32 v210, v211
	s_waitcnt lgkmcnt(1)
	v_mfma_f32_32x32x16_bf16 v[80:95], v[228:231], v[104:107], v[80:95]
	s_waitcnt lgkmcnt(0)
	v_mfma_f32_32x32x16_bf16 v[64:79], v[232:235], v[104:107], v[64:79]
	ds_read_b128 v[228:231], v203 offset:32768
	ds_read_b128 v[232:235], v203 offset:40960
	s_waitcnt lgkmcnt(1)
	v_mfma_f32_32x32x16_bf16 v[80:95], v[228:231], v[100:103], v[80:95]
	s_waitcnt lgkmcnt(0)
	v_mfma_f32_32x32x16_bf16 v[64:79], v[232:235], v[100:103], v[64:79]
	ds_read_b128 v[228:231], v204 offset:32768
	ds_read_b128 v[232:235], v204 offset:40960
	s_waitcnt lgkmcnt(1)
	v_mfma_f32_32x32x16_bf16 v[80:95], v[228:231], v[96:99], v[80:95]
	s_waitcnt lgkmcnt(0)
	v_mfma_f32_32x32x16_bf16 v[64:79], v[232:235], v[96:99], v[64:79]
	s_cmp_gt_u32 s57, 60
	s_cselect_b64 s[28:29], -1, 0
	s_and_b64 vcc, exec, s[28:29]
	s_cbranch_vccnz .LBB0_919
	v_add_co_u32_e32 v128, vcc, 0x40760000, v186
	s_nop 1
	v_addc_co_u32_e32 v129, vcc, 0, v187, vcc
	v_add_co_u32_e32 v132, vcc, 0x407a0000, v186
	s_nop 1
	v_addc_co_u32_e32 v133, vcc, 0, v187, vcc
	v_add_co_u32_e32 v136, vcc, 0x49d80000, v184
	global_load_dwordx4 v[128:131], v[128:129], off offset:2560
	s_nop 0
	global_load_dwordx4 v[132:135], v[132:133], off offset:2560
	v_addc_co_u32_e32 v137, vcc, 0, v185, vcc
	v_add_co_u32_e32 v140, vcc, 0x49d84000, v184
	s_nop 1
	v_addc_co_u32_e32 v141, vcc, 0, v185, vcc
	global_load_dwordx4 v[136:139], v[136:137], off offset:512
	s_nop 0
	global_load_dwordx4 v[140:143], v[140:141], off offset:512
.LBB0_919:
	ds_read_b64_tr_b16 v[184:185], v191 offset:0x0
	ds_read_b64_tr_b16 v[186:187], v191 offset:0x100
	ds_read_b64_tr_b16 v[212:213], v191 offset:0x1000
	ds_read_b64_tr_b16 v[214:215], v191 offset:0x1100
	ds_read_b64_tr_b16 v[218:219], v191 offset:0x2000
	ds_read_b64_tr_b16 v[220:221], v191 offset:0x2100
	ds_read_b64_tr_b16 v[222:223], v191 offset:0x3000
	ds_read_b64_tr_b16 v[224:225], v191 offset:0x3100
	s_waitcnt lgkmcnt(0)
	s_nop 0
	v_mfma_f32_32x32x16_bf16 v[0:15], v[160:163], v[184:187], v[0:15]
	ds_read_b64_tr_b16 v[184:185], v191 offset:0x200
	ds_read_b64_tr_b16 v[186:187], v191 offset:0x300
	v_mfma_f32_32x32x16_bf16 v[0:15], v[164:167], v[212:215], v[0:15]
	ds_read_b64_tr_b16 v[212:213], v191 offset:0x1200
	ds_read_b64_tr_b16 v[214:215], v191 offset:0x1300
	v_mfma_f32_32x32x16_bf16 v[0:15], v[168:171], v[218:221], v[0:15]
	ds_read_b64_tr_b16 v[218:219], v191 offset:0x2200
	ds_read_b64_tr_b16 v[220:221], v191 offset:0x2300
	ds_read_b64_tr_b16 v[226:227], v191 offset:0x3200
	ds_read_b64_tr_b16 v[228:229], v191 offset:0x3300
	s_waitcnt lgkmcnt(0)
	v_mfma_f32_32x32x16_bf16 v[0:15], v[172:175], v[222:225], v[0:15]
	v_mfma_f32_32x32x16_bf16 v[48:63], v[160:163], v[184:187], v[48:63]
	ds_read_b64_tr_b16 v[184:185], v191 offset:0x400
	ds_read_b64_tr_b16 v[186:187], v191 offset:0x500
	v_mfma_f32_32x32x16_bf16 v[48:63], v[164:167], v[212:215], v[48:63]
	ds_read_b64_tr_b16 v[212:213], v191 offset:0x1400
	ds_read_b64_tr_b16 v[214:215], v191 offset:0x1500
	v_mfma_f32_32x32x16_bf16 v[48:63], v[168:171], v[218:221], v[48:63]
	ds_read_b64_tr_b16 v[218:219], v191 offset:0x2400
	ds_read_b64_tr_b16 v[220:221], v191 offset:0x2500
	ds_read_b64_tr_b16 v[222:223], v191 offset:0x3400
	ds_read_b64_tr_b16 v[224:225], v191 offset:0x3500
	s_waitcnt lgkmcnt(0)
	v_mfma_f32_32x32x16_bf16 v[48:63], v[172:175], v[226:229], v[48:63]
	v_mfma_f32_32x32x16_bf16 v[16:31], v[160:163], v[184:187], v[16:31]
	ds_read_b64_tr_b16 v[184:185], v191 offset:0x600
	ds_read_b64_tr_b16 v[186:187], v191 offset:0x700
	v_mfma_f32_32x32x16_bf16 v[16:31], v[164:167], v[212:215], v[16:31]
	ds_read_b64_tr_b16 v[212:213], v191 offset:0x1600
	ds_read_b64_tr_b16 v[214:215], v191 offset:0x1700
	v_mfma_f32_32x32x16_bf16 v[16:31], v[168:171], v[218:221], v[16:31]
	ds_read_b64_tr_b16 v[218:219], v191 offset:0x2600
	ds_read_b64_tr_b16 v[220:221], v191 offset:0x2700
	ds_read_b64_tr_b16 v[226:227], v191 offset:0x3600
	ds_read_b64_tr_b16 v[228:229], v191 offset:0x3700
	s_waitcnt lgkmcnt(0)
	v_mfma_f32_32x32x16_bf16 v[16:31], v[172:175], v[222:225], v[16:31]
	v_mfma_f32_32x32x16_bf16 v[32:47], v[160:163], v[184:187], v[32:47]
	v_max_f32_e32 v188, v81, v81
	v_max_f32_e32 v189, v80, v80
	v_max_f32_e32 v188, v189, v188
	v_max3_f32 v188, v188, v82, v83
	v_max3_f32 v188, v188, v84, v85
	v_max3_f32 v160, v188, v86, v87
	v_max3_f32 v160, v160, v88, v89
	v_max3_f32 v160, v160, v90, v91
	v_mfma_f32_32x32x16_bf16 v[32:47], v[164:167], v[212:215], v[32:47]
	v_max3_f32 v160, v160, v92, v93
	v_max3_f32 v160, v160, v94, v95
	v_max3_f32 v160, v160, v64, v65
	v_max3_f32 v160, v160, v66, v67
	v_max3_f32 v160, v160, v68, v69
	v_max3_f32 v160, v160, v70, v71
	v_max3_f32 v160, v160, v72, v73
	v_max3_f32 v160, v160, v74, v75
	v_mfma_f32_32x32x16_bf16 v[32:47], v[168:171], v[218:221], v[32:47]
	v_max3_f32 v160, v160, v76, v77
	v_max3_f32 v160, v160, v78, v79
	v_mov_b32_e32 v161, v160
	s_nop 1
	v_permlane32_swap_b32_e32 v160, v161
	v_max_f32_e32 v161, v161, v161
	v_max_f32_e32 v160, v160, v160
	v_max_f32_e32 v160, v160, v161
	v_max_f32_e32 v162, v209, v209
	v_sub_f32_e32 v161, v160, v209
	v_max_f32_e32 v160, v162, v160
	v_mfma_f32_32x32x16_bf16 v[32:47], v[172:175], v[226:229], v[32:47]
	v_sub_f32_e32 v162, v209, v160
	v_mul_f32_e32 v162, 0x3e0293ee, v162
	v_exp_f32_e32 v162, v162
	v_cmp_ge_f32_e32 vcc, s9, v161
	s_cmp_eq_u64 vcc, exec
	s_cselect_b64 s[4:5], -1, 0
	s_barrier
	s_waitcnt vmcnt(4)
	v_cndmask_b32_e64 v161, v162, 1.0, s[4:5]
	v_cmp_gt_f32_e32 vcc, 1.0, v161
	s_waitcnt vmcnt(3)
	ds_write_b128 v193, v[144:147] offset:16384
	s_waitcnt vmcnt(2)
	ds_write_b128 v194, v[148:151] offset:16384
	s_waitcnt vmcnt(1)
	ds_write_b128 v195, v[152:155] offset:49152
	s_waitcnt vmcnt(0)
	ds_write_b128 v196, v[156:159] offset:49152
	s_cbranch_vccz .LBB0_923
	s_and_saveexec_b64 s[38:39], s[2:3]
	ds_write_b32 v179, v161 offset:128
	s_or_b64 exec, exec, s[38:39]
	s_waitcnt lgkmcnt(0)
	v_add_u32_e32 v156, s56, v176
	ds_read_b128 v[144:147], v156 offset:224
	ds_read_b128 v[148:151], v156 offset:192
	ds_read_b128 v[152:155], v156 offset:160
	ds_read_b128 v[156:159], v156 offset:128
	s_waitcnt lgkmcnt(3)
	v_pk_mul_f32 v[12:13], v[12:13], v[144:145]
	s_waitcnt lgkmcnt(2)
	v_pk_mul_f32 v[8:9], v[8:9], v[148:149]
	s_waitcnt lgkmcnt(1)
	v_pk_mul_f32 v[4:5], v[4:5], v[152:153]
	v_pk_mul_f32 v[14:15], v[14:15], v[146:147]
	v_pk_mul_f32 v[10:11], v[10:11], v[150:151]
	v_pk_mul_f32 v[6:7], v[6:7], v[154:155]
	s_waitcnt lgkmcnt(0)
	v_pk_mul_f32 v[2:3], v[2:3], v[158:159]
	v_pk_mul_f32 v[0:1], v[0:1], v[156:157]
	v_pk_mul_f32 v[60:61], v[60:61], v[144:145]
	v_pk_mul_f32 v[56:57], v[56:57], v[148:149]
	v_pk_mul_f32 v[52:53], v[52:53], v[152:153]
	v_pk_mul_f32 v[62:63], v[62:63], v[146:147]
	v_pk_mul_f32 v[58:59], v[58:59], v[150:151]
	v_pk_mul_f32 v[54:55], v[54:55], v[154:155]
	v_pk_mul_f32 v[50:51], v[50:51], v[158:159]
	v_pk_mul_f32 v[48:49], v[48:49], v[156:157]
	v_pk_mul_f32 v[28:29], v[28:29], v[144:145]
	v_pk_mul_f32 v[24:25], v[24:25], v[148:149]
	v_pk_mul_f32 v[20:21], v[20:21], v[152:153]
	v_pk_mul_f32 v[30:31], v[30:31], v[146:147]
	v_pk_mul_f32 v[26:27], v[26:27], v[150:151]
	v_pk_mul_f32 v[22:23], v[22:23], v[154:155]
	v_pk_mul_f32 v[18:19], v[18:19], v[158:159]
	v_pk_mul_f32 v[16:17], v[16:17], v[156:157]
	v_pk_mul_f32 v[44:45], v[44:45], v[144:145]
	v_pk_mul_f32 v[40:41], v[40:41], v[148:149]
	v_pk_mul_f32 v[36:37], v[36:37], v[152:153]
	v_pk_mul_f32 v[46:47], v[46:47], v[146:147]
	v_pk_mul_f32 v[42:43], v[42:43], v[150:151]
	v_pk_mul_f32 v[38:39], v[38:39], v[154:155]
	v_pk_mul_f32 v[34:35], v[34:35], v[158:159]
	v_pk_mul_f32 v[32:33], v[32:33], v[156:157]

.LBB0_925:
	ds_read_b128 v[64:67], v197 offset:49152
	ds_read_b128 v[68:71], v197 offset:57344
	v_exp_f32_e32 v152, v152
	v_exp_f32_e32 v153, v153
	v_exp_f32_e32 v150, v150
	s_waitcnt lgkmcnt(1)
	v_mfma_f32_32x32x16_bf16 v[80:95], v[64:67], v[124:127], 0
	v_exp_f32_e32 v151, v151
	v_exp_f32_e32 v148, v148
	s_waitcnt lgkmcnt(0)
	v_mfma_f32_32x32x16_bf16 v[64:79], v[68:71], v[124:127], 0
	ds_read_b128 v[124:127], v198 offset:49152
	ds_read_b128 v[128:131], v198 offset:57344
	ds_read_b128 v[132:135], v199 offset:49152
	ds_read_b128 v[136:139], v199 offset:57344
	s_waitcnt lgkmcnt(3)
	v_mfma_f32_32x32x16_bf16 v[80:95], v[124:127], v[120:123], v[80:95]
	ds_read_b128 v[124:127], v200 offset:49152
	ds_read_b128 v[140:143], v200 offset:57344
	ds_read_b128 v[180:183], v201 offset:49152
	ds_read_b128 v[194:197], v201 offset:57344
	ds_read_b128 v[198:201], v202 offset:49152
	ds_read_b128 v[206:209], v202 offset:57344
	ds_read_b128 v[210:213], v203 offset:49152
	ds_read_b128 v[218:221], v203 offset:57344
	s_waitcnt lgkmcnt(10)
	v_mfma_f32_32x32x16_bf16 v[64:79], v[128:131], v[120:123], v[64:79]
	ds_read_b128 v[120:123], v204 offset:49152
	ds_read_b128 v[128:131], v204 offset:57344
	s_waitcnt lgkmcnt(11)
	v_mfma_f32_32x32x16_bf16 v[80:95], v[132:135], v[116:119], v[80:95]
	v_exp_f32_e32 v132, v149
	v_exp_f32_e32 v133, v146
	v_exp_f32_e32 v134, v147
	v_exp_f32_e32 v135, v144
	v_exp_f32_e32 v144, v145
	v_exp_f32_e32 v145, v158
	v_exp_f32_e32 v146, v159
	s_waitcnt lgkmcnt(10)
	v_mfma_f32_32x32x16_bf16 v[64:79], v[136:139], v[116:119], v[64:79]
	v_add_f32_e32 v116, 0, v170
	v_add_f32_e32 v116, v171, v116
	v_add_f32_e32 v116, v172, v116
	v_add_f32_e32 v116, v173, v116
	v_add_f32_e32 v116, v174, v116
	v_add_f32_e32 v116, v184, v116
	v_add_f32_e32 v116, v175, v116
	s_waitcnt lgkmcnt(9)
	v_mfma_f32_32x32x16_bf16 v[80:95], v[124:127], v[112:115], v[80:95]
	v_add_f32_e32 v116, v185, v116
	v_add_f32_e32 v116, v162, v116
	v_add_f32_e32 v116, v163, v116
	v_exp_f32_e32 v118, v156
	v_exp_f32_e32 v119, v157
	v_exp_f32_e32 v136, v154
	v_exp_f32_e32 v137, v155
	s_waitcnt lgkmcnt(8)
	v_mfma_f32_32x32x16_bf16 v[64:79], v[140:143], v[112:115], v[64:79]
	v_add_f32_e32 v112, v164, v116
	v_add_f32_e32 v112, v166, v112
	v_add_f32_e32 v112, v165, v112
	v_add_f32_e32 v112, v167, v112
	v_add_f32_e32 v112, v168, v112
	v_add_f32_e32 v112, v169, v112
	v_add_f32_e32 v112, v152, v112
	s_waitcnt lgkmcnt(7)
	v_mfma_f32_32x32x16_bf16 v[80:95], v[180:183], v[108:111], v[80:95]
	v_add_f32_e32 v112, v153, v112
	v_add_f32_e32 v112, v150, v112
	v_add_f32_e32 v112, v151, v112
	v_add_f32_e32 v112, v148, v112
	v_add_f32_e32 v112, v132, v112
	v_add_f32_e32 v112, v133, v112
	v_add_f32_e32 v112, v134, v112
	s_waitcnt lgkmcnt(6)
	v_mfma_f32_32x32x16_bf16 v[64:79], v[194:197], v[108:111], v[64:79]
	v_add_f32_e32 v108, v135, v112
	v_add_f32_e32 v108, v144, v108
	v_add_f32_e32 v108, v145, v108
	v_add_f32_e32 v108, v146, v108
	v_add_f32_e32 v108, v118, v108
	v_add_f32_e32 v108, v119, v108
	v_add_f32_e32 v108, v136, v108
	s_waitcnt lgkmcnt(5)
	v_mfma_f32_32x32x16_bf16 v[80:95], v[198:201], v[104:107], v[80:95]
	v_add_f32_e32 v108, v137, v108
	v_mov_b32_e32 v109, v108
	s_nop 1
	v_permlane32_swap_b32_e32 v108, v109
	v_cvt_pk_bf16_f32 v110, v170, v171
	v_cvt_pk_bf16_f32 v111, v172, v173
	v_cvt_pk_bf16_f32 v112, v174, v184
	s_waitcnt lgkmcnt(4)
	v_mfma_f32_32x32x16_bf16 v[64:79], v[206:209], v[104:107], v[64:79]
	v_cvt_pk_bf16_f32 v113, v175, v185
	v_cvt_pk_bf16_f32 v104, v162, v163
	v_cvt_pk_bf16_f32 v105, v164, v166
	v_cvt_pk_bf16_f32 v106, v165, v167
	v_cvt_pk_bf16_f32 v107, v168, v169
	v_cvt_pk_bf16_f32 v114, v152, v153
	v_cvt_pk_bf16_f32 v115, v150, v151
	s_waitcnt lgkmcnt(3)
	v_mfma_f32_32x32x16_bf16 v[80:95], v[210:213], v[100:103], v[80:95]
	v_cvt_pk_bf16_f32 v116, v148, v132
	v_cvt_pk_bf16_f32 v117, v133, v134
	s_waitcnt lgkmcnt(2)
	v_mfma_f32_32x32x16_bf16 v[64:79], v[218:221], v[100:103], v[64:79]
	v_cvt_pk_bf16_f32 v100, v135, v144
	v_cvt_pk_bf16_f32 v101, v145, v146
	v_cvt_pk_bf16_f32 v102, v118, v119
	v_cvt_pk_bf16_f32 v103, v136, v137
	s_waitcnt lgkmcnt(1)
	v_mfma_f32_32x32x16_bf16 v[80:95], v[120:123], v[96:99], v[80:95]
	s_waitcnt lgkmcnt(0)
	v_mfma_f32_32x32x16_bf16 v[64:79], v[128:131], v[96:99], v[64:79]
	ds_read_b64_tr_b16 v[96:97], v192 offset:0x0
	ds_read_b64_tr_b16 v[98:99], v192 offset:0x100
	ds_read_b64_tr_b16 v[118:119], v192 offset:0x1000
	ds_read_b64_tr_b16 v[120:121], v192 offset:0x1100
	ds_read_b64_tr_b16 v[122:123], v192 offset:0x2000
	ds_read_b64_tr_b16 v[124:125], v192 offset:0x2100
	ds_read_b64_tr_b16 v[126:127], v192 offset:0x3000
	ds_read_b64_tr_b16 v[128:129], v192 offset:0x3100
	s_waitcnt lgkmcnt(0)
	s_nop 0
	v_mfma_f32_32x32x16_bf16 v[0:15], v[110:113], v[96:99], v[0:15]
	ds_read_b64_tr_b16 v[96:97], v192 offset:0x200
	ds_read_b64_tr_b16 v[98:99], v192 offset:0x300
	v_mfma_f32_32x32x16_bf16 v[0:15], v[104:107], v[118:121], v[0:15]
	ds_read_b64_tr_b16 v[118:119], v192 offset:0x1200
	ds_read_b64_tr_b16 v[120:121], v192 offset:0x1300
	v_mfma_f32_32x32x16_bf16 v[0:15], v[114:117], v[122:125], v[0:15]
	ds_read_b64_tr_b16 v[122:123], v192 offset:0x2200
	ds_read_b64_tr_b16 v[124:125], v192 offset:0x2300
	ds_read_b64_tr_b16 v[130:131], v192 offset:0x3200
	ds_read_b64_tr_b16 v[132:133], v192 offset:0x3300
	s_waitcnt lgkmcnt(0)
	v_mfma_f32_32x32x16_bf16 v[0:15], v[100:103], v[126:129], v[0:15]
	v_mfma_f32_32x32x16_bf16 v[48:63], v[110:113], v[96:99], v[48:63]
	ds_read_b64_tr_b16 v[96:97], v192 offset:0x400
	ds_read_b64_tr_b16 v[98:99], v192 offset:0x500
	v_mfma_f32_32x32x16_bf16 v[48:63], v[104:107], v[118:121], v[48:63]
	ds_read_b64_tr_b16 v[118:119], v192 offset:0x1400
	ds_read_b64_tr_b16 v[120:121], v192 offset:0x1500
	v_mfma_f32_32x32x16_bf16 v[48:63], v[114:117], v[122:125], v[48:63]
	ds_read_b64_tr_b16 v[122:123], v192 offset:0x2400
	ds_read_b64_tr_b16 v[124:125], v192 offset:0x2500
	ds_read_b64_tr_b16 v[126:127], v192 offset:0x3400
	ds_read_b64_tr_b16 v[128:129], v192 offset:0x3500
	s_waitcnt lgkmcnt(0)
	v_mfma_f32_32x32x16_bf16 v[48:63], v[100:103], v[130:133], v[48:63]
	v_mfma_f32_32x32x16_bf16 v[16:31], v[110:113], v[96:99], v[16:31]
	ds_read_b64_tr_b16 v[96:97], v192 offset:0x600
	ds_read_b64_tr_b16 v[98:99], v192 offset:0x700
	v_mfma_f32_32x32x16_bf16 v[16:31], v[104:107], v[118:121], v[16:31]
	ds_read_b64_tr_b16 v[118:119], v192 offset:0x1600
	ds_read_b64_tr_b16 v[120:121], v192 offset:0x1700
	v_mfma_f32_32x32x16_bf16 v[16:31], v[114:117], v[122:125], v[16:31]
	ds_read_b64_tr_b16 v[122:123], v192 offset:0x2600
	ds_read_b64_tr_b16 v[124:125], v192 offset:0x2700
	ds_read_b64_tr_b16 v[130:131], v192 offset:0x3600
	ds_read_b64_tr_b16 v[132:133], v192 offset:0x3700
	s_waitcnt lgkmcnt(0)
	v_mfma_f32_32x32x16_bf16 v[16:31], v[100:103], v[126:129], v[16:31]
	v_mfma_f32_32x32x16_bf16 v[32:47], v[110:113], v[96:99], v[32:47]
	v_max_f32_e32 v126, v81, v81
	v_max_f32_e32 v127, v80, v80
	v_max_f32_e32 v126, v127, v126
	v_max3_f32 v126, v126, v82, v83
	v_max3_f32 v126, v126, v84, v85
	v_max3_f32 v96, v126, v86, v87
	v_max3_f32 v96, v96, v88, v89
	v_max3_f32 v96, v96, v90, v91
	v_mfma_f32_32x32x16_bf16 v[32:47], v[104:107], v[118:121], v[32:47]
	v_max3_f32 v96, v96, v92, v93
	v_max3_f32 v96, v96, v94, v95
	v_max3_f32 v96, v96, v64, v65
	v_max3_f32 v96, v96, v66, v67
	v_max3_f32 v96, v96, v68, v69
	v_max3_f32 v96, v96, v70, v71
	v_max3_f32 v96, v96, v72, v73
	v_max3_f32 v96, v96, v74, v75
	v_mfma_f32_32x32x16_bf16 v[32:47], v[114:117], v[122:125], v[32:47]
	v_max3_f32 v96, v96, v76, v77
	v_max3_f32 v96, v96, v78, v79
	v_mov_b32_e32 v97, v96
	s_nop 1
	v_permlane32_swap_b32_e32 v96, v97
	v_max_f32_e32 v97, v97, v97
	v_max_f32_e32 v96, v96, v96
	v_max_f32_e32 v96, v96, v97
	v_max_f32_e32 v97, v160, v160
	v_max_f32_e32 v97, v97, v96
	v_sub_f32_e32 v98, v96, v160
	v_mfma_f32_32x32x16_bf16 v[32:47], v[100:103], v[130:133], v[32:47]
	v_sub_f32_e32 v96, v160, v97
	v_mul_f32_e32 v96, 0x3e0293ee, v96
	v_exp_f32_e32 v96, v96
	v_cmp_ge_f32_e32 vcc, s9, v98
	s_cmp_eq_u64 vcc, exec
	s_cselect_b64 s[4:5], -1, 0
	v_cndmask_b32_e64 v96, v96, 1.0, s[4:5]
	v_cmp_gt_f32_e32 vcc, 1.0, v96
	s_barrier
	s_cbranch_vccz .LBB0_929
	s_and_saveexec_b64 s[28:29], s[2:3]
	ds_write_b32 v179, v96 offset:128
	s_or_b64 exec, exec, s[28:29]
	s_waitcnt lgkmcnt(0)
	v_add_u32_e32 v106, s56, v176
	ds_read_b128 v[98:101], v106 offset:224
	ds_read_b128 v[102:105], v106 offset:192
	ds_read_b128 v[110:113], v106 offset:160
	ds_read_b128 v[114:117], v106 offset:128
	s_waitcnt lgkmcnt(3)
	v_pk_mul_f32 v[12:13], v[12:13], v[98:99]
	s_waitcnt lgkmcnt(2)
	v_pk_mul_f32 v[8:9], v[8:9], v[102:103]
	s_waitcnt lgkmcnt(1)
	v_pk_mul_f32 v[4:5], v[4:5], v[110:111]
	v_pk_mul_f32 v[14:15], v[14:15], v[100:101]
	v_pk_mul_f32 v[10:11], v[10:11], v[104:105]
	v_pk_mul_f32 v[6:7], v[6:7], v[112:113]
	s_waitcnt lgkmcnt(0)
	v_pk_mul_f32 v[2:3], v[2:3], v[116:117]
	v_pk_mul_f32 v[0:1], v[0:1], v[114:115]
	v_pk_mul_f32 v[60:61], v[60:61], v[98:99]
	v_pk_mul_f32 v[56:57], v[56:57], v[102:103]
	v_pk_mul_f32 v[52:53], v[52:53], v[110:111]
	v_pk_mul_f32 v[62:63], v[62:63], v[100:101]
	v_pk_mul_f32 v[58:59], v[58:59], v[104:105]
	v_pk_mul_f32 v[54:55], v[54:55], v[112:113]
	v_pk_mul_f32 v[50:51], v[50:51], v[116:117]
	v_pk_mul_f32 v[48:49], v[48:49], v[114:115]
	v_pk_mul_f32 v[28:29], v[28:29], v[98:99]
	v_pk_mul_f32 v[24:25], v[24:25], v[102:103]
	v_pk_mul_f32 v[20:21], v[20:21], v[110:111]
	v_pk_mul_f32 v[30:31], v[30:31], v[100:101]
	v_pk_mul_f32 v[26:27], v[26:27], v[104:105]
	v_pk_mul_f32 v[22:23], v[22:23], v[112:113]
	v_pk_mul_f32 v[18:19], v[18:19], v[116:117]
	v_pk_mul_f32 v[16:17], v[16:17], v[114:115]
	v_pk_mul_f32 v[44:45], v[44:45], v[98:99]
	v_pk_mul_f32 v[40:41], v[40:41], v[102:103]
	v_pk_mul_f32 v[36:37], v[36:37], v[110:111]
	v_pk_mul_f32 v[46:47], v[46:47], v[100:101]
	v_pk_mul_f32 v[42:43], v[42:43], v[104:105]
	v_pk_mul_f32 v[38:39], v[38:39], v[112:113]
	v_pk_mul_f32 v[34:35], v[34:35], v[116:117]
	v_pk_mul_f32 v[32:33], v[32:33], v[114:115]
.LBB0_929:
	v_cndmask_b32_e64 v97, v97, v160, s[4:5]
	v_mul_f32_e32 v97, 0xbe0293ee, v97
	v_fmamk_f32 v80, v80, 0x3e0293ee, v97
	v_fmamk_f32 v81, v81, 0x3e0293ee, v97
	v_fmamk_f32 v106, v93, 0x3e0293ee, v97
	v_fmamk_f32 v93, v74, 0x3e0293ee, v97
	v_exp_f32_e32 v74, v80
	v_fmamk_f32 v82, v82, 0x3e0293ee, v97
	v_fmamk_f32 v107, v94, 0x3e0293ee, v97
	v_fmamk_f32 v94, v75, 0x3e0293ee, v97
	v_exp_f32_e32 v75, v81
	v_fmamk_f32 v83, v83, 0x3e0293ee, v97
	v_fmamk_f32 v110, v95, 0x3e0293ee, v97
	v_fmamk_f32 v95, v76, 0x3e0293ee, v97
	v_exp_f32_e32 v76, v82
	v_fmamk_f32 v84, v84, 0x3e0293ee, v97
	v_fmamk_f32 v64, v64, 0x3e0293ee, v97
	v_exp_f32_e32 v80, v83
	v_fmamk_f32 v98, v85, 0x3e0293ee, v97
	v_fmamk_f32 v99, v86, 0x3e0293ee, v97
	v_fmamk_f32 v100, v87, 0x3e0293ee, v97
	v_fmamk_f32 v101, v88, 0x3e0293ee, v97
	v_fmamk_f32 v102, v89, 0x3e0293ee, v97
	v_fmamk_f32 v103, v90, 0x3e0293ee, v97
	v_fmamk_f32 v104, v91, 0x3e0293ee, v97
	v_fmamk_f32 v105, v92, 0x3e0293ee, v97
	v_fmamk_f32 v65, v65, 0x3e0293ee, v97
	v_fmamk_f32 v85, v66, 0x3e0293ee, v97
	v_fmamk_f32 v86, v67, 0x3e0293ee, v97
	v_fmamk_f32 v87, v68, 0x3e0293ee, v97
	v_fmamk_f32 v88, v69, 0x3e0293ee, v97
	v_fmamk_f32 v89, v70, 0x3e0293ee, v97
	v_fmamk_f32 v90, v71, 0x3e0293ee, v97
	v_fmamk_f32 v91, v72, 0x3e0293ee, v97
	v_fmamk_f32 v92, v73, 0x3e0293ee, v97
	v_exp_f32_e32 v81, v84
	v_fmamk_f32 v77, v77, 0x3e0293ee, v97
	v_fmamk_f32 v78, v78, 0x3e0293ee, v97
	v_fmac_f32_e32 v97, 0x3e0293ee, v79
	v_exp_f32_e32 v79, v64
	v_add_f32_e32 v64, 0, v74
	v_exp_f32_e32 v82, v98
	v_add_f32_e32 v64, v75, v64
	v_exp_f32_e32 v83, v99
	v_add_f32_e32 v64, v76, v64
	v_exp_f32_e32 v84, v100
	v_add_f32_e32 v64, v80, v64
	v_exp_f32_e32 v66, v101
	v_add_f32_e32 v64, v81, v64
	v_exp_f32_e32 v67, v102
	v_add_f32_e32 v64, v82, v64
	v_exp_f32_e32 v68, v103
	v_add_f32_e32 v64, v83, v64
	v_exp_f32_e32 v69, v104
	v_add_f32_e32 v64, v84, v64
	v_exp_f32_e32 v70, v105
	v_add_f32_e32 v64, v66, v64
	v_exp_f32_e32 v71, v106
	v_add_f32_e32 v64, v67, v64
	v_exp_f32_e32 v72, v107
	v_add_f32_e32 v64, v68, v64
	v_exp_f32_e32 v73, v110
	v_add_f32_e32 v64, v69, v64
	v_add_f32_e32 v64, v70, v64
	v_exp_f32_e32 v98, v65
	v_add_f32_e32 v64, v71, v64
	v_exp_f32_e32 v85, v85
	v_add_f32_e32 v64, v72, v64
	v_exp_f32_e32 v86, v86
	v_add_f32_e32 v64, v73, v64
	v_exp_f32_e32 v87, v87
	v_add_f32_e32 v64, v79, v64
	v_exp_f32_e32 v88, v88
	v_add_f32_e32 v64, v98, v64
	v_exp_f32_e32 v89, v89
	v_add_f32_e32 v64, v85, v64
	v_exp_f32_e32 v90, v90
	v_add_f32_e32 v64, v86, v64
	v_exp_f32_e32 v91, v91
	v_add_f32_e32 v64, v87, v64
	v_exp_f32_e32 v92, v92
	v_add_f32_e32 v64, v88, v64
	v_exp_f32_e32 v93, v93
	v_add_f32_e32 v64, v89, v64
	v_exp_f32_e32 v94, v94
	v_add_f32_e32 v64, v90, v64
	v_exp_f32_e32 v95, v95
	v_add_f32_e32 v64, v91, v64
	v_exp_f32_e32 v99, v77
	v_add_f32_e32 v64, v92, v64
	v_exp_f32_e32 v100, v78
	v_add_f32_e32 v64, v93, v64
	v_exp_f32_e32 v97, v97
	v_add_f32_e32 v64, v94, v64
	v_add_f32_e32 v64, v95, v64
	v_add_f32_e32 v64, v99, v64
	v_add_f32_e32 v64, v100, v64
	v_add_f32_e32 v64, v97, v64
	v_mov_b32_e32 v65, v64
	s_nop 1
	v_permlane32_swap_b32_e32 v64, v65
	v_cvt_pk_bf16_f32 v74, v74, v75
	v_cvt_pk_bf16_f32 v75, v76, v80
	v_cvt_pk_bf16_f32 v76, v81, v82
	v_cvt_pk_bf16_f32 v77, v83, v84
	v_cvt_pk_bf16_f32 v66, v66, v67
	v_cvt_pk_bf16_f32 v67, v68, v69
	v_cvt_pk_bf16_f32 v68, v70, v71
	v_cvt_pk_bf16_f32 v69, v72, v73
	v_cvt_pk_bf16_f32 v70, v79, v98
	v_cvt_pk_bf16_f32 v71, v85, v86
	v_cvt_pk_bf16_f32 v72, v87, v88
	v_cvt_pk_bf16_f32 v73, v89, v90
	v_cvt_pk_bf16_f32 v78, v91, v92
	v_cvt_pk_bf16_f32 v79, v93, v94
	v_cvt_pk_bf16_f32 v80, v95, v99
	v_cvt_pk_bf16_f32 v81, v100, v97
	ds_read_b64_tr_b16 v[82:83], v191 offset:0x0
	ds_read_b64_tr_b16 v[84:85], v191 offset:0x100
	ds_read_b64_tr_b16 v[86:87], v191 offset:0x1000
	ds_read_b64_tr_b16 v[88:89], v191 offset:0x1100
	ds_read_b64_tr_b16 v[90:91], v191 offset:0x2000
	ds_read_b64_tr_b16 v[92:93], v191 offset:0x2100
	ds_read_b64_tr_b16 v[98:99], v191 offset:0x3000
	ds_read_b64_tr_b16 v[100:101], v191 offset:0x3100
	s_waitcnt lgkmcnt(0)
	s_nop 0
	v_mfma_f32_32x32x16_bf16 v[0:15], v[74:77], v[82:85], v[0:15]
	ds_read_b64_tr_b16 v[82:83], v191 offset:0x200
	ds_read_b64_tr_b16 v[84:85], v191 offset:0x300
	v_mfma_f32_32x32x16_bf16 v[0:15], v[66:69], v[86:89], v[0:15]
	ds_read_b64_tr_b16 v[86:87], v191 offset:0x1200
	ds_read_b64_tr_b16 v[88:89], v191 offset:0x1300
	v_mfma_f32_32x32x16_bf16 v[0:15], v[70:73], v[90:93], v[0:15]
	ds_read_b64_tr_b16 v[90:91], v191 offset:0x2200
	ds_read_b64_tr_b16 v[92:93], v191 offset:0x2300
	ds_read_b64_tr_b16 v[102:103], v191 offset:0x3200
	ds_read_b64_tr_b16 v[104:105], v191 offset:0x3300
	s_waitcnt lgkmcnt(0)
	v_mfma_f32_32x32x16_bf16 v[0:15], v[78:81], v[98:101], v[0:15]
	v_mfma_f32_32x32x16_bf16 v[48:63], v[74:77], v[82:85], v[48:63]
	ds_read_b64_tr_b16 v[82:83], v191 offset:0x400
	ds_read_b64_tr_b16 v[84:85], v191 offset:0x500
	v_mfma_f32_32x32x16_bf16 v[48:63], v[66:69], v[86:89], v[48:63]
	ds_read_b64_tr_b16 v[86:87], v191 offset:0x1400
	ds_read_b64_tr_b16 v[88:89], v191 offset:0x1500
	v_mfma_f32_32x32x16_bf16 v[48:63], v[70:73], v[90:93], v[48:63]
	ds_read_b64_tr_b16 v[90:91], v191 offset:0x2400
	ds_read_b64_tr_b16 v[92:93], v191 offset:0x2500
	ds_read_b64_tr_b16 v[98:99], v191 offset:0x3400
	ds_read_b64_tr_b16 v[100:101], v191 offset:0x3500
	s_waitcnt lgkmcnt(0)
	v_mfma_f32_32x32x16_bf16 v[48:63], v[78:81], v[102:105], v[48:63]
	v_mfma_f32_32x32x16_bf16 v[16:31], v[74:77], v[82:85], v[16:31]
	ds_read_b64_tr_b16 v[82:83], v191 offset:0x600
	ds_read_b64_tr_b16 v[84:85], v191 offset:0x700
	v_mfma_f32_32x32x16_bf16 v[16:31], v[66:69], v[86:89], v[16:31]
	ds_read_b64_tr_b16 v[86:87], v191 offset:0x1600
	ds_read_b64_tr_b16 v[88:89], v191 offset:0x1700
	v_mfma_f32_32x32x16_bf16 v[16:31], v[70:73], v[90:93], v[16:31]
	ds_read_b64_tr_b16 v[90:91], v191 offset:0x2600
	ds_read_b64_tr_b16 v[92:93], v191 offset:0x2700
	ds_read_b64_tr_b16 v[102:103], v191 offset:0x3600
	ds_read_b64_tr_b16 v[104:105], v191 offset:0x3700
	s_waitcnt lgkmcnt(0)
	v_mfma_f32_32x32x16_bf16 v[16:31], v[78:81], v[98:101], v[16:31]
	v_mfma_f32_32x32x16_bf16 v[32:47], v[74:77], v[82:85], v[32:47]
	v_mfma_f32_32x32x16_bf16 v[32:47], v[66:69], v[86:89], v[32:47]
	v_mfma_f32_32x32x16_bf16 v[32:47], v[70:73], v[90:93], v[32:47]
	v_mfma_f32_32x32x16_bf16 v[32:47], v[78:81], v[102:105], v[32:47]
	s_and_saveexec_b64 s[4:5], s[2:3]
	s_cbranch_execz .LBB0_903
	v_add_f32_e32 v66, v108, v109
	v_fmac_f32_e32 v66, v190, v161
	v_add_f32_e32 v64, v64, v65
	v_fmac_f32_e32 v64, v66, v96
	ds_write_b32 v179, v64
	s_branch .LBB0_903

.LBB0_944:
	s_and_b64 vcc, exec, s[24:25]
	s_cbranch_vccz .LBB0_933
	s_ashr_i32 s2, s68, 4
	s_mul_hi_i32 s3, s2, 0x2aaaaaab
	s_load_dwordx2 s[24:25], s[4:5], 0x78
	s_lshr_b32 s4, s3, 31
	s_add_i32 s3, s3, s4
	s_mul_i32 s3, s3, 6
	s_sub_i32 s69, s2, s3
	s_mul_hi_i32 s2, s68, 0x2aaaaaab
	s_lshr_b32 s3, s2, 31
	s_ashr_i32 s2, s2, 4
	s_add_i32 s4, s2, s3
	s_ashr_i32 s5, s4, 31
	s_lshl_b32 s2, s68, 8
	s_lshl_b64 s[26:27], s[4:5], 12
	s_and_b32 s2, s2, 0xf00
	s_or_b32 s26, s26, s2
	s_mul_i32 s2, s27, 0xa00
	s_mul_hi_u32 s3, s26, 0xa00
	s_add_i32 s3, s3, s2
	s_mul_i32 s2, s26, 0xa00
	s_add_u32 s28, s22, s2
	s_mul_i32 s2, s69, 0xc0
	s_addc_u32 s29, s23, s3
	s_ashr_i32 s3, s2, 31
	s_lshl_b64 s[2:3], s[2:3], 1
	s_add_u32 s2, s28, s2
	s_addc_u32 s3, s29, s3
	s_add_u32 s34, s2, 0x4bb60200
	s_addc_u32 s35, s3, 0
	s_mul_i32 s3, s4, 0xc00000
	s_mul_hi_i32 s2, s4, 0xc00000
	s_add_u32 s30, s22, s3
	s_addc_u32 s31, s23, s2
	s_lshl_b32 s2, s69, 8
	s_ashr_i32 s3, s2, 31
	s_lshl_b64 s[28:29], s[2:3], 1
	s_add_u32 s2, s30, s28
	s_addc_u32 s3, s31, s29
	s_waitcnt lgkmcnt(0)
	s_add_u32 s2, s2, 0x4e360200
	s_addc_u32 s3, s3, 0
	v_ashrrev_i32_e32 v53, 4, v52
	v_lshlrev_b32_e32 v24, 3, v52
	s_lshl_b64 s[30:31], s[4:5], 19
	v_and_b32_e32 v62, 0x78, v24
	v_ashrrev_i32_e32 v20, 3, v52
	v_mad_i64_i32 v[0:1], s[40:41], v53, s19, 0
	s_add_u32 s38, s22, s30
	v_add_u32_e32 v25, 32, v53
	v_or_b32_e32 v0, v0, v62
	v_ashrrev_i32_e32 v21, 31, v20
	s_addc_u32 s39, s23, s31
	v_lshlrev_b32_e32 v54, 4, v52
	v_lshl_add_u64 v[4:5], v[0:1], 1, s[2:3]
	v_mad_i64_i32 v[0:1], s[40:41], v25, s19, 0
	v_lshlrev_b64 v[48:49], 7, v[20:21]
	v_or_b32_e32 v0, v0, v62
	v_lshl_add_u64 v[16:17], s[38:39], 0, v[48:49]
	v_and_b32_e32 v58, 0x70, v54
	v_mov_b32_e32 v59, v145
	v_lshl_add_u64 v[12:13], v[0:1], 1, s[2:3]
	v_lshl_add_u64 v[50:51], v[16:17], 0, v[58:59]
	global_load_dwordx4 v[0:3], v[4:5], off offset:256
	s_nop 0
	global_load_dwordx4 v[4:7], v[4:5], off
	s_nop 0
	global_load_dwordx4 v[8:11], v[12:13], off offset:256
	s_nop 0
	global_load_dwordx4 v[12:15], v[12:13], off
	v_add_co_u32_e32 v16, vcc, s33, v50
	v_readfirstlane_b32 s5, v52
	s_nop 0
	v_addc_co_u32_e32 v17, vcc, 0, v51, vcc
	s_ashr_i32 s37, s5, 1
	global_load_dwordx4 v[16:19], v[16:17], off offset:512
	v_mov_b32_e32 v21, s37
	v_bfe_u32 v171, v52, 5, 1
	v_bfi_b32 v21, s17, v21, v52
	v_mov_b64_e32 v[22:23], s[34:35]
	v_mad_i64_i32 v[22:23], s[34:35], v21, s9, v[22:23]
	v_lshlrev_b32_e32 v144, 4, v171
	v_lshl_add_u64 v[22:23], v[22:23], 0, v[144:145]
	global_load_dwordx4 v[140:143], v[22:23], off
	global_load_dwordx4 v[136:139], v[22:23], off offset:32
	global_load_dwordx4 v[132:135], v[22:23], off offset:64
	global_load_dwordx4 v[128:131], v[22:23], off offset:96
	global_load_dwordx4 v[124:127], v[22:23], off offset:128
	global_load_dwordx4 v[120:123], v[22:23], off offset:160
	global_load_dwordx4 v[116:119], v[22:23], off offset:192
	global_load_dwordx4 v[112:115], v[22:23], off offset:224
	global_load_dwordx4 v[108:111], v[22:23], off offset:256
	global_load_dwordx4 v[104:107], v[22:23], off offset:288
	global_load_dwordx4 v[100:103], v[22:23], off offset:320
	global_load_dwordx4 v[96:99], v[22:23], off offset:352
	v_and_b32_e32 v21, 0xfffff0, v53
	v_lshlrev_b32_e32 v22, 1, v53
	v_and_or_b32 v21, v22, 8, v21
	v_lshrrev_b32_e32 v22, 1, v53
	v_lshrrev_b32_e32 v21, 1, v21
	v_bfe_u32 v23, v24, 5, 2
	v_and_b32_e32 v24, 3, v53
	v_and_b32_e32 v27, 0xfffff0, v25
	v_lshlrev_b32_e32 v25, 1, v25
	v_or_b32_e32 v21, v21, v23
	v_and_or_b32 v22, v22, 4, v24
	v_lshlrev_b32_e32 v24, 1, v62
	v_and_or_b32 v25, v25, 8, v27
	v_lshlrev_b32_e32 v21, 9, v21
	v_lshlrev_b32_e32 v22, 6, v22
	v_and_b32_e32 v26, 48, v24
	v_lshrrev_b32_e32 v25, 1, v25
	v_or3_b32 v21, v21, v22, v26
	v_or_b32_e32 v23, v25, v23
	v_lshlrev_b32_e32 v23, 9, v23
	v_add_u32_e32 v175, 0, v21
	v_or3_b32 v22, v23, v22, v26
	s_waitcnt vmcnt(0)
	v_and_b32_e32 v146, 31, v52
	v_add_u32_e32 v176, 0, v22
	v_or_b32_e32 v59, 32, v144
	v_or_b32_e32 v60, 64, v144
	v_or_b32_e32 v61, 0x60, v144
	v_bitop3_b32 v63, v144, v58, s52 bitop3:0x36
	v_bitop3_b32 v64, v144, v58, s53 bitop3:0x36
	v_bitop3_b32 v65, v144, v58, s16 bitop3:0x36
	v_bitop3_b32 v66, v144, v58, s54 bitop3:0x36
	v_bitop3_b32 v67, v144, v58, s0 bitop3:0x36
	v_and_b32_e32 v74, 63, v52
	v_bitop3_b32 v68, v144, v58, s55 bitop3:0x36
	v_bitop3_b32 v70, v144, v58, s56 bitop3:0x36
	v_bitop3_b32 v71, v144, v58, s57 bitop3:0x36
	s_and_b32 s34, s37, 0xffffffe0
	s_mov_b32 s37, s36
	s_mov_b32 s38, s36
	s_mov_b32 s39, s36
	s_mov_b32 s40, s36
	s_mov_b32 s41, s36
	s_mov_b32 s42, s36
	s_mov_b32 s43, s36
	s_mov_b32 s44, s36
	s_mov_b32 s45, s36
	s_mov_b32 s46, s36
	s_mov_b32 s47, s36
	s_mov_b32 s48, s36
	s_mov_b32 s49, s36
	s_mov_b32 s50, s36
	s_mov_b32 s51, s36
	v_add_co_u32_e32 v50, vcc, s59, v50
	s_and_b32 s5, s5, 0x3fffffc0
	s_nop 0
	v_addc_co_u32_e32 v51, vcc, 0, v51, vcc
	s_lshl_b32 s5, s5, 2
	s_waitcnt vmcnt(16)
	ds_write_b128 v175, v[0:3]
	v_mul_lo_u32 v0, v53, s1
	v_bitop3_b32 v1, v24, v52, s21 bitop3:0x78
	v_lshlrev_b32_e32 v2, 4, v20
	v_add3_u32 v177, v1, v0, 0
	v_mul_lo_u32 v0, v20, s1
	v_or_b32_e32 v1, 0x100, v58
	v_and_b32_e32 v2, 0x70, v2
	s_waitcnt vmcnt(14)
	ds_write_b128 v176, v[8:11]
	v_xad_u32 v0, v1, v2, v0
	v_mul_u32_u24_e32 v8, 0x180, v146
	v_add_u32_e32 v178, 0, v0
	v_bitop3_b32 v0, v144, v8, v58 bitop3:0xde
	v_add_u32_e32 v179, 0, v0
	ds_write_b128 v177, v[4:7] offset:32768
	s_waitcnt vmcnt(13)
	ds_write_b128 v177, v[12:15] offset:45056
	s_waitcnt vmcnt(12)
	ds_write_b128 v178, v[16:19] offset:32768
	s_waitcnt lgkmcnt(0)
	s_barrier
	ds_read_b128 v[0:3], v179 offset:32768
	ds_read_b128 v[4:7], v179 offset:45056
	s_waitcnt vmcnt(11) lgkmcnt(1)
	v_mfma_f32_32x32x16_bf16 v[32:47], v[0:3], v[140:143], 0
	v_bitop3_b32 v0, v59, v8, v58 bitop3:0xde
	v_add_u32_e32 v180, 0, v0
	s_add_i32 s35, s5, 0
	s_add_i32 s35, s35, 0x14000
	s_cmp_lg_u32 0, -1
	s_cselect_b32 s5, 0, 0
	v_lshl_add_u64 v[150:151], s[30:31], 0, v[48:49]
	s_waitcnt lgkmcnt(0)
	v_mfma_f32_32x32x16_bf16 v[16:31], v[4:7], v[140:143], 0
	ds_read_b128 v[0:3], v180 offset:32768
	ds_read_b128 v[4:7], v180 offset:45056
	v_add_u32_e32 v191, 0x3000, v177
	s_mov_b32 s70, -1
	v_lshl_add_u32 v147, v146, 2, s35
	v_mov_b32_e32 v172, 0
	s_waitcnt vmcnt(10) lgkmcnt(1)
	v_mfma_f32_32x32x16_bf16 v[32:47], v[0:3], v[136:139], v[32:47]
	v_bitop3_b32 v0, v60, v8, v58 bitop3:0xde
	v_add_u32_e32 v181, 0, v0
	s_waitcnt lgkmcnt(0)
	v_mfma_f32_32x32x16_bf16 v[16:31], v[4:7], v[136:139], v[16:31]
	ds_read_b128 v[0:3], v181 offset:32768
	ds_read_b128 v[4:7], v181 offset:45056
	s_waitcnt vmcnt(9) lgkmcnt(1)
	v_mfma_f32_32x32x16_bf16 v[32:47], v[0:3], v[132:135], v[32:47]
	v_bitop3_b32 v0, v61, v8, v58 bitop3:0xde
	v_add_u32_e32 v182, 0, v0
	v_lshlrev_b32_e32 v8, 3, v74
	s_waitcnt lgkmcnt(0)
	v_mfma_f32_32x32x16_bf16 v[16:31], v[4:7], v[132:135], v[16:31]
	ds_read_b128 v[0:3], v182 offset:32768
	ds_read_b128 v[4:7], v182 offset:45056
	s_waitcnt vmcnt(8) lgkmcnt(1)
	v_mfma_f32_32x32x16_bf16 v[32:47], v[0:3], v[128:131], v[32:47]
	v_mad_u32_u24 v0, v146, s1, v63
	v_add_u32_e32 v183, 0, v0
	s_waitcnt lgkmcnt(0)
	v_mfma_f32_32x32x16_bf16 v[16:31], v[4:7], v[128:131], v[16:31]
	ds_read_b128 v[0:3], v183 offset:32768
	ds_read_b128 v[4:7], v183 offset:45056
	s_waitcnt vmcnt(7) lgkmcnt(1)
	v_mfma_f32_32x32x16_bf16 v[32:47], v[0:3], v[124:127], v[32:47]
	v_mad_u32_u24 v0, v146, s1, v64
	v_add_u32_e32 v184, 0, v0
	s_waitcnt lgkmcnt(0)
	v_mfma_f32_32x32x16_bf16 v[16:31], v[4:7], v[124:127], v[16:31]
	ds_read_b128 v[0:3], v184 offset:32768
	ds_read_b128 v[4:7], v184 offset:45056
	s_waitcnt vmcnt(6) lgkmcnt(1)
	v_mfma_f32_32x32x16_bf16 v[32:47], v[0:3], v[120:123], v[32:47]
	v_mad_u32_u24 v0, v146, s1, v65
	v_add_u32_e32 v185, 0, v0
	s_waitcnt lgkmcnt(0)
	v_mfma_f32_32x32x16_bf16 v[16:31], v[4:7], v[120:123], v[16:31]
	ds_read_b128 v[0:3], v185 offset:32768
	ds_read_b128 v[4:7], v185 offset:45056
	s_waitcnt vmcnt(5) lgkmcnt(1)
	v_mfma_f32_32x32x16_bf16 v[32:47], v[0:3], v[116:119], v[32:47]
	v_mad_u32_u24 v0, v146, s1, v66
	v_add_u32_e32 v186, 0, v0
	ds_read_b128 v[0:3], v186 offset:32768
	s_waitcnt lgkmcnt(1)
	v_mfma_f32_32x32x16_bf16 v[16:31], v[4:7], v[116:119], v[16:31]
	ds_read_b128 v[4:7], v186 offset:45056
	s_waitcnt vmcnt(4) lgkmcnt(1)
	v_mfma_f32_32x32x16_bf16 v[32:47], v[0:3], v[112:115], v[32:47]
	v_mad_u32_u24 v0, v146, s1, v67
	v_add_u32_e32 v187, 0, v0
	ds_read_b128 v[0:3], v187 offset:32768
	s_waitcnt lgkmcnt(1)
	v_mfma_f32_32x32x16_bf16 v[16:31], v[4:7], v[112:115], v[16:31]
	v_and_b32_e32 v4, 0xc0, v54
	v_lshlrev_b32_e32 v5, 1, v52
	v_and_or_b32 v4, v8, 24, v4
	v_and_b32_e32 v5, 32, v5
	v_lshlrev_b32_e32 v6, 3, v8
	v_and_b32_e32 v6, 0x800, v6
	v_or3_b32 v75, v4, v5, v6
	ds_read_b128 v[4:7], v187 offset:45056
	s_waitcnt vmcnt(3) lgkmcnt(1)
	v_mfma_f32_32x32x16_bf16 v[32:47], v[0:3], v[108:111], v[32:47]
	v_mad_u32_u24 v0, v146, s1, v68
	v_add_u32_e32 v188, 0, v0
	ds_read_b128 v[0:3], v188 offset:32768
	v_add_u32_e32 v174, s5, v75
	s_waitcnt lgkmcnt(1)
	v_mfma_f32_32x32x16_bf16 v[16:31], v[4:7], v[108:111], v[16:31]
	v_mov_b32_e32 v4, 0x3000
	v_mad_u32_u24 v69, v146, s1, v4
	ds_read_b128 v[4:7], v188 offset:45056
	v_bitop3_b32 v76, v144, v69, v58 bitop3:0xde
	v_bitop3_b32 v77, v59, v69, v58 bitop3:0xde
	v_bitop3_b32 v78, v60, v69, v58 bitop3:0xde
	v_bitop3_b32 v79, v61, v69, v58 bitop3:0xde
	s_waitcnt vmcnt(2) lgkmcnt(1)
	v_mfma_f32_32x32x16_bf16 v[32:47], v[0:3], v[104:107], v[32:47]
	v_mad_u32_u24 v0, v146, s1, v70
	v_add_u32_e32 v189, 0, v0
	ds_read_b128 v[0:3], v189 offset:32768
	v_add_u32_e32 v83, v66, v69
	v_add_u32_e32 v84, v67, v69
	v_add_u32_e32 v80, v63, v69
	v_add_u32_e32 v81, v64, v69
	s_waitcnt lgkmcnt(1)
	v_mfma_f32_32x32x16_bf16 v[16:31], v[4:7], v[104:107], v[16:31]
	ds_read_b128 v[4:7], v189 offset:45056
	v_add_u32_e32 v82, v65, v69
	v_add_u32_e32 v85, v68, v69
	v_add_u32_e32 v86, v70, v69
	v_add_u32_e32 v87, v71, v69
	v_add_u32_e32 v203, 0, v76
	v_add_u32_e32 v204, 0, v77
	s_waitcnt vmcnt(1) lgkmcnt(1)
	v_mfma_f32_32x32x16_bf16 v[32:47], v[0:3], v[100:103], v[32:47]
	v_mad_u32_u24 v0, v146, s1, v71
	v_add_u32_e32 v190, 0, v0
	ds_read_b128 v[54:57], v190 offset:32768
	ds_read_b128 v[58:61], v190 offset:45056
	v_add_u32_e32 v201, 0, v78
	v_add_u32_e32 v202, 0, v79
	v_add_u32_e32 v199, 0, v80
	s_waitcnt lgkmcnt(2)
	v_mfma_f32_32x32x16_bf16 v[16:31], v[4:7], v[100:103], v[16:31]
	v_mov_b64_e32 v[0:1], s[36:37]
	v_mov_b64_e32 v[2:3], s[38:39]
	v_mov_b64_e32 v[4:5], s[40:41]
	v_mov_b64_e32 v[6:7], s[42:43]
	v_mov_b64_e32 v[8:9], s[44:45]
	v_mov_b64_e32 v[10:11], s[46:47]
	v_mov_b64_e32 v[12:13], s[48:49]
	s_waitcnt vmcnt(0) lgkmcnt(1)
	v_mfma_f32_32x32x16_bf16 v[32:47], v[54:57], v[96:99], v[32:47]
	v_add_u32_e32 v54, 64, v53
	v_mov_b64_e32 v[14:15], s[50:51]
	v_mad_i64_i32 v[54:55], s[38:39], v54, s19, 0
	v_or_b32_e32 v54, v54, v62
	v_add_u32_e32 v200, 0, v81
	v_add_u32_e32 v197, 0, v82
	s_waitcnt lgkmcnt(0)
	v_mfma_f32_32x32x16_bf16 v[16:31], v[58:61], v[96:99], v[16:31]
	v_lshl_add_u64 v[58:59], v[54:55], 1, s[2:3]
	v_add_u32_e32 v54, 0x60, v53
	v_mad_i64_i32 v[54:55], s[38:39], v54, s19, 0
	v_or_b32_e32 v54, v54, v62
	v_lshl_add_u64 v[66:67], v[54:55], 1, s[2:3]
	global_load_dwordx4 v[54:57], v[58:59], off offset:256
	s_nop 0
	global_load_dwordx4 v[58:61], v[58:59], off
	s_nop 0
	global_load_dwordx4 v[62:65], v[66:67], off offset:256
	s_nop 0
	global_load_dwordx4 v[66:69], v[66:67], off
	v_max_f32_e32 v88, v33, v33
	global_load_dwordx4 v[70:73], v[50:51], off offset:512
	v_max_f32_e32 v89, v32, v32
	v_max_f32_e32 v50, v89, v88
	v_max3_f32 v50, v50, v34, v35
	v_max3_f32 v50, v50, v36, v37
	v_max3_f32 v50, v50, v38, v39
	v_max3_f32 v50, v50, v40, v41
	v_max3_f32 v50, v50, v42, v43
	v_max3_f32 v50, v50, v44, v45
	v_max3_f32 v50, v50, v46, v47
	v_max3_f32 v50, v50, v16, v17
	v_max3_f32 v50, v50, v18, v19
	v_max3_f32 v50, v50, v20, v21
	v_max3_f32 v50, v50, v22, v23
	v_max3_f32 v50, v50, v24, v25
	v_max3_f32 v50, v50, v26, v27
	v_max3_f32 v50, v50, v28, v29
	v_max3_f32 v50, v50, v30, v31
	v_mov_b32_e32 v51, v50
	s_nop 1
	v_permlane32_swap_b32_e32 v50, v51
	v_max_f32_e32 v51, v51, v51
	v_max_f32_e32 v50, v50, v50
	v_max_f32_e32 v50, v50, v51
	v_add_f32_e32 v51, 0x7149f2ca, v50
	v_max_f32_e32 v50, 0xf149f2ca, v50
	v_cmp_ge_f32_e32 vcc, s58, v51
	v_sub_f32_e32 v51, 0xf149f2ca, v50
	v_mul_f32_e32 v51, 0x3dd53b94, v51
	v_exp_f32_e32 v51, v51
	s_cmp_eq_u64 vcc, exec
	s_cselect_b64 vcc, -1, 0
	v_mov_b32_e32 v88, 0xf149f2ca
	v_cndmask_b32_e32 v205, v50, v88, vcc
	v_mul_f32_e32 v50, 0xbdd53b94, v205
	v_cndmask_b32_e64 v196, v51, 1.0, vcc
	v_mov_b32_e32 v51, v50
	v_fmac_f32_e32 v51, 0x3dd53b94, v47
	v_pk_fma_f32 v[162:163], v[16:17], s[8:9], v[50:51] op_sel_hi:[1,0,0]
	s_addk_i32 s5, 0x4000
	v_mad_i64_i32 v[16:17], s[38:39], v53, s60, 0
	v_fmamk_f32 v32, v32, 0x3dd53b94, v50
	v_fmamk_f32 v33, v33, 0x3dd53b94, v50
	v_fmamk_f32 v34, v34, 0x3dd53b94, v50
	v_fmamk_f32 v35, v35, 0x3dd53b94, v50
	v_fmamk_f32 v36, v36, 0x3dd53b94, v50
	v_fmamk_f32 v37, v37, 0x3dd53b94, v50
	v_fmamk_f32 v38, v38, 0x3dd53b94, v50
	v_fmamk_f32 v39, v39, 0x3dd53b94, v50
	v_fmamk_f32 v40, v40, 0x3dd53b94, v50
	v_fmamk_f32 v41, v41, 0x3dd53b94, v50
	v_fmamk_f32 v42, v42, 0x3dd53b94, v50
	v_fmamk_f32 v43, v43, 0x3dd53b94, v50
	v_fmamk_f32 v44, v44, 0x3dd53b94, v50
	v_fmamk_f32 v45, v45, 0x3dd53b94, v50
	v_fmamk_f32 v46, v46, 0x3dd53b94, v50
	v_pk_fma_f32 v[160:161], v[18:19], s[8:9], v[50:51] op_sel_hi:[1,0,0]
	v_add_u32_e32 v173, s5, v75
	v_mad_i64_i32 v[16:17], s[4:5], s4, v170, v[16:17]
	v_and_b32_e32 v18, 15, v52
	v_exp_f32_e32 v219, v32
	v_exp_f32_e32 v220, v33
	v_exp_f32_e32 v221, v34
	v_exp_f32_e32 v223, v35
	v_exp_f32_e32 v224, v36
	v_exp_f32_e32 v226, v37
	v_exp_f32_e32 v222, v38
	v_exp_f32_e32 v225, v39
	v_exp_f32_e32 v210, v40
	v_exp_f32_e32 v212, v41
	v_exp_f32_e32 v213, v42
	v_exp_f32_e32 v217, v43
	v_exp_f32_e32 v211, v44
	v_exp_f32_e32 v214, v45
	v_exp_f32_e32 v215, v46
	v_exp_f32_e32 v218, v51
	v_lshl_or_b32 v16, v18, 4, v16
	s_waitcnt vmcnt(0)
	v_lshl_add_u64 v[148:149], v[16:17], 0, s[28:29]
	v_and_b32_e32 v16, 7, v52
	v_pk_fma_f32 v[158:159], v[30:31], s[8:9], v[50:51] op_sel_hi:[1,0,0]
	v_pk_fma_f32 v[164:165], v[28:29], s[8:9], v[50:51] op_sel_hi:[1,0,0]
	v_pk_fma_f32 v[166:167], v[26:27], s[8:9], v[50:51] op_sel_hi:[1,0,0]
	v_pk_fma_f32 v[152:153], v[24:25], s[8:9], v[50:51] op_sel_hi:[1,0,0]
	v_pk_fma_f32 v[154:155], v[22:23], s[8:9], v[50:51] op_sel_hi:[1,0,0]
	v_pk_fma_f32 v[156:157], v[20:21], s[8:9], v[50:51] op_sel_hi:[1,0,0]
	s_waitcnt vmcnt(4)
	ds_write_b128 v175, v[54:57] offset:16384
	s_waitcnt vmcnt(2)
	ds_write_b128 v176, v[62:65] offset:16384
	ds_write_b128 v177, v[58:61] offset:57344
	s_waitcnt vmcnt(1)
	ds_write_b128 v191, v[66:69] offset:57344
	s_waitcnt vmcnt(0)
	ds_write_b128 v178, v[70:73] offset:57344
	v_lshl_or_b32 v150, v16, 4, v150
	v_mov_b64_e32 v[62:63], v[14:15]
	v_mov_b64_e32 v[30:31], v[14:15]
	v_mov_b64_e32 v[46:47], v[14:15]
	v_cmp_gt_u32_e64 s[2:3], 32, v74
	v_add_u32_e32 v198, 0, v83
	v_add_u32_e32 v194, 0, v84
	v_add_u32_e32 v195, 0, v85
	v_add_u32_e32 v192, 0, v86
	v_add_u32_e32 v193, 0, v87
	v_mov_b64_e32 v[60:61], v[12:13]
	v_mov_b64_e32 v[58:59], v[10:11]
	v_mov_b64_e32 v[56:57], v[8:9]
	v_mov_b64_e32 v[54:55], v[6:7]
	v_mov_b64_e32 v[52:53], v[4:5]
	v_mov_b64_e32 v[50:51], v[2:3]
	v_mov_b64_e32 v[48:49], v[0:1]
	v_mov_b64_e32 v[28:29], v[12:13]
	v_mov_b64_e32 v[26:27], v[10:11]
	v_mov_b64_e32 v[24:25], v[8:9]
	v_mov_b64_e32 v[22:23], v[6:7]
	v_mov_b64_e32 v[20:21], v[4:5]
	v_mov_b64_e32 v[18:19], v[2:3]
	v_mov_b64_e32 v[16:17], v[0:1]
	v_mov_b64_e32 v[44:45], v[12:13]
	v_mov_b64_e32 v[42:43], v[10:11]
	v_mov_b64_e32 v[40:41], v[8:9]
	v_mov_b64_e32 v[38:39], v[6:7]
	v_mov_b64_e32 v[36:37], v[4:5]
	v_mov_b64_e32 v[34:35], v[2:3]
	v_mov_b64_e32 v[32:33], v[0:1]
	s_waitcnt lgkmcnt(0)
	s_barrier
.LBB0_946:
	ds_read_b128 v[64:67], v179 offset:57344
	ds_read_b128 v[68:71], v203 offset:57344
	ds_read_b128 v[206:209], v180 offset:57344
	ds_read_b128 v[228:231], v204 offset:57344
	v_exp_f32_e32 v216, v156
	v_add_f32_e32 v156, 0, v219
	s_waitcnt lgkmcnt(3)
	v_mfma_f32_32x32x16_bf16 v[80:95], v[64:67], v[140:143], 0
	v_add_f32_e32 v156, v220, v156
	v_add_f32_e32 v156, v221, v156
	v_add_f32_e32 v156, v223, v156
	v_add_f32_e32 v156, v224, v156
	v_add_f32_e32 v156, v226, v156
	v_add_f32_e32 v156, v222, v156
	v_add_f32_e32 v156, v225, v156
	s_waitcnt lgkmcnt(2)
	v_mfma_f32_32x32x16_bf16 v[64:79], v[68:71], v[140:143], 0
	v_add_f32_e32 v156, v210, v156
	v_add_f32_e32 v156, v212, v156
	v_add_f32_e32 v156, v213, v156
	v_add_f32_e32 v156, v217, v156
	v_exp_f32_e32 v168, v162
	v_add_f32_e32 v156, v211, v156
	v_exp_f32_e32 v169, v163
	s_waitcnt lgkmcnt(1)
	v_mfma_f32_32x32x16_bf16 v[80:95], v[206:209], v[136:139], v[80:95]
	v_add_f32_e32 v156, v214, v156
	v_add_f32_e32 v156, v215, v156
	v_add_f32_e32 v156, v218, v156
	v_add_f32_e32 v156, v168, v156
	v_exp_f32_e32 v227, v157
	v_add_f32_e32 v156, v169, v156
	v_exp_f32_e32 v154, v154
	s_waitcnt lgkmcnt(0)
	v_mfma_f32_32x32x16_bf16 v[64:79], v[228:231], v[136:139], v[64:79]
	ds_read_b128 v[206:209], v181 offset:57344
	ds_read_b128 v[228:231], v201 offset:57344
	v_exp_f32_e32 v155, v155
	v_exp_f32_e32 v152, v152
	v_exp_f32_e32 v153, v153
	v_exp_f32_e32 v232, v158
	v_exp_f32_e32 v233, v159
	v_cvt_pk_bf16_f32 v158, v224, v226
	s_waitcnt lgkmcnt(1)
	v_mfma_f32_32x32x16_bf16 v[80:95], v[206:209], v[132:135], v[80:95]
	v_cvt_pk_bf16_f32 v162, v211, v214
	v_cvt_pk_bf16_f32 v211, v232, v233
	v_cvt_pk_bf16_f32 v157, v221, v223
	v_cvt_pk_bf16_f32 v159, v222, v225
	v_cvt_pk_bf16_f32 v163, v215, v218
	s_waitcnt lgkmcnt(0)
	v_mfma_f32_32x32x16_bf16 v[64:79], v[228:231], v[132:135], v[64:79]
	ds_read_b128 v[206:209], v182 offset:57344
	ds_read_b128 v[228:231], v202 offset:57344
	s_waitcnt lgkmcnt(1)
	v_mfma_f32_32x32x16_bf16 v[80:95], v[206:209], v[128:131], v[80:95]
	s_waitcnt lgkmcnt(0)
	v_mfma_f32_32x32x16_bf16 v[64:79], v[228:231], v[128:131], v[64:79]
	ds_read_b128 v[206:209], v183 offset:57344
	ds_read_b128 v[228:231], v199 offset:57344
	s_waitcnt lgkmcnt(1)
	v_mfma_f32_32x32x16_bf16 v[80:95], v[206:209], v[124:127], v[80:95]
	s_waitcnt lgkmcnt(0)
	v_mfma_f32_32x32x16_bf16 v[64:79], v[228:231], v[124:127], v[64:79]
	ds_read_b128 v[206:209], v184 offset:57344
	ds_read_b128 v[228:231], v200 offset:57344
	s_waitcnt lgkmcnt(1)
	v_mfma_f32_32x32x16_bf16 v[80:95], v[206:209], v[120:123], v[80:95]
	s_waitcnt lgkmcnt(0)
	v_mfma_f32_32x32x16_bf16 v[64:79], v[228:231], v[120:123], v[64:79]
	ds_read_b128 v[206:209], v185 offset:57344
	ds_read_b128 v[228:231], v197 offset:57344
	s_waitcnt lgkmcnt(1)
	v_mfma_f32_32x32x16_bf16 v[80:95], v[206:209], v[116:119], v[80:95]
	s_waitcnt lgkmcnt(0)
	v_mfma_f32_32x32x16_bf16 v[64:79], v[228:231], v[116:119], v[64:79]
	ds_read_b128 v[206:209], v186 offset:57344
	ds_read_b128 v[228:231], v198 offset:57344
	s_waitcnt lgkmcnt(1)
	v_mfma_f32_32x32x16_bf16 v[80:95], v[206:209], v[112:115], v[80:95]
	s_waitcnt lgkmcnt(0)
	v_mfma_f32_32x32x16_bf16 v[64:79], v[228:231], v[112:115], v[64:79]
	ds_read_b128 v[206:209], v187 offset:57344
	ds_read_b128 v[228:231], v194 offset:57344
	s_waitcnt lgkmcnt(1)
	v_mfma_f32_32x32x16_bf16 v[80:95], v[206:209], v[108:111], v[80:95]
	s_waitcnt lgkmcnt(0)
	v_mfma_f32_32x32x16_bf16 v[64:79], v[228:231], v[108:111], v[64:79]
	ds_read_b128 v[206:209], v188 offset:57344
	ds_read_b128 v[228:231], v195 offset:57344
	s_waitcnt lgkmcnt(1)
	v_mfma_f32_32x32x16_bf16 v[80:95], v[206:209], v[104:107], v[80:95]
	s_waitcnt lgkmcnt(0)
	v_mfma_f32_32x32x16_bf16 v[64:79], v[228:231], v[104:107], v[64:79]
	ds_read_b128 v[206:209], v189 offset:57344
	ds_read_b128 v[228:231], v192 offset:57344
	s_waitcnt lgkmcnt(1)
	v_mfma_f32_32x32x16_bf16 v[80:95], v[206:209], v[100:103], v[80:95]
	s_waitcnt lgkmcnt(0)
	v_mfma_f32_32x32x16_bf16 v[64:79], v[228:231], v[100:103], v[64:79]
	ds_read_b128 v[206:209], v190 offset:57344
	ds_read_b128 v[228:231], v193 offset:57344
	s_waitcnt lgkmcnt(1)
	v_mfma_f32_32x32x16_bf16 v[80:95], v[206:209], v[96:99], v[80:95]
	v_exp_f32_e32 v208, v160
	v_exp_f32_e32 v209, v161
	v_cvt_pk_bf16_f32 v160, v210, v212
	v_cvt_pk_bf16_f32 v161, v213, v217
	v_add_f32_e32 v156, v208, v156
	v_add_f32_e32 v156, v209, v156
	v_add_f32_e32 v156, v216, v156
	v_add_f32_e32 v156, v227, v156
	s_waitcnt lgkmcnt(0)
	v_mfma_f32_32x32x16_bf16 v[64:79], v[228:231], v[96:99], v[64:79]
	v_exp_f32_e32 v228, v166
	v_add_f32_e32 v156, v154, v156
	v_exp_f32_e32 v229, v167
	v_add_f32_e32 v156, v155, v156
	v_exp_f32_e32 v230, v164
	v_add_f32_e32 v156, v152, v156
	v_exp_f32_e32 v231, v165
	v_add_f32_e32 v156, v153, v156
	v_add_f32_e32 v156, v228, v156
	v_add_f32_e32 v156, v229, v156
	v_add_f32_e32 v156, v230, v156
	v_add_f32_e32 v156, v231, v156
	v_add_f32_e32 v156, v232, v156
	v_add_f32_e32 v206, v233, v156
	v_mov_b32_e32 v207, v206
	v_cvt_pk_bf16_f32 v156, v219, v220
	v_cvt_pk_bf16_f32 v165, v208, v209
	v_cvt_pk_bf16_f32 v209, v228, v229
	v_permlane32_swap_b32_e32 v206, v207
	v_cvt_pk_bf16_f32 v164, v168, v169
	v_cvt_pk_bf16_f32 v166, v216, v227
	v_cvt_pk_bf16_f32 v167, v154, v155
	v_cvt_pk_bf16_f32 v208, v152, v153
	v_cvt_pk_bf16_f32 v210, v230, v231
	v_lshl_add_u64 v[152:153], s[22:23], 0, v[148:149]
	v_add_co_u32_e32 v154, vcc, s61, v152
	s_nop 1
	v_addc_co_u32_e32 v155, vcc, 0, v153, vcc
	v_add_co_u32_e32 v168, vcc, s62, v152
	s_nop 1
	v_addc_co_u32_e32 v169, vcc, 0, v153, vcc
	global_load_dwordx4 v[212:215], v[154:155], off offset:768
	global_load_dwordx4 v[218:221], v[154:155], off offset:512
	global_load_dwordx4 v[222:225], v[168:169], off offset:768
	global_load_dwordx4 v[226:229], v[168:169], off offset:512
	v_lshl_add_u64 v[154:155], s[22:23], 0, v[150:151]
	v_add_co_u32_e32 v168, vcc, s63, v154
	s_nop 1
	v_addc_co_u32_e32 v169, vcc, 0, v155, vcc
	global_load_dwordx4 v[230:233], v[168:169], off offset:512
	ds_read_b64_tr_b16 v[234:235], v174 offset:0x0
	ds_read_b64_tr_b16 v[236:237], v174 offset:0x100
	ds_read_b64_tr_b16 v[238:239], v174 offset:0x1000
	ds_read_b64_tr_b16 v[240:241], v174 offset:0x1100
	ds_read_b64_tr_b16 v[242:243], v174 offset:0x2000
	ds_read_b64_tr_b16 v[244:245], v174 offset:0x2100
	ds_read_b64_tr_b16 v[246:247], v174 offset:0x3000
	ds_read_b64_tr_b16 v[248:249], v174 offset:0x3100
	s_waitcnt lgkmcnt(0)
	s_nop 0
	v_mfma_f32_32x32x16_bf16 v[0:15], v[156:159], v[234:237], v[0:15]
	ds_read_b64_tr_b16 v[234:235], v174 offset:0x200
	ds_read_b64_tr_b16 v[236:237], v174 offset:0x300
	v_mfma_f32_32x32x16_bf16 v[0:15], v[160:163], v[238:241], v[0:15]
	ds_read_b64_tr_b16 v[238:239], v174 offset:0x1200
	ds_read_b64_tr_b16 v[240:241], v174 offset:0x1300
	v_mfma_f32_32x32x16_bf16 v[0:15], v[164:167], v[242:245], v[0:15]
	ds_read_b64_tr_b16 v[242:243], v174 offset:0x2200
	ds_read_b64_tr_b16 v[244:245], v174 offset:0x2300
	ds_read_b64_tr_b16 v[250:251], v174 offset:0x3200
	ds_read_b64_tr_b16 v[252:253], v174 offset:0x3300
	s_waitcnt lgkmcnt(0)
	v_mfma_f32_32x32x16_bf16 v[0:15], v[208:211], v[246:249], v[0:15]
	v_mfma_f32_32x32x16_bf16 v[48:63], v[156:159], v[234:237], v[48:63]
	ds_read_b64_tr_b16 v[234:235], v174 offset:0x400
	ds_read_b64_tr_b16 v[236:237], v174 offset:0x500
	v_mfma_f32_32x32x16_bf16 v[48:63], v[160:163], v[238:241], v[48:63]
	ds_read_b64_tr_b16 v[238:239], v174 offset:0x1400
	ds_read_b64_tr_b16 v[240:241], v174 offset:0x1500
	v_mfma_f32_32x32x16_bf16 v[48:63], v[164:167], v[242:245], v[48:63]
	ds_read_b64_tr_b16 v[242:243], v174 offset:0x2400
	ds_read_b64_tr_b16 v[244:245], v174 offset:0x2500
	ds_read_b64_tr_b16 v[246:247], v174 offset:0x3400
	ds_read_b64_tr_b16 v[248:249], v174 offset:0x3500
	s_waitcnt lgkmcnt(0)
	v_mfma_f32_32x32x16_bf16 v[48:63], v[208:211], v[250:253], v[48:63]
	v_mfma_f32_32x32x16_bf16 v[16:31], v[156:159], v[234:237], v[16:31]
	ds_read_b64_tr_b16 v[234:235], v174 offset:0x600
	ds_read_b64_tr_b16 v[236:237], v174 offset:0x700
	v_mfma_f32_32x32x16_bf16 v[16:31], v[160:163], v[238:241], v[16:31]
	ds_read_b64_tr_b16 v[238:239], v174 offset:0x1600
	ds_read_b64_tr_b16 v[240:241], v174 offset:0x1700
	v_mfma_f32_32x32x16_bf16 v[16:31], v[164:167], v[242:245], v[16:31]
	ds_read_b64_tr_b16 v[242:243], v174 offset:0x2600
	ds_read_b64_tr_b16 v[244:245], v174 offset:0x2700
	ds_read_b64_tr_b16 v[250:251], v174 offset:0x3600
	ds_read_b64_tr_b16 v[252:253], v174 offset:0x3700
	s_waitcnt lgkmcnt(0)
	v_mfma_f32_32x32x16_bf16 v[16:31], v[208:211], v[246:249], v[16:31]
	v_mfma_f32_32x32x16_bf16 v[32:47], v[156:159], v[234:237], v[32:47]
	v_max_f32_e32 v168, v81, v81
	v_max_f32_e32 v169, v80, v80
	v_max_f32_e32 v168, v169, v168
	v_max3_f32 v168, v168, v82, v83
	v_max3_f32 v168, v168, v84, v85
	v_max3_f32 v156, v168, v86, v87
	v_max3_f32 v156, v156, v88, v89
	v_max3_f32 v156, v156, v90, v91
	v_mfma_f32_32x32x16_bf16 v[32:47], v[160:163], v[238:241], v[32:47]
	v_max3_f32 v156, v156, v92, v93
	v_max3_f32 v156, v156, v94, v95
	v_max3_f32 v156, v156, v64, v65
	v_max3_f32 v156, v156, v66, v67
	v_max3_f32 v156, v156, v68, v69
	v_max3_f32 v156, v156, v70, v71
	v_max3_f32 v156, v156, v72, v73
	v_max3_f32 v156, v156, v74, v75
	v_mfma_f32_32x32x16_bf16 v[32:47], v[164:167], v[242:245], v[32:47]
	v_max3_f32 v156, v156, v76, v77
	v_max3_f32 v156, v156, v78, v79
	v_mov_b32_e32 v157, v156
	s_nop 1
	v_permlane32_swap_b32_e32 v156, v157
	v_max_f32_e32 v157, v157, v157
	v_max_f32_e32 v156, v156, v156
	v_max_f32_e32 v156, v156, v157
	v_max_f32_e32 v158, v205, v205
	v_sub_f32_e32 v157, v156, v205
	v_max_f32_e32 v156, v158, v156
	v_mfma_f32_32x32x16_bf16 v[32:47], v[208:211], v[250:253], v[32:47]
	v_sub_f32_e32 v158, v205, v156
	v_mul_f32_e32 v158, 0x3dd53b94, v158
	v_exp_f32_e32 v158, v158
	v_cmp_ge_f32_e32 vcc, s58, v157
	s_cmp_eq_u64 vcc, exec
	s_cselect_b64 s[4:5], -1, 0
	s_barrier
	s_waitcnt vmcnt(0)
	v_cndmask_b32_e64 v209, v158, 1.0, s[4:5]
	v_cmp_gt_f32_e32 vcc, 1.0, v209
	s_waitcnt vmcnt(4)
	ds_write_b128 v175, v[212:215]
	s_waitcnt vmcnt(2)
	ds_write_b128 v176, v[222:225]
	ds_write_b128 v177, v[218:221] offset:32768
	s_waitcnt vmcnt(1)
	ds_write_b128 v177, v[226:229] offset:45056
	s_waitcnt vmcnt(0)
	ds_write_b128 v178, v[230:233] offset:32768
	s_cbranch_vccz .LBB0_950
	s_and_saveexec_b64 s[28:29], s[2:3]
	ds_write_b32 v147, v209 offset:128
	s_or_b64 exec, exec, s[28:29]
	s_waitcnt lgkmcnt(0)
	v_add_u32_e32 v157, s35, v144
	ds_read_b128 v[158:161], v157 offset:224
	ds_read_b128 v[162:165], v157 offset:192
	ds_read_b128 v[210:213], v157 offset:160
	ds_read_b128 v[218:221], v157 offset:128
	s_waitcnt lgkmcnt(3)
	v_pk_mul_f32 v[12:13], v[12:13], v[158:159]
	s_waitcnt lgkmcnt(2)
	v_pk_mul_f32 v[8:9], v[8:9], v[162:163]
	s_waitcnt lgkmcnt(1)
	v_pk_mul_f32 v[4:5], v[4:5], v[210:211]
	v_pk_mul_f32 v[14:15], v[14:15], v[160:161]
	v_pk_mul_f32 v[10:11], v[10:11], v[164:165]
	v_pk_mul_f32 v[6:7], v[6:7], v[212:213]
	s_waitcnt lgkmcnt(0)
	v_pk_mul_f32 v[2:3], v[2:3], v[220:221]
	v_pk_mul_f32 v[0:1], v[0:1], v[218:219]
	v_pk_mul_f32 v[60:61], v[60:61], v[158:159]
	v_pk_mul_f32 v[56:57], v[56:57], v[162:163]
	v_pk_mul_f32 v[52:53], v[52:53], v[210:211]
	v_pk_mul_f32 v[62:63], v[62:63], v[160:161]
	v_pk_mul_f32 v[58:59], v[58:59], v[164:165]
	v_pk_mul_f32 v[54:55], v[54:55], v[212:213]
	v_pk_mul_f32 v[50:51], v[50:51], v[220:221]
	v_pk_mul_f32 v[48:49], v[48:49], v[218:219]
	v_pk_mul_f32 v[28:29], v[28:29], v[158:159]
	v_pk_mul_f32 v[24:25], v[24:25], v[162:163]
	v_pk_mul_f32 v[20:21], v[20:21], v[210:211]
	v_pk_mul_f32 v[30:31], v[30:31], v[160:161]
	v_pk_mul_f32 v[26:27], v[26:27], v[164:165]
	v_pk_mul_f32 v[22:23], v[22:23], v[212:213]
	v_pk_mul_f32 v[18:19], v[18:19], v[220:221]
	v_pk_mul_f32 v[16:17], v[16:17], v[218:219]
	v_pk_mul_f32 v[44:45], v[44:45], v[158:159]
	v_pk_mul_f32 v[40:41], v[40:41], v[162:163]
	v_pk_mul_f32 v[36:37], v[36:37], v[210:211]
	v_pk_mul_f32 v[46:47], v[46:47], v[160:161]
	v_pk_mul_f32 v[42:43], v[42:43], v[164:165]
	v_pk_mul_f32 v[38:39], v[38:39], v[212:213]
	v_pk_mul_f32 v[34:35], v[34:35], v[220:221]
	v_pk_mul_f32 v[32:33], v[32:33], v[218:219]
.LBB0_950:
	v_cndmask_b32_e64 v156, v156, v205, s[4:5]
	v_mul_f32_e32 v213, 0xbdd53b94, v156
	v_fmamk_f32 v87, v87, 0x3dd53b94, v213
	v_exp_f32_e32 v208, v87
	v_fmamk_f32 v80, v80, 0x3dd53b94, v213
	v_fmamk_f32 v81, v81, 0x3dd53b94, v213
	v_fmamk_f32 v82, v82, 0x3dd53b94, v213
	v_fmamk_f32 v83, v83, 0x3dd53b94, v213
	v_fmamk_f32 v84, v84, 0x3dd53b94, v213
	v_fmamk_f32 v85, v85, 0x3dd53b94, v213
	v_fmamk_f32 v86, v86, 0x3dd53b94, v213
	v_fmamk_f32 v88, v88, 0x3dd53b94, v213
	v_fmamk_f32 v89, v89, 0x3dd53b94, v213
	v_fmamk_f32 v90, v90, 0x3dd53b94, v213
	v_fmamk_f32 v91, v91, 0x3dd53b94, v213
	v_fmamk_f32 v92, v92, 0x3dd53b94, v213
	v_fmamk_f32 v93, v93, 0x3dd53b94, v213
	v_fmamk_f32 v94, v94, 0x3dd53b94, v213
	v_fmamk_f32 v95, v95, 0x3dd53b94, v213
	v_fmamk_f32 v227, v68, 0x3dd53b94, v213
	v_fmamk_f32 v228, v77, 0x3dd53b94, v213
	v_fmamk_f32 v223, v64, 0x3dd53b94, v213
	v_fmamk_f32 v224, v65, 0x3dd53b94, v213
	v_fmamk_f32 v225, v66, 0x3dd53b94, v213
	v_fmamk_f32 v226, v67, 0x3dd53b94, v213
	v_fmamk_f32 v215, v69, 0x3dd53b94, v213
	v_fmamk_f32 v217, v70, 0x3dd53b94, v213
	v_fmamk_f32 v218, v71, 0x3dd53b94, v213
	v_fmamk_f32 v219, v72, 0x3dd53b94, v213
	v_fmamk_f32 v220, v73, 0x3dd53b94, v213
	v_fmamk_f32 v221, v74, 0x3dd53b94, v213
	v_fmamk_f32 v222, v75, 0x3dd53b94, v213
	v_fmamk_f32 v214, v76, 0x3dd53b94, v213
	v_exp_f32_e32 v165, v80
	v_exp_f32_e32 v167, v81
	v_exp_f32_e32 v205, v82
	v_exp_f32_e32 v210, v83
	v_exp_f32_e32 v211, v84
	v_exp_f32_e32 v212, v85
	v_exp_f32_e32 v166, v86
	v_exp_f32_e32 v158, v88
	v_exp_f32_e32 v161, v89
	v_exp_f32_e32 v162, v90
	v_exp_f32_e32 v164, v91
	v_exp_f32_e32 v157, v92
	v_exp_f32_e32 v159, v93
	v_exp_f32_e32 v160, v94
	v_exp_f32_e32 v163, v95
	v_fmamk_f32 v229, v78, 0x3dd53b94, v213
	v_fmac_f32_e32 v213, 0x3dd53b94, v79
	s_waitcnt lgkmcnt(0)
	s_barrier
	ds_read_b128 v[64:67], v179 offset:32768
	ds_read_b128 v[68:71], v179 offset:45056
	ds_read_b128 v[230:233], v180 offset:32768
	ds_read_b128 v[234:237], v180 offset:45056
	v_exp_f32_e32 v168, v223
	v_exp_f32_e32 v169, v224
	s_waitcnt lgkmcnt(3)
	v_mfma_f32_32x32x16_bf16 v[80:95], v[64:67], v[140:143], 0
	v_exp_f32_e32 v216, v225
	v_exp_f32_e32 v223, v226
	v_exp_f32_e32 v224, v227
	v_exp_f32_e32 v215, v215
	v_exp_f32_e32 v217, v217
	v_exp_f32_e32 v225, v218
	v_exp_f32_e32 v226, v219
	s_waitcnt lgkmcnt(2)
	v_mfma_f32_32x32x16_bf16 v[64:79], v[68:71], v[140:143], 0
	v_exp_f32_e32 v222, v222
	v_exp_f32_e32 v214, v214
	v_exp_f32_e32 v229, v229
	v_cvt_pk_bf16_f32 v218, v165, v167
	v_cvt_pk_bf16_f32 v219, v205, v210
	s_waitcnt lgkmcnt(1)
	v_mfma_f32_32x32x16_bf16 v[80:95], v[230:233], v[136:139], v[80:95]
	s_waitcnt lgkmcnt(0)
	v_mfma_f32_32x32x16_bf16 v[64:79], v[234:237], v[136:139], v[64:79]
	ds_read_b128 v[230:233], v181 offset:32768
	ds_read_b128 v[234:237], v181 offset:45056
	s_waitcnt lgkmcnt(1)
	v_mfma_f32_32x32x16_bf16 v[80:95], v[230:233], v[132:135], v[80:95]
	s_waitcnt lgkmcnt(0)
	v_mfma_f32_32x32x16_bf16 v[64:79], v[234:237], v[132:135], v[64:79]
	ds_read_b128 v[230:233], v182 offset:32768
	ds_read_b128 v[234:237], v182 offset:45056
	s_waitcnt lgkmcnt(1)
	v_mfma_f32_32x32x16_bf16 v[80:95], v[230:233], v[128:131], v[80:95]
	s_waitcnt lgkmcnt(0)
	v_mfma_f32_32x32x16_bf16 v[64:79], v[234:237], v[128:131], v[64:79]
	ds_read_b128 v[230:233], v183 offset:32768
	ds_read_b128 v[234:237], v183 offset:45056
	s_waitcnt lgkmcnt(1)
	v_mfma_f32_32x32x16_bf16 v[80:95], v[230:233], v[124:127], v[80:95]
	s_waitcnt lgkmcnt(0)
	v_mfma_f32_32x32x16_bf16 v[64:79], v[234:237], v[124:127], v[64:79]
	ds_read_b128 v[230:233], v184 offset:32768
	ds_read_b128 v[234:237], v184 offset:45056
	s_waitcnt lgkmcnt(1)
	v_mfma_f32_32x32x16_bf16 v[80:95], v[230:233], v[120:123], v[80:95]
	s_waitcnt lgkmcnt(0)
	v_mfma_f32_32x32x16_bf16 v[64:79], v[234:237], v[120:123], v[64:79]
	ds_read_b128 v[230:233], v185 offset:32768
	ds_read_b128 v[234:237], v185 offset:45056
	s_waitcnt lgkmcnt(1)
	v_mfma_f32_32x32x16_bf16 v[80:95], v[230:233], v[116:119], v[80:95]
	s_waitcnt lgkmcnt(0)
	v_mfma_f32_32x32x16_bf16 v[64:79], v[234:237], v[116:119], v[64:79]
	ds_read_b128 v[230:233], v186 offset:32768
	ds_read_b128 v[234:237], v186 offset:45056
	s_waitcnt lgkmcnt(1)
	v_mfma_f32_32x32x16_bf16 v[80:95], v[230:233], v[112:115], v[80:95]
	s_waitcnt lgkmcnt(0)
	v_mfma_f32_32x32x16_bf16 v[64:79], v[234:237], v[112:115], v[64:79]
	ds_read_b128 v[230:233], v187 offset:32768
	ds_read_b128 v[234:237], v187 offset:45056
	s_waitcnt lgkmcnt(1)
	v_mfma_f32_32x32x16_bf16 v[80:95], v[230:233], v[108:111], v[80:95]
	s_waitcnt lgkmcnt(0)
	v_mfma_f32_32x32x16_bf16 v[64:79], v[234:237], v[108:111], v[64:79]
	ds_read_b128 v[230:233], v188 offset:32768
	ds_read_b128 v[234:237], v188 offset:45056
	s_waitcnt lgkmcnt(1)
	v_mfma_f32_32x32x16_bf16 v[80:95], v[230:233], v[104:107], v[80:95]
	s_waitcnt lgkmcnt(0)
	v_mfma_f32_32x32x16_bf16 v[64:79], v[234:237], v[104:107], v[64:79]
	ds_read_b128 v[230:233], v189 offset:32768
	ds_read_b128 v[234:237], v189 offset:45056
	s_waitcnt lgkmcnt(1)
	v_mfma_f32_32x32x16_bf16 v[80:95], v[230:233], v[100:103], v[80:95]
	s_waitcnt lgkmcnt(0)
	v_mfma_f32_32x32x16_bf16 v[64:79], v[234:237], v[100:103], v[64:79]
	ds_read_b128 v[230:233], v190 offset:32768
	ds_read_b128 v[234:237], v190 offset:45056
	s_waitcnt lgkmcnt(1)
	v_mfma_f32_32x32x16_bf16 v[80:95], v[230:233], v[96:99], v[80:95]
	v_exp_f32_e32 v233, v213
	v_add_f32_e32 v213, 0, v165
	v_add_f32_e32 v213, v167, v213
	v_add_f32_e32 v213, v205, v213
	v_add_f32_e32 v213, v210, v213
	v_add_f32_e32 v213, v211, v213
	v_add_f32_e32 v213, v212, v213
	v_add_f32_e32 v213, v166, v213
	v_add_f32_e32 v213, v208, v213
	v_add_f32_e32 v213, v158, v213
	v_add_f32_e32 v213, v161, v213
	v_add_f32_e32 v213, v162, v213
	v_add_f32_e32 v213, v164, v213
	v_add_f32_e32 v213, v157, v213
	v_add_f32_e32 v213, v159, v213
	v_add_f32_e32 v213, v160, v213
	v_add_f32_e32 v213, v163, v213
	v_add_f32_e32 v213, v168, v213
	v_add_f32_e32 v213, v169, v213
	v_add_f32_e32 v213, v216, v213
	v_add_f32_e32 v213, v223, v213
	v_add_f32_e32 v213, v224, v213
	v_exp_f32_e32 v230, v220
	v_add_f32_e32 v213, v215, v213
	v_exp_f32_e32 v231, v221
	v_add_f32_e32 v213, v217, v213
	v_add_f32_e32 v213, v225, v213
	v_add_f32_e32 v213, v226, v213
	v_exp_f32_e32 v232, v228
	v_add_f32_e32 v213, v230, v213
	s_waitcnt lgkmcnt(0)
	v_mfma_f32_32x32x16_bf16 v[64:79], v[234:237], v[96:99], v[64:79]
	v_add_f32_e32 v213, v231, v213
	v_add_f32_e32 v213, v222, v213
	v_add_f32_e32 v213, v214, v213
	v_add_f32_e32 v213, v232, v213
	v_add_f32_e32 v213, v229, v213
	v_add_f32_e32 v227, v233, v213
	v_mov_b32_e32 v228, v227
	s_nop 1
	v_permlane32_swap_b32_e32 v227, v228
	v_cvt_pk_bf16_f32 v220, v211, v212
	v_cvt_pk_bf16_f32 v221, v166, v208
	v_cvt_pk_bf16_f32 v210, v158, v161
	v_cvt_pk_bf16_f32 v211, v162, v164
	v_cvt_pk_bf16_f32 v212, v157, v159
	v_cvt_pk_bf16_f32 v213, v160, v163
	v_cvt_pk_bf16_f32 v158, v168, v169
	v_cvt_pk_bf16_f32 v159, v216, v223
	v_cvt_pk_bf16_f32 v160, v224, v215
	v_cvt_pk_bf16_f32 v161, v217, v225
	v_cvt_pk_bf16_f32 v162, v226, v230
	v_cvt_pk_bf16_f32 v163, v231, v222
	v_cvt_pk_bf16_f32 v164, v214, v232
	v_cvt_pk_bf16_f32 v165, v229, v233
	v_add_co_u32_e32 v166, vcc, s64, v152
	s_nop 1
	v_addc_co_u32_e32 v167, vcc, 0, v153, vcc
	v_add_co_u32_e32 v152, vcc, s65, v152
	s_nop 1
	v_addc_co_u32_e32 v153, vcc, 0, v153, vcc
	global_load_dwordx4 v[222:225], v[166:167], off offset:768
	global_load_dwordx4 v[230:233], v[166:167], off offset:512
	global_load_dwordx4 v[234:237], v[152:153], off offset:768
	global_load_dwordx4 v[238:241], v[152:153], off offset:512
	v_add_co_u32_e32 v152, vcc, s66, v154
	s_nop 1
	v_addc_co_u32_e32 v153, vcc, 0, v155, vcc
	global_load_dwordx4 v[242:245], v[152:153], off offset:512
	ds_read_b64_tr_b16 v[152:153], v173 offset:0x0
	ds_read_b64_tr_b16 v[154:155], v173 offset:0x100
	ds_read_b64_tr_b16 v[246:247], v173 offset:0x1000
	ds_read_b64_tr_b16 v[248:249], v173 offset:0x1100
	ds_read_b64_tr_b16 v[250:251], v173 offset:0x2000
	ds_read_b64_tr_b16 v[252:253], v173 offset:0x2100
	ds_read_b64_tr_b16 v[166:167], v173 offset:0x3000
	ds_read_b64_tr_b16 v[168:169], v173 offset:0x3100
	s_waitcnt lgkmcnt(0)
	s_nop 0
	v_mfma_f32_32x32x16_bf16 v[0:15], v[218:221], v[152:155], v[0:15]
	ds_read_b64_tr_b16 v[152:153], v173 offset:0x200
	ds_read_b64_tr_b16 v[154:155], v173 offset:0x300
	v_mfma_f32_32x32x16_bf16 v[0:15], v[210:213], v[246:249], v[0:15]
	ds_read_b64_tr_b16 v[246:247], v173 offset:0x1200
	ds_read_b64_tr_b16 v[248:249], v173 offset:0x1300
	v_mfma_f32_32x32x16_bf16 v[0:15], v[158:161], v[250:253], v[0:15]
	ds_read_b64_tr_b16 v[250:251], v173 offset:0x2200
	ds_read_b64_tr_b16 v[252:253], v173 offset:0x2300
	ds_read_b64_tr_b16 v[214:215], v173 offset:0x3200
	ds_read_b64_tr_b16 v[216:217], v173 offset:0x3300
	s_waitcnt lgkmcnt(0)
	v_mfma_f32_32x32x16_bf16 v[0:15], v[162:165], v[166:169], v[0:15]
	v_mfma_f32_32x32x16_bf16 v[48:63], v[218:221], v[152:155], v[48:63]
	ds_read_b64_tr_b16 v[152:153], v173 offset:0x400
	ds_read_b64_tr_b16 v[154:155], v173 offset:0x500
	ds_read_b64_tr_b16 v[166:167], v173 offset:0x1400
	ds_read_b64_tr_b16 v[168:169], v173 offset:0x1500
	v_mfma_f32_32x32x16_bf16 v[48:63], v[210:213], v[246:249], v[48:63]
	ds_read_b64_tr_b16 v[246:247], v173 offset:0x2400
	ds_read_b64_tr_b16 v[248:249], v173 offset:0x2500
	v_mfma_f32_32x32x16_bf16 v[48:63], v[158:161], v[250:253], v[48:63]
	ds_read_b64_tr_b16 v[250:251], v173 offset:0x3400
	ds_read_b64_tr_b16 v[252:253], v173 offset:0x3500
	s_waitcnt lgkmcnt(0)
	v_mfma_f32_32x32x16_bf16 v[48:63], v[162:165], v[214:217], v[48:63]
	v_mfma_f32_32x32x16_bf16 v[16:31], v[218:221], v[152:155], v[16:31]
	ds_read_b64_tr_b16 v[152:153], v173 offset:0x600
	ds_read_b64_tr_b16 v[154:155], v173 offset:0x700
	v_mfma_f32_32x32x16_bf16 v[16:31], v[210:213], v[166:169], v[16:31]
	ds_read_b64_tr_b16 v[166:167], v173 offset:0x1600
	ds_read_b64_tr_b16 v[168:169], v173 offset:0x1700
	ds_read_b64_tr_b16 v[214:215], v173 offset:0x2600
	ds_read_b64_tr_b16 v[216:217], v173 offset:0x2700
	v_mfma_f32_32x32x16_bf16 v[16:31], v[158:161], v[246:249], v[16:31]
	ds_read_b64_tr_b16 v[246:247], v173 offset:0x3600
	ds_read_b64_tr_b16 v[248:249], v173 offset:0x3700
	s_waitcnt lgkmcnt(0)
	v_mfma_f32_32x32x16_bf16 v[16:31], v[162:165], v[250:253], v[16:31]
	v_mfma_f32_32x32x16_bf16 v[32:47], v[218:221], v[152:155], v[32:47]
	v_max_f32_e32 v157, v81, v81
	v_max_f32_e32 v205, v80, v80
	v_max_f32_e32 v157, v205, v157
	v_max3_f32 v157, v157, v82, v83
	v_max3_f32 v157, v157, v84, v85
	v_max3_f32 v152, v157, v86, v87
	v_max3_f32 v152, v152, v88, v89
	v_max3_f32 v152, v152, v90, v91
	v_mfma_f32_32x32x16_bf16 v[32:47], v[210:213], v[166:169], v[32:47]
	v_max3_f32 v152, v152, v92, v93
	v_max3_f32 v152, v152, v94, v95
	v_max3_f32 v152, v152, v64, v65
	v_max3_f32 v152, v152, v66, v67
	v_max3_f32 v152, v152, v68, v69
	v_max3_f32 v152, v152, v70, v71
	v_max3_f32 v152, v152, v72, v73
	v_max3_f32 v152, v152, v74, v75
	v_mfma_f32_32x32x16_bf16 v[32:47], v[158:161], v[214:217], v[32:47]
	v_max3_f32 v152, v152, v76, v77
	v_max3_f32 v152, v152, v78, v79
	v_mov_b32_e32 v153, v152
	s_nop 1
	v_permlane32_swap_b32_e32 v152, v153
	v_max_f32_e32 v153, v153, v153
	v_max_f32_e32 v152, v152, v152
	v_max_f32_e32 v152, v152, v153
	v_max_f32_e32 v154, v156, v156
	v_sub_f32_e32 v153, v152, v156
	v_max_f32_e32 v152, v154, v152
	v_mfma_f32_32x32x16_bf16 v[32:47], v[162:165], v[246:249], v[32:47]
	v_sub_f32_e32 v154, v156, v152
	v_mul_f32_e32 v154, 0x3dd53b94, v154
	v_exp_f32_e32 v154, v154
	v_cmp_ge_f32_e32 vcc, s58, v153
	s_cmp_eq_u64 vcc, exec
	s_cselect_b64 s[4:5], -1, 0
	s_barrier
	s_waitcnt vmcnt(0)
	v_cndmask_b32_e64 v208, v154, 1.0, s[4:5]
	v_cmp_gt_f32_e32 vcc, 1.0, v208
	s_waitcnt vmcnt(4)
	ds_write_b128 v175, v[222:225] offset:16384
	s_waitcnt vmcnt(2)
	ds_write_b128 v176, v[234:237] offset:16384
	ds_write_b128 v177, v[230:233] offset:57344
	s_waitcnt vmcnt(1)
	ds_write_b128 v191, v[238:241] offset:57344
	s_waitcnt vmcnt(0)
	ds_write_b128 v178, v[242:245] offset:57344
	s_cbranch_vccz .LBB0_954
	s_and_saveexec_b64 s[28:29], s[2:3]
	ds_write_b32 v147, v208 offset:128
	s_or_b64 exec, exec, s[28:29]
	s_waitcnt lgkmcnt(0)
	v_add_u32_e32 v153, s35, v144
	ds_read_b128 v[158:161], v153 offset:224
	ds_read_b128 v[162:165], v153 offset:192
	ds_read_b128 v[166:169], v153 offset:160
	ds_read_b128 v[210:213], v153 offset:128
	s_waitcnt lgkmcnt(3)
	v_pk_mul_f32 v[12:13], v[12:13], v[158:159]
	s_waitcnt lgkmcnt(2)
	v_pk_mul_f32 v[8:9], v[8:9], v[162:163]
	s_waitcnt lgkmcnt(1)
	v_pk_mul_f32 v[4:5], v[4:5], v[166:167]
	v_pk_mul_f32 v[14:15], v[14:15], v[160:161]
	v_pk_mul_f32 v[10:11], v[10:11], v[164:165]
	v_pk_mul_f32 v[6:7], v[6:7], v[168:169]
	s_waitcnt lgkmcnt(0)
	v_pk_mul_f32 v[2:3], v[2:3], v[212:213]
	v_pk_mul_f32 v[0:1], v[0:1], v[210:211]
	v_pk_mul_f32 v[60:61], v[60:61], v[158:159]
	v_pk_mul_f32 v[56:57], v[56:57], v[162:163]
	v_pk_mul_f32 v[52:53], v[52:53], v[166:167]
	v_pk_mul_f32 v[62:63], v[62:63], v[160:161]
	v_pk_mul_f32 v[58:59], v[58:59], v[164:165]
	v_pk_mul_f32 v[54:55], v[54:55], v[168:169]
	v_pk_mul_f32 v[50:51], v[50:51], v[212:213]
	v_pk_mul_f32 v[48:49], v[48:49], v[210:211]
	v_pk_mul_f32 v[28:29], v[28:29], v[158:159]
	v_pk_mul_f32 v[24:25], v[24:25], v[162:163]
	v_pk_mul_f32 v[20:21], v[20:21], v[166:167]
	v_pk_mul_f32 v[30:31], v[30:31], v[160:161]
	v_pk_mul_f32 v[26:27], v[26:27], v[164:165]
	v_pk_mul_f32 v[22:23], v[22:23], v[168:169]
	v_pk_mul_f32 v[18:19], v[18:19], v[212:213]
	v_pk_mul_f32 v[16:17], v[16:17], v[210:211]
	v_pk_mul_f32 v[44:45], v[44:45], v[158:159]
	v_pk_mul_f32 v[40:41], v[40:41], v[162:163]
	v_pk_mul_f32 v[36:37], v[36:37], v[166:167]
	v_pk_mul_f32 v[46:47], v[46:47], v[160:161]
	v_pk_mul_f32 v[42:43], v[42:43], v[164:165]
	v_pk_mul_f32 v[38:39], v[38:39], v[168:169]
	v_pk_mul_f32 v[34:35], v[34:35], v[212:213]
	v_pk_mul_f32 v[32:33], v[32:33], v[210:211]

.LBB0_956:
	ds_read_b128 v[64:67], v179 offset:57344
	ds_read_b128 v[148:151], v180 offset:57344
	v_exp_f32_e32 v162, v162
	v_exp_f32_e32 v163, v163
	v_exp_f32_e32 v160, v160
	s_waitcnt lgkmcnt(1)
	v_mfma_f32_32x32x16_bf16 v[80:95], v[64:67], v[140:143], 0
	ds_read_b128 v[64:67], v203 offset:57344
	ds_read_b128 v[176:179], v204 offset:57344
	v_exp_f32_e32 v161, v161
	v_exp_f32_e32 v156, v156
	s_waitcnt lgkmcnt(1)
	v_mfma_f32_32x32x16_bf16 v[64:79], v[64:67], v[140:143], 0
	v_mfma_f32_32x32x16_bf16 v[80:95], v[148:151], v[136:139], v[80:95]
	s_waitcnt lgkmcnt(0)
	v_mfma_f32_32x32x16_bf16 v[64:79], v[176:179], v[136:139], v[64:79]
	ds_read_b128 v[136:139], v181 offset:57344
	ds_read_b128 v[140:143], v182 offset:57344
	s_waitcnt lgkmcnt(1)
	v_mfma_f32_32x32x16_bf16 v[80:95], v[136:139], v[132:135], v[80:95]
	ds_read_b128 v[136:139], v201 offset:57344
	ds_read_b128 v[148:151], v202 offset:57344
	s_waitcnt lgkmcnt(1)
	v_mfma_f32_32x32x16_bf16 v[64:79], v[136:139], v[132:135], v[64:79]
	v_mfma_f32_32x32x16_bf16 v[80:95], v[140:143], v[128:131], v[80:95]
	s_waitcnt lgkmcnt(0)
	v_mfma_f32_32x32x16_bf16 v[64:79], v[148:151], v[128:131], v[64:79]
	ds_read_b128 v[128:131], v183 offset:57344
	ds_read_b128 v[132:135], v184 offset:57344
	s_waitcnt lgkmcnt(1)
	v_mfma_f32_32x32x16_bf16 v[80:95], v[128:131], v[124:127], v[80:95]
	ds_read_b128 v[128:131], v199 offset:57344
	ds_read_b128 v[136:139], v200 offset:57344
	s_waitcnt lgkmcnt(1)
	v_mfma_f32_32x32x16_bf16 v[64:79], v[128:131], v[124:127], v[64:79]
	ds_read_b128 v[124:127], v185 offset:57344
	ds_read_b128 v[128:131], v186 offset:57344
	v_mfma_f32_32x32x16_bf16 v[80:95], v[132:135], v[120:123], v[80:95]
	ds_read_b128 v[132:135], v197 offset:57344
	ds_read_b128 v[140:143], v198 offset:57344
	ds_read_b128 v[148:151], v187 offset:57344
	ds_read_b128 v[176:179], v188 offset:57344
	ds_read_b128 v[180:183], v194 offset:57344
	ds_read_b128 v[184:187], v195 offset:57344
	ds_read_b128 v[194:197], v189 offset:57344
	ds_read_b128 v[188:191], v190 offset:57344
	s_waitcnt lgkmcnt(10)
	v_mfma_f32_32x32x16_bf16 v[64:79], v[136:139], v[120:123], v[64:79]
	ds_read_b128 v[120:123], v192 offset:57344
	ds_read_b128 v[136:139], v193 offset:57344
	s_waitcnt lgkmcnt(11)
	v_mfma_f32_32x32x16_bf16 v[80:95], v[124:127], v[116:119], v[80:95]
	v_exp_f32_e32 v124, v157
	v_exp_f32_e32 v125, v154
	v_exp_f32_e32 v126, v155
	v_exp_f32_e32 v127, v152
	v_exp_f32_e32 v152, v153
	v_exp_f32_e32 v153, v166
	v_exp_f32_e32 v154, v167
	s_waitcnt lgkmcnt(9)
	v_mfma_f32_32x32x16_bf16 v[64:79], v[132:135], v[116:119], v[64:79]
	v_add_f32_e32 v116, 0, v219
	v_add_f32_e32 v116, v220, v116
	v_add_f32_e32 v116, v221, v116
	v_add_f32_e32 v116, v223, v116
	v_add_f32_e32 v116, v224, v116
	v_add_f32_e32 v116, v226, v116
	v_add_f32_e32 v116, v222, v116
	v_mfma_f32_32x32x16_bf16 v[80:95], v[128:131], v[112:115], v[80:95]
	v_add_f32_e32 v116, v225, v116
	v_add_f32_e32 v116, v210, v116
	v_add_f32_e32 v116, v212, v116
	v_exp_f32_e32 v118, v164
	v_exp_f32_e32 v119, v165
	v_exp_f32_e32 v132, v158
	v_exp_f32_e32 v133, v159
	s_waitcnt lgkmcnt(8)
	v_mfma_f32_32x32x16_bf16 v[64:79], v[140:143], v[112:115], v[64:79]
	v_add_f32_e32 v112, v213, v116
	v_add_f32_e32 v112, v217, v112
	v_add_f32_e32 v112, v211, v112
	v_add_f32_e32 v112, v214, v112
	v_add_f32_e32 v112, v215, v112
	v_add_f32_e32 v112, v218, v112
	v_add_f32_e32 v112, v162, v112
	s_waitcnt lgkmcnt(7)
	v_mfma_f32_32x32x16_bf16 v[80:95], v[148:151], v[108:111], v[80:95]
	v_add_f32_e32 v112, v163, v112
	v_add_f32_e32 v112, v160, v112
	v_add_f32_e32 v112, v161, v112
	v_add_f32_e32 v112, v156, v112
	v_add_f32_e32 v112, v124, v112
	v_add_f32_e32 v112, v125, v112
	v_add_f32_e32 v112, v126, v112
	s_waitcnt lgkmcnt(5)
	v_mfma_f32_32x32x16_bf16 v[64:79], v[180:183], v[108:111], v[64:79]
	v_add_f32_e32 v108, v127, v112
	v_add_f32_e32 v108, v152, v108
	v_add_f32_e32 v108, v153, v108
	v_add_f32_e32 v108, v154, v108
	v_add_f32_e32 v108, v118, v108
	v_add_f32_e32 v108, v119, v108
	v_add_f32_e32 v108, v132, v108
	v_mfma_f32_32x32x16_bf16 v[80:95], v[176:179], v[104:107], v[80:95]
	v_add_f32_e32 v108, v133, v108
	v_mov_b32_e32 v109, v108
	s_nop 1
	v_permlane32_swap_b32_e32 v108, v109
	v_cvt_pk_bf16_f32 v110, v219, v220
	v_cvt_pk_bf16_f32 v111, v221, v223
	v_cvt_pk_bf16_f32 v112, v224, v226
	s_waitcnt lgkmcnt(4)
	v_mfma_f32_32x32x16_bf16 v[64:79], v[184:187], v[104:107], v[64:79]
	v_cvt_pk_bf16_f32 v113, v222, v225
	v_cvt_pk_bf16_f32 v104, v210, v212
	v_cvt_pk_bf16_f32 v105, v213, v217
	v_cvt_pk_bf16_f32 v106, v211, v214
	v_cvt_pk_bf16_f32 v107, v215, v218
	v_cvt_pk_bf16_f32 v114, v162, v163
	v_cvt_pk_bf16_f32 v115, v160, v161
	s_waitcnt lgkmcnt(3)
	v_mfma_f32_32x32x16_bf16 v[80:95], v[194:197], v[100:103], v[80:95]
	v_cvt_pk_bf16_f32 v116, v156, v124
	v_cvt_pk_bf16_f32 v117, v125, v126
	s_waitcnt lgkmcnt(1)
	v_mfma_f32_32x32x16_bf16 v[64:79], v[120:123], v[100:103], v[64:79]
	v_cvt_pk_bf16_f32 v100, v127, v152
	v_cvt_pk_bf16_f32 v101, v153, v154
	v_cvt_pk_bf16_f32 v102, v118, v119
	v_cvt_pk_bf16_f32 v103, v132, v133
	v_mfma_f32_32x32x16_bf16 v[80:95], v[188:191], v[96:99], v[80:95]
	s_waitcnt lgkmcnt(0)
	v_mfma_f32_32x32x16_bf16 v[64:79], v[136:139], v[96:99], v[64:79]
	ds_read_b64_tr_b16 v[96:97], v174 offset:0x0
	ds_read_b64_tr_b16 v[98:99], v174 offset:0x100
	ds_read_b64_tr_b16 v[118:119], v174 offset:0x1000
	ds_read_b64_tr_b16 v[120:121], v174 offset:0x1100
	ds_read_b64_tr_b16 v[122:123], v174 offset:0x2000
	ds_read_b64_tr_b16 v[124:125], v174 offset:0x2100
	ds_read_b64_tr_b16 v[126:127], v174 offset:0x3000
	ds_read_b64_tr_b16 v[128:129], v174 offset:0x3100
	s_waitcnt lgkmcnt(0)
	s_nop 0
	v_mfma_f32_32x32x16_bf16 v[0:15], v[110:113], v[96:99], v[0:15]
	ds_read_b64_tr_b16 v[96:97], v174 offset:0x200
	ds_read_b64_tr_b16 v[98:99], v174 offset:0x300
	v_mfma_f32_32x32x16_bf16 v[0:15], v[104:107], v[118:121], v[0:15]
	ds_read_b64_tr_b16 v[118:119], v174 offset:0x1200
	ds_read_b64_tr_b16 v[120:121], v174 offset:0x1300
	v_mfma_f32_32x32x16_bf16 v[0:15], v[114:117], v[122:125], v[0:15]
	ds_read_b64_tr_b16 v[122:123], v174 offset:0x2200
	ds_read_b64_tr_b16 v[124:125], v174 offset:0x2300
	ds_read_b64_tr_b16 v[130:131], v174 offset:0x3200
	ds_read_b64_tr_b16 v[132:133], v174 offset:0x3300
	s_waitcnt lgkmcnt(0)
	v_mfma_f32_32x32x16_bf16 v[0:15], v[100:103], v[126:129], v[0:15]
	v_mfma_f32_32x32x16_bf16 v[48:63], v[110:113], v[96:99], v[48:63]
	ds_read_b64_tr_b16 v[96:97], v174 offset:0x400
	ds_read_b64_tr_b16 v[98:99], v174 offset:0x500
	v_mfma_f32_32x32x16_bf16 v[48:63], v[104:107], v[118:121], v[48:63]
	ds_read_b64_tr_b16 v[118:119], v174 offset:0x1400
	ds_read_b64_tr_b16 v[120:121], v174 offset:0x1500
	v_mfma_f32_32x32x16_bf16 v[48:63], v[114:117], v[122:125], v[48:63]
	ds_read_b64_tr_b16 v[122:123], v174 offset:0x2400
	ds_read_b64_tr_b16 v[124:125], v174 offset:0x2500
	ds_read_b64_tr_b16 v[126:127], v174 offset:0x3400
	ds_read_b64_tr_b16 v[128:129], v174 offset:0x3500
	s_waitcnt lgkmcnt(0)
	v_mfma_f32_32x32x16_bf16 v[48:63], v[100:103], v[130:133], v[48:63]
	v_mfma_f32_32x32x16_bf16 v[16:31], v[110:113], v[96:99], v[16:31]
	ds_read_b64_tr_b16 v[96:97], v174 offset:0x600
	ds_read_b64_tr_b16 v[98:99], v174 offset:0x700
	v_mfma_f32_32x32x16_bf16 v[16:31], v[104:107], v[118:121], v[16:31]
	ds_read_b64_tr_b16 v[118:119], v174 offset:0x1600
	ds_read_b64_tr_b16 v[120:121], v174 offset:0x1700
	v_mfma_f32_32x32x16_bf16 v[16:31], v[114:117], v[122:125], v[16:31]
	ds_read_b64_tr_b16 v[122:123], v174 offset:0x2600
	ds_read_b64_tr_b16 v[124:125], v174 offset:0x2700
	ds_read_b64_tr_b16 v[130:131], v174 offset:0x3600
	ds_read_b64_tr_b16 v[132:133], v174 offset:0x3700
	s_waitcnt lgkmcnt(0)
	v_mfma_f32_32x32x16_bf16 v[16:31], v[100:103], v[126:129], v[16:31]
	v_mfma_f32_32x32x16_bf16 v[32:47], v[110:113], v[96:99], v[32:47]
	v_max_f32_e32 v126, v81, v81
	v_max_f32_e32 v127, v80, v80
	v_max_f32_e32 v126, v127, v126
	v_max3_f32 v126, v126, v82, v83
	v_max3_f32 v126, v126, v84, v85
	v_max3_f32 v96, v126, v86, v87
	v_max3_f32 v96, v96, v88, v89
	v_max3_f32 v96, v96, v90, v91
	v_mfma_f32_32x32x16_bf16 v[32:47], v[104:107], v[118:121], v[32:47]
	v_max3_f32 v96, v96, v92, v93
	v_max3_f32 v96, v96, v94, v95
	v_max3_f32 v96, v96, v64, v65
	v_max3_f32 v96, v96, v66, v67
	v_max3_f32 v96, v96, v68, v69
	v_max3_f32 v96, v96, v70, v71
	v_max3_f32 v96, v96, v72, v73
	v_max3_f32 v96, v96, v74, v75
	v_mfma_f32_32x32x16_bf16 v[32:47], v[114:117], v[122:125], v[32:47]
	v_max3_f32 v96, v96, v76, v77
	v_max3_f32 v96, v96, v78, v79
	v_mov_b32_e32 v97, v96
	s_nop 1
	v_permlane32_swap_b32_e32 v96, v97
	v_max_f32_e32 v97, v97, v97
	v_max_f32_e32 v96, v96, v96
	v_max_f32_e32 v96, v96, v97
	v_max_f32_e32 v97, v205, v205
	v_max_f32_e32 v97, v97, v96
	v_sub_f32_e32 v98, v96, v205
	v_mfma_f32_32x32x16_bf16 v[32:47], v[100:103], v[130:133], v[32:47]
	v_sub_f32_e32 v96, v205, v97
	v_mul_f32_e32 v96, 0x3dd53b94, v96
	v_exp_f32_e32 v96, v96
	v_cmp_ge_f32_e32 vcc, s58, v98
	s_cmp_eq_u64 vcc, exec
	s_cselect_b64 s[4:5], -1, 0
	v_cndmask_b32_e64 v96, v96, 1.0, s[4:5]
	v_cmp_gt_f32_e32 vcc, 1.0, v96
	s_barrier
	s_cbranch_vccz .LBB0_960
	s_and_saveexec_b64 s[28:29], s[2:3]
	ds_write_b32 v147, v96 offset:128
	s_or_b64 exec, exec, s[28:29]
	s_waitcnt lgkmcnt(0)
	v_add_u32_e32 v106, s35, v144
	ds_read_b128 v[98:101], v106 offset:224
	ds_read_b128 v[102:105], v106 offset:192
	ds_read_b128 v[110:113], v106 offset:160
	ds_read_b128 v[114:117], v106 offset:128
	s_waitcnt lgkmcnt(3)
	v_pk_mul_f32 v[12:13], v[12:13], v[98:99]
	s_waitcnt lgkmcnt(2)
	v_pk_mul_f32 v[8:9], v[8:9], v[102:103]
	s_waitcnt lgkmcnt(1)
	v_pk_mul_f32 v[4:5], v[4:5], v[110:111]
	v_pk_mul_f32 v[14:15], v[14:15], v[100:101]
	v_pk_mul_f32 v[10:11], v[10:11], v[104:105]
	v_pk_mul_f32 v[6:7], v[6:7], v[112:113]
	s_waitcnt lgkmcnt(0)
	v_pk_mul_f32 v[2:3], v[2:3], v[116:117]
	v_pk_mul_f32 v[0:1], v[0:1], v[114:115]
	v_pk_mul_f32 v[60:61], v[60:61], v[98:99]
	v_pk_mul_f32 v[56:57], v[56:57], v[102:103]
	v_pk_mul_f32 v[52:53], v[52:53], v[110:111]
	v_pk_mul_f32 v[62:63], v[62:63], v[100:101]
	v_pk_mul_f32 v[58:59], v[58:59], v[104:105]
	v_pk_mul_f32 v[54:55], v[54:55], v[112:113]
	v_pk_mul_f32 v[50:51], v[50:51], v[116:117]
	v_pk_mul_f32 v[48:49], v[48:49], v[114:115]
	v_pk_mul_f32 v[28:29], v[28:29], v[98:99]
	v_pk_mul_f32 v[24:25], v[24:25], v[102:103]
	v_pk_mul_f32 v[20:21], v[20:21], v[110:111]
	v_pk_mul_f32 v[30:31], v[30:31], v[100:101]
	v_pk_mul_f32 v[26:27], v[26:27], v[104:105]
	v_pk_mul_f32 v[22:23], v[22:23], v[112:113]
	v_pk_mul_f32 v[18:19], v[18:19], v[116:117]
	v_pk_mul_f32 v[16:17], v[16:17], v[114:115]
	v_pk_mul_f32 v[44:45], v[44:45], v[98:99]
	v_pk_mul_f32 v[40:41], v[40:41], v[102:103]
	v_pk_mul_f32 v[36:37], v[36:37], v[110:111]
	v_pk_mul_f32 v[46:47], v[46:47], v[100:101]
	v_pk_mul_f32 v[42:43], v[42:43], v[104:105]
	v_pk_mul_f32 v[38:39], v[38:39], v[112:113]
	v_pk_mul_f32 v[34:35], v[34:35], v[116:117]
	v_pk_mul_f32 v[32:33], v[32:33], v[114:115]
.LBB0_960:
	v_cndmask_b32_e64 v97, v97, v205, s[4:5]
	v_mul_f32_e32 v97, 0xbdd53b94, v97
	v_fmamk_f32 v80, v80, 0x3dd53b94, v97
	v_fmamk_f32 v81, v81, 0x3dd53b94, v97
	v_fmamk_f32 v106, v93, 0x3dd53b94, v97
	v_fmamk_f32 v93, v74, 0x3dd53b94, v97
	v_exp_f32_e32 v74, v80
	v_fmamk_f32 v82, v82, 0x3dd53b94, v97
	v_fmamk_f32 v107, v94, 0x3dd53b94, v97
	v_fmamk_f32 v94, v75, 0x3dd53b94, v97
	v_exp_f32_e32 v75, v81
	v_fmamk_f32 v83, v83, 0x3dd53b94, v97
	v_fmamk_f32 v110, v95, 0x3dd53b94, v97
	v_fmamk_f32 v95, v76, 0x3dd53b94, v97
	v_exp_f32_e32 v76, v82
	v_fmamk_f32 v84, v84, 0x3dd53b94, v97
	v_fmamk_f32 v64, v64, 0x3dd53b94, v97
	v_exp_f32_e32 v80, v83
	v_fmamk_f32 v98, v85, 0x3dd53b94, v97
	v_fmamk_f32 v99, v86, 0x3dd53b94, v97
	v_fmamk_f32 v100, v87, 0x3dd53b94, v97
	v_fmamk_f32 v101, v88, 0x3dd53b94, v97
	v_fmamk_f32 v102, v89, 0x3dd53b94, v97
	v_fmamk_f32 v103, v90, 0x3dd53b94, v97
	v_fmamk_f32 v104, v91, 0x3dd53b94, v97
	v_fmamk_f32 v105, v92, 0x3dd53b94, v97
	v_fmamk_f32 v65, v65, 0x3dd53b94, v97
	v_fmamk_f32 v85, v66, 0x3dd53b94, v97
	v_fmamk_f32 v86, v67, 0x3dd53b94, v97
	v_fmamk_f32 v87, v68, 0x3dd53b94, v97
	v_fmamk_f32 v88, v69, 0x3dd53b94, v97
	v_fmamk_f32 v89, v70, 0x3dd53b94, v97
	v_fmamk_f32 v90, v71, 0x3dd53b94, v97
	v_fmamk_f32 v91, v72, 0x3dd53b94, v97
	v_fmamk_f32 v92, v73, 0x3dd53b94, v97
	v_exp_f32_e32 v81, v84
	v_fmamk_f32 v77, v77, 0x3dd53b94, v97
	v_fmamk_f32 v78, v78, 0x3dd53b94, v97
	v_fmac_f32_e32 v97, 0x3dd53b94, v79
	v_exp_f32_e32 v79, v64
	v_add_f32_e32 v64, 0, v74
	v_exp_f32_e32 v82, v98
	v_add_f32_e32 v64, v75, v64
	v_exp_f32_e32 v83, v99
	v_add_f32_e32 v64, v76, v64
	v_exp_f32_e32 v84, v100
	v_add_f32_e32 v64, v80, v64
	v_exp_f32_e32 v66, v101
	v_add_f32_e32 v64, v81, v64
	v_exp_f32_e32 v67, v102
	v_add_f32_e32 v64, v82, v64
	v_exp_f32_e32 v68, v103
	v_add_f32_e32 v64, v83, v64
	v_exp_f32_e32 v69, v104
	v_add_f32_e32 v64, v84, v64
	v_exp_f32_e32 v70, v105
	v_add_f32_e32 v64, v66, v64
	v_exp_f32_e32 v71, v106
	v_add_f32_e32 v64, v67, v64
	v_exp_f32_e32 v72, v107
	v_add_f32_e32 v64, v68, v64
	v_exp_f32_e32 v73, v110
	v_add_f32_e32 v64, v69, v64
	v_add_f32_e32 v64, v70, v64
	v_exp_f32_e32 v98, v65
	v_add_f32_e32 v64, v71, v64
	v_exp_f32_e32 v85, v85
	v_add_f32_e32 v64, v72, v64
	v_exp_f32_e32 v86, v86
	v_add_f32_e32 v64, v73, v64
	v_exp_f32_e32 v87, v87
	v_add_f32_e32 v64, v79, v64
	v_exp_f32_e32 v88, v88
	v_add_f32_e32 v64, v98, v64
	v_exp_f32_e32 v89, v89
	v_add_f32_e32 v64, v85, v64
	v_exp_f32_e32 v90, v90
	v_add_f32_e32 v64, v86, v64
	v_exp_f32_e32 v91, v91
	v_add_f32_e32 v64, v87, v64
	v_exp_f32_e32 v92, v92
	v_add_f32_e32 v64, v88, v64
	v_exp_f32_e32 v93, v93
	v_add_f32_e32 v64, v89, v64
	v_exp_f32_e32 v94, v94
	v_add_f32_e32 v64, v90, v64
	v_exp_f32_e32 v95, v95
	v_add_f32_e32 v64, v91, v64
	v_exp_f32_e32 v99, v77
	v_add_f32_e32 v64, v92, v64
	v_exp_f32_e32 v100, v78
	v_add_f32_e32 v64, v93, v64
	v_exp_f32_e32 v97, v97
	v_add_f32_e32 v64, v94, v64
	v_add_f32_e32 v64, v95, v64
	v_add_f32_e32 v64, v99, v64
	v_add_f32_e32 v64, v100, v64
	v_add_f32_e32 v64, v97, v64
	v_mov_b32_e32 v65, v64
	s_nop 1
	v_permlane32_swap_b32_e32 v64, v65
	v_cvt_pk_bf16_f32 v74, v74, v75
	v_cvt_pk_bf16_f32 v75, v76, v80
	v_cvt_pk_bf16_f32 v76, v81, v82
	v_cvt_pk_bf16_f32 v77, v83, v84
	v_cvt_pk_bf16_f32 v66, v66, v67
	v_cvt_pk_bf16_f32 v67, v68, v69
	v_cvt_pk_bf16_f32 v68, v70, v71
	v_cvt_pk_bf16_f32 v69, v72, v73
	v_cvt_pk_bf16_f32 v70, v79, v98
	v_cvt_pk_bf16_f32 v71, v85, v86
	v_cvt_pk_bf16_f32 v72, v87, v88
	v_cvt_pk_bf16_f32 v73, v89, v90
	v_cvt_pk_bf16_f32 v78, v91, v92
	v_cvt_pk_bf16_f32 v79, v93, v94
	v_cvt_pk_bf16_f32 v80, v95, v99
	v_cvt_pk_bf16_f32 v81, v100, v97
	ds_read_b64_tr_b16 v[82:83], v173 offset:0x0
	ds_read_b64_tr_b16 v[84:85], v173 offset:0x100
	ds_read_b64_tr_b16 v[86:87], v173 offset:0x1000
	ds_read_b64_tr_b16 v[88:89], v173 offset:0x1100
	ds_read_b64_tr_b16 v[90:91], v173 offset:0x2000
	ds_read_b64_tr_b16 v[92:93], v173 offset:0x2100
	ds_read_b64_tr_b16 v[98:99], v173 offset:0x3000
	ds_read_b64_tr_b16 v[100:101], v173 offset:0x3100
	s_waitcnt lgkmcnt(0)
	s_nop 0
	v_mfma_f32_32x32x16_bf16 v[0:15], v[74:77], v[82:85], v[0:15]
	ds_read_b64_tr_b16 v[82:83], v173 offset:0x200
	ds_read_b64_tr_b16 v[84:85], v173 offset:0x300
	v_mfma_f32_32x32x16_bf16 v[0:15], v[66:69], v[86:89], v[0:15]
	ds_read_b64_tr_b16 v[86:87], v173 offset:0x1200
	ds_read_b64_tr_b16 v[88:89], v173 offset:0x1300
	v_mfma_f32_32x32x16_bf16 v[0:15], v[70:73], v[90:93], v[0:15]
	ds_read_b64_tr_b16 v[90:91], v173 offset:0x2200
	ds_read_b64_tr_b16 v[92:93], v173 offset:0x2300
	ds_read_b64_tr_b16 v[102:103], v173 offset:0x3200
	ds_read_b64_tr_b16 v[104:105], v173 offset:0x3300
	s_waitcnt lgkmcnt(0)
	v_mfma_f32_32x32x16_bf16 v[0:15], v[78:81], v[98:101], v[0:15]
	v_mfma_f32_32x32x16_bf16 v[48:63], v[74:77], v[82:85], v[48:63]
	ds_read_b64_tr_b16 v[82:83], v173 offset:0x400
	ds_read_b64_tr_b16 v[84:85], v173 offset:0x500
	v_mfma_f32_32x32x16_bf16 v[48:63], v[66:69], v[86:89], v[48:63]
	ds_read_b64_tr_b16 v[86:87], v173 offset:0x1400
	ds_read_b64_tr_b16 v[88:89], v173 offset:0x1500
	v_mfma_f32_32x32x16_bf16 v[48:63], v[70:73], v[90:93], v[48:63]
	ds_read_b64_tr_b16 v[90:91], v173 offset:0x2400
	ds_read_b64_tr_b16 v[92:93], v173 offset:0x2500
	ds_read_b64_tr_b16 v[98:99], v173 offset:0x3400
	ds_read_b64_tr_b16 v[100:101], v173 offset:0x3500
	s_waitcnt lgkmcnt(0)
	v_mfma_f32_32x32x16_bf16 v[48:63], v[78:81], v[102:105], v[48:63]
	v_mfma_f32_32x32x16_bf16 v[16:31], v[74:77], v[82:85], v[16:31]
	ds_read_b64_tr_b16 v[82:83], v173 offset:0x600
	ds_read_b64_tr_b16 v[84:85], v173 offset:0x700
	v_mfma_f32_32x32x16_bf16 v[16:31], v[66:69], v[86:89], v[16:31]
	ds_read_b64_tr_b16 v[86:87], v173 offset:0x1600
	ds_read_b64_tr_b16 v[88:89], v173 offset:0x1700
	v_mfma_f32_32x32x16_bf16 v[16:31], v[70:73], v[90:93], v[16:31]
	ds_read_b64_tr_b16 v[90:91], v173 offset:0x2600
	ds_read_b64_tr_b16 v[92:93], v173 offset:0x2700
	ds_read_b64_tr_b16 v[102:103], v173 offset:0x3600
	ds_read_b64_tr_b16 v[104:105], v173 offset:0x3700
	s_waitcnt lgkmcnt(0)
	v_mfma_f32_32x32x16_bf16 v[16:31], v[78:81], v[98:101], v[16:31]
	v_mfma_f32_32x32x16_bf16 v[32:47], v[74:77], v[82:85], v[32:47]
	v_mfma_f32_32x32x16_bf16 v[32:47], v[66:69], v[86:89], v[32:47]
	v_mfma_f32_32x32x16_bf16 v[32:47], v[70:73], v[90:93], v[32:47]
	v_mfma_f32_32x32x16_bf16 v[32:47], v[78:81], v[102:105], v[32:47]
	s_and_saveexec_b64 s[4:5], s[2:3]
	s_cbranch_execz .LBB0_932
	v_add_f32_e32 v66, v108, v109
	v_fmac_f32_e32 v66, v172, v208
	v_add_f32_e32 v64, v64, v65
	v_fmac_f32_e32 v64, v66, v96
	ds_write_b32 v147, v64
	s_branch .LBB0_932

.LBB0_2189:
	s_load_dwordx2 s[30:31], s[2:3], 0x78
	s_ashr_i32 s2, s57, 4
	s_mul_hi_i32 s3, s2, 0x2aaaaaab
	s_lshr_b32 s4, s3, 31
	s_add_i32 s3, s3, s4
	s_mul_i32 s3, s3, 6
	s_sub_i32 s2, s2, s3
	s_mul_hi_i32 s3, s57, 0x2aaaaaab
	s_lshr_b32 s4, s3, 31
	s_ashr_i32 s3, s3, 4
	s_add_i32 s28, s3, s4
	s_mul_i32 s3, s2, 0x56
	s_lshr_b32 s4, s3, 8
	s_bfe_u32 s3, s3, 0x1000f
	s_add_i32 s4, s4, s3
	s_ashr_i32 s29, s28, 31
	s_lshl_b32 s3, s57, 8
	s_lshl_b64 s[34:35], s[28:29], 12
	s_and_b32 s3, s3, 0xf00
	s_or_b32 s34, s34, s3
	s_sext_i32_i8 s37, s4
	s_mul_i32 s3, s35, 0x600
	s_mul_hi_u32 s4, s34, 0x600
	s_add_i32 s4, s4, s3
	s_mul_i32 s3, s34, 0x600
	s_add_u32 s5, s26, s3
	s_addc_u32 s4, s27, s4
	s_lshl_b32 s24, s2, 7
	s_ashr_i32 s25, s24, 31
	s_lshl_b64 s[2:3], s[24:25], 1
	s_add_u32 s2, s5, s2
	s_addc_u32 s3, s4, s3
	s_add_u32 s38, s2, 0x48560200
	s_addc_u32 s39, s3, 0
	s_lshl_b64 s[4:5], s[28:29], 21
	s_add_u32 s40, s26, s4
	s_addc_u32 s41, s27, s5
	s_lshl_b32 s2, s37, 7
	s_ashr_i32 s3, s2, 31
	s_lshl_b64 s[52:53], s[2:3], 1
	s_add_u32 s2, s40, s52
	s_addc_u32 s3, s41, s53
	s_add_u32 s2, s2, 0x49d60200
	s_addc_u32 s3, s3, 0
	s_lshl_b64 s[28:29], s[28:29], 25
	s_add_u32 s37, s26, s28
	s_addc_u32 s40, s27, s29
	s_add_u32 s37, s37, s52
	s_waitcnt lgkmcnt(0)
	s_addc_u32 s40, s40, s53
	s_add_u32 s54, s37, 0x40560a00
	v_ashrrev_i32_e32 v54, 4, v0
	v_lshlrev_b32_e32 v1, 3, v0
	v_ashrrev_i32_e32 v55, 31, v54
	s_addc_u32 s55, s40, 0
	v_and_b32_e32 v2, 0x78, v1
	v_lshlrev_b64 v[48:49], 13, v[54:55]
	v_lshlrev_b32_e32 v52, 1, v2
	v_add_u32_e32 v18, 32, v54
	v_lshl_add_u64 v[2:3], s[54:55], 0, v[48:49]
	v_mov_b32_e32 v53, v177
	v_lshl_add_u64 v[2:3], v[2:3], 0, v[52:53]
	v_ashrrev_i32_e32 v19, 31, v18
	global_load_dwordx4 v[2:5], v[2:3], off
	v_lshlrev_b64 v[6:7], 13, v[18:19]
	v_lshlrev_b64 v[50:51], 9, v[54:55]
	v_lshl_add_u64 v[6:7], s[54:55], 0, v[6:7]
	v_lshl_add_u64 v[10:11], s[2:3], 0, v[50:51]
	v_lshl_add_u64 v[6:7], v[6:7], 0, v[52:53]
	v_lshl_add_u64 v[10:11], v[10:11], 0, v[52:53]
	global_load_dwordx4 v[6:9], v[6:7], off
	v_lshlrev_b64 v[14:15], 9, v[18:19]
	global_load_dwordx4 v[10:13], v[10:11], off
	v_lshl_add_u64 v[14:15], s[2:3], 0, v[14:15]
	v_lshl_add_u64 v[14:15], v[14:15], 0, v[52:53]
	v_readfirstlane_b32 s37, v0
	global_load_dwordx4 v[14:17], v[14:15], off
	s_ashr_i32 s40, s37, 1
	v_mov_b32_e32 v19, s40
	v_bfe_u32 v189, v0, 5, 1
	v_bfi_b32 v19, s1, v19, v0
	v_mov_b64_e32 v[20:21], s[38:39]
	v_mad_i64_i32 v[20:21], s[38:39], v19, s0, v[20:21]
	v_lshlrev_b32_e32 v176, 4, v189
	v_lshl_add_u64 v[20:21], v[20:21], 0, v[176:177]
	global_load_dwordx4 v[124:127], v[20:21], off
	global_load_dwordx4 v[120:123], v[20:21], off offset:32
	global_load_dwordx4 v[116:119], v[20:21], off offset:64
	global_load_dwordx4 v[112:115], v[20:21], off offset:96
	global_load_dwordx4 v[108:111], v[20:21], off offset:128
	global_load_dwordx4 v[104:107], v[20:21], off offset:160
	global_load_dwordx4 v[100:103], v[20:21], off offset:192
	global_load_dwordx4 v[96:99], v[20:21], off offset:224
	v_and_b32_e32 v19, 0xfffff0, v54
	v_lshlrev_b32_e32 v20, 1, v54
	v_and_or_b32 v19, v20, 8, v19
	v_and_b32_e32 v22, 0xfffff0, v18
	v_lshlrev_b32_e32 v23, 1, v18
	v_lshrrev_b32_e32 v20, 1, v54
	v_lshrrev_b32_e32 v19, 1, v19
	v_bfe_u32 v1, v1, 5, 2
	v_and_b32_e32 v21, 3, v54
	v_and_or_b32 v22, v23, 8, v22
	v_or_b32_e32 v19, v19, v1
	v_and_or_b32 v20, v20, 4, v21
	v_lshrrev_b32_e32 v22, 1, v22
	v_lshlrev_b32_e32 v19, 9, v19
	v_lshlrev_b32_e32 v20, 6, v20
	v_and_b32_e32 v21, 48, v52
	v_or_b32_e32 v1, v22, v1
	v_or3_b32 v19, v19, v20, v21
	v_lshlrev_b32_e32 v1, 9, v1
	v_or3_b32 v1, v1, v20, v21
	v_add_u32_e32 v193, 0, v19
	s_waitcnt vmcnt(0)
	v_add_u32_e32 v194, 0, v1
	v_lshlrev_b32_e32 v1, 8, v54
	v_and_b32_e32 v178, 31, v0
	v_lshlrev_b32_e32 v78, 4, v0
	v_and_b32_e32 v79, 63, v0
	v_add_u32_e32 v64, 64, v54
	v_add_u32_e32 v66, 0x60, v54
	v_ashrrev_i32_e32 v65, 31, v64
	v_ashrrev_i32_e32 v67, 31, v66
	v_add_u32_e32 v72, 0xa0, v54
	v_ashrrev_i32_e32 v73, 31, v72
	v_add_u32_e32 v54, 0x80, v54
	v_lshlrev_b64 v[74:75], 9, v[72:73]
	v_lshlrev_b64 v[72:73], 13, v[72:73]
	v_lshl_add_u64 v[74:75], s[2:3], 0, v[74:75]
	v_lshl_add_u64 v[72:73], s[54:55], 0, v[72:73]
	v_lshl_add_u64 v[74:75], v[74:75], 0, v[52:53]
	v_lshl_add_u64 v[72:73], v[72:73], 0, v[52:53]
	s_and_b32 s37, s37, 0x3fffffc0
	s_lshl_b32 s37, s37, 2
	s_add_i32 s59, s37, 0
	s_add_i32 s59, s59, 0x10000
	s_and_b32 s58, s40, 0xffffffe0
	s_cmp_lg_u32 0, -1
	s_cselect_b32 s61, 0, 0
	s_mov_b32 s37, s36
	s_mov_b32 s38, s36
	s_mov_b32 s39, s36
	s_mov_b32 s40, s36
	s_mov_b32 s41, s36
	s_mov_b32 s42, s36
	s_mov_b32 s43, s36
	s_mov_b32 s44, s36
	s_waitcnt vmcnt(11)
	ds_write_b128 v193, v[2:5]
	v_and_b32_e32 v2, 0x70, v0
	v_bitop3_b32 v1, v52, v1, v2 bitop3:0xde
	v_add_u32_e32 v195, 0, v1
	v_lshlrev_b32_e32 v1, 8, v18
	v_bitop3_b32 v1, v52, v1, v2 bitop3:0xde
	v_add_u32_e32 v196, 0, v1
	s_waitcnt vmcnt(10)
	ds_write_b128 v194, v[6:9]
	s_mov_b32 s45, s36
	s_waitcnt vmcnt(9)
	ds_write_b128 v195, v[10:13] offset:32768
	v_lshlrev_b32_e32 v10, 8, v178
	v_and_b32_e32 v11, 0x70, v78
	v_bitop3_b32 v1, v176, v10, v11 bitop3:0xde
	v_add_u32_e32 v197, 0, v1
	s_waitcnt vmcnt(8)
	ds_write_b128 v196, v[14:17] offset:32768
	s_waitcnt lgkmcnt(0)
	s_barrier
	ds_read_b128 v[2:5], v197 offset:32768
	ds_read_b128 v[6:9], v197 offset:40960
	s_waitcnt vmcnt(7) lgkmcnt(1)
	v_mfma_f32_32x32x16_bf16 v[32:47], v[2:5], v[124:127], 0
	v_or_b32_e32 v1, 32, v176
	v_bitop3_b32 v1, v1, v10, v11 bitop3:0xde
	v_add_u32_e32 v198, 0, v1
	v_or_b32_e32 v1, 64, v176
	v_bitop3_b32 v1, v1, v10, v11 bitop3:0xde
	v_add_u32_e32 v199, 0, v1
	v_or_b32_e32 v1, 0x60, v176
	s_waitcnt lgkmcnt(0)
	v_mfma_f32_32x32x16_bf16 v[16:31], v[6:9], v[124:127], 0
	ds_read_b128 v[2:5], v198 offset:32768
	ds_read_b128 v[6:9], v198 offset:40960
	v_bitop3_b32 v1, v1, v10, v11 bitop3:0xde
	v_add_u32_e32 v200, 0, v1
	v_or_b32_e32 v1, 0x80, v176
	v_bitop3_b32 v1, v1, v10, v11 bitop3:0xde
	v_add_u32_e32 v201, 0, v1
	v_or_b32_e32 v1, 0xa0, v176
	s_waitcnt vmcnt(6) lgkmcnt(1)
	v_mfma_f32_32x32x16_bf16 v[32:47], v[2:5], v[120:123], v[32:47]
	v_bitop3_b32 v1, v1, v10, v11 bitop3:0xde
	v_add_u32_e32 v202, 0, v1
	v_lshlrev_b32_e32 v12, 3, v79
	v_and_b32_e32 v1, 0xc0, v78
	s_mov_b32 s46, s36
	s_mov_b32 s47, s36
	s_mov_b32 s48, s36
	s_waitcnt lgkmcnt(0)
	v_mfma_f32_32x32x16_bf16 v[16:31], v[6:9], v[120:123], v[16:31]
	ds_read_b128 v[2:5], v199 offset:32768
	ds_read_b128 v[6:9], v199 offset:40960
	s_mov_b32 s49, s36
	s_mov_b32 s50, s36
	s_mov_b32 s51, s36
	s_mov_b32 s60, 1
	v_lshl_add_u32 v179, v178, 2, s59
	v_mov_b32_e32 v190, 0
	s_waitcnt vmcnt(5) lgkmcnt(1)
	v_mfma_f32_32x32x16_bf16 v[32:47], v[2:5], v[116:119], v[32:47]
	s_waitcnt lgkmcnt(0)
	v_mfma_f32_32x32x16_bf16 v[16:31], v[6:9], v[116:119], v[16:31]
	ds_read_b128 v[2:5], v200 offset:32768
	ds_read_b128 v[6:9], v200 offset:40960
	s_waitcnt vmcnt(4) lgkmcnt(1)
	v_mfma_f32_32x32x16_bf16 v[32:47], v[2:5], v[112:115], v[32:47]
	s_waitcnt lgkmcnt(0)
	v_mfma_f32_32x32x16_bf16 v[16:31], v[6:9], v[112:115], v[16:31]
	ds_read_b128 v[2:5], v201 offset:32768
	ds_read_b128 v[6:9], v201 offset:40960
	s_waitcnt vmcnt(3) lgkmcnt(1)
	v_mfma_f32_32x32x16_bf16 v[32:47], v[2:5], v[108:111], v[32:47]
	ds_read_b128 v[2:5], v202 offset:32768
	s_waitcnt lgkmcnt(1)
	v_mfma_f32_32x32x16_bf16 v[16:31], v[6:9], v[108:111], v[16:31]
	ds_read_b128 v[6:9], v202 offset:40960
	s_waitcnt vmcnt(2) lgkmcnt(1)
	v_mfma_f32_32x32x16_bf16 v[32:47], v[2:5], v[104:107], v[32:47]
	v_lshlrev_b32_e32 v5, 1, v0
	v_or_b32_e32 v0, 0xc0, v176
	v_bitop3_b32 v0, v0, v10, v11 bitop3:0xde
	v_add_u32_e32 v203, 0, v0
	v_and_or_b32 v4, v12, 24, v1
	ds_read_b128 v[0:3], v203 offset:32768
	v_and_b32_e32 v5, 32, v5
	s_waitcnt lgkmcnt(1)
	v_mfma_f32_32x32x16_bf16 v[16:31], v[6:9], v[104:107], v[16:31]
	v_lshlrev_b32_e32 v6, 3, v12
	v_and_b32_e32 v6, 0x800, v6
	v_or3_b32 v80, v4, v5, v6
	ds_read_b128 v[4:7], v203 offset:40960
	v_add_u32_e32 v192, s61, v80
	s_waitcnt vmcnt(1) lgkmcnt(1)
	v_mfma_f32_32x32x16_bf16 v[32:47], v[0:3], v[100:103], v[32:47]
	v_or_b32_e32 v0, 0xe0, v176
	v_bitop3_b32 v0, v0, v10, v11 bitop3:0xde
	v_add_u32_e32 v204, 0, v0
	ds_read_b128 v[0:3], v204 offset:32768
	ds_read_b128 v[56:59], v204 offset:40960
	s_waitcnt lgkmcnt(2)
	v_mfma_f32_32x32x16_bf16 v[16:31], v[4:7], v[100:103], v[16:31]
	s_waitcnt vmcnt(0) lgkmcnt(1)
	v_mfma_f32_32x32x16_bf16 v[32:47], v[0:3], v[96:99], v[32:47]
	v_mov_b64_e32 v[0:1], s[36:37]
	v_mov_b64_e32 v[14:15], s[50:51]
	v_mov_b64_e32 v[2:3], s[38:39]
	v_mov_b64_e32 v[4:5], s[40:41]
	v_mov_b64_e32 v[6:7], s[42:43]
	v_mov_b64_e32 v[8:9], s[44:45]
	v_mov_b64_e32 v[10:11], s[46:47]
	s_waitcnt lgkmcnt(0)
	v_mfma_f32_32x32x16_bf16 v[16:31], v[56:59], v[96:99], v[16:31]
	s_nop 2
	v_max_f32_e32 v55, v33, v33
	v_max_f32_e32 v56, v32, v32
	v_max_f32_e32 v55, v56, v55
	v_max3_f32 v55, v55, v34, v35
	v_max3_f32 v55, v55, v36, v37
	v_max3_f32 v55, v55, v38, v39
	v_max3_f32 v55, v55, v40, v41
	v_max3_f32 v55, v55, v42, v43
	v_max3_f32 v55, v55, v44, v45
	v_max3_f32 v55, v55, v46, v47
	v_max3_f32 v55, v55, v16, v17
	v_max3_f32 v55, v55, v18, v19
	v_max3_f32 v55, v55, v20, v21
	v_max3_f32 v55, v55, v22, v23
	v_max3_f32 v55, v55, v24, v25
	v_max3_f32 v55, v55, v26, v27
	v_lshlrev_b64 v[56:57], 13, v[64:65]
	v_lshlrev_b64 v[58:59], 13, v[66:67]
	v_lshlrev_b64 v[64:65], 9, v[64:65]
	v_lshlrev_b64 v[66:67], 9, v[66:67]
	v_max3_f32 v55, v55, v28, v29
	v_lshl_add_u64 v[56:57], s[54:55], 0, v[56:57]
	v_lshl_add_u64 v[58:59], s[54:55], 0, v[58:59]
	v_lshl_add_u64 v[64:65], s[2:3], 0, v[64:65]
	v_lshl_add_u64 v[66:67], s[2:3], 0, v[66:67]
	v_max3_f32 v81, v55, v30, v31
	v_lshl_add_u64 v[56:57], v[56:57], 0, v[52:53]
	v_lshl_add_u64 v[60:61], v[58:59], 0, v[52:53]
	v_lshl_add_u64 v[64:65], v[64:65], 0, v[52:53]
	v_lshl_add_u64 v[68:69], v[66:67], 0, v[52:53]
	v_ashrrev_i32_e32 v55, 31, v54
	global_load_dwordx4 v[56:59], v[56:57], off
	s_nop 0
	global_load_dwordx4 v[60:63], v[60:61], off
	s_nop 0
	global_load_dwordx4 v[64:67], v[64:65], off
	s_nop 0
	global_load_dwordx4 v[68:71], v[68:69], off
	v_lshlrev_b64 v[76:77], 9, v[54:55]
	v_lshlrev_b64 v[54:55], 13, v[54:55]
	v_lshl_add_u64 v[76:77], s[2:3], 0, v[76:77]
	v_lshl_add_u64 v[54:55], s[54:55], 0, v[54:55]
	v_lshl_add_u64 v[76:77], v[76:77], 0, v[52:53]
	global_load_dwordx4 v[140:143], v[74:75], off
	global_load_dwordx4 v[136:139], v[76:77], off
	v_lshl_add_u64 v[52:53], v[54:55], 0, v[52:53]
	global_load_dwordx4 v[132:135], v[72:73], off
	global_load_dwordx4 v[128:131], v[52:53], off
	v_mov_b32_e32 v82, v81
	s_nop 1
	v_permlane32_swap_b32_e32 v81, v82
	v_max_f32_e32 v52, v82, v82
	v_max_f32_e32 v53, v81, v81
	v_max_f32_e32 v52, v53, v52
	v_add_f32_e32 v53, 0x7149f2ca, v52
	v_max_f32_e32 v52, 0xf149f2ca, v52
	v_cmp_ge_f32_e32 vcc, s9, v53
	v_sub_f32_e32 v53, 0xf149f2ca, v52
	v_mul_f32_e32 v53, 0x3e0293ee, v53
	v_exp_f32_e32 v53, v53
	s_cmp_eq_u64 vcc, exec
	s_cselect_b64 vcc, -1, 0
	v_cndmask_b32_e32 v160, v52, v188, vcc
	v_mul_f32_e32 v52, 0xbe0293ee, v160
	v_cndmask_b32_e64 v205, v53, 1.0, vcc
	v_mov_b32_e32 v53, v52
	v_fmac_f32_e32 v53, 0x3e0293ee, v47
	v_pk_fma_f32 v[150:151], v[18:19], s[8:9], v[52:53] op_sel_hi:[1,0,0]
	v_pk_fma_f32 v[152:153], v[16:17], s[8:9], v[52:53] op_sel_hi:[1,0,0]
	v_lshl_add_u64 v[16:17], s[4:5], 0, v[50:51]
	v_and_b32_e32 v18, 0xf0, v78
	v_fmamk_f32 v32, v32, 0x3e0293ee, v52
	v_fmamk_f32 v33, v33, 0x3e0293ee, v52
	v_fmamk_f32 v34, v34, 0x3e0293ee, v52
	v_fmamk_f32 v35, v35, 0x3e0293ee, v52
	v_fmamk_f32 v36, v36, 0x3e0293ee, v52
	v_fmamk_f32 v37, v37, 0x3e0293ee, v52
	v_fmamk_f32 v38, v38, 0x3e0293ee, v52
	v_fmamk_f32 v39, v39, 0x3e0293ee, v52
	v_fmamk_f32 v40, v40, 0x3e0293ee, v52
	v_fmamk_f32 v41, v41, 0x3e0293ee, v52
	v_fmamk_f32 v42, v42, 0x3e0293ee, v52
	v_fmamk_f32 v43, v43, 0x3e0293ee, v52
	v_fmamk_f32 v44, v44, 0x3e0293ee, v52
	v_fmamk_f32 v45, v45, 0x3e0293ee, v52
	v_fmamk_f32 v46, v46, 0x3e0293ee, v52
	v_or_b32_e32 v16, v16, v18
	v_exp_f32_e32 v170, v32
	v_exp_f32_e32 v171, v33
	v_exp_f32_e32 v172, v34
	v_exp_f32_e32 v173, v35
	v_exp_f32_e32 v174, v36
	v_exp_f32_e32 v184, v37
	v_exp_f32_e32 v175, v38
	v_exp_f32_e32 v185, v39
	v_exp_f32_e32 v162, v40
	v_exp_f32_e32 v163, v41
	v_exp_f32_e32 v164, v42
	v_exp_f32_e32 v166, v43
	v_exp_f32_e32 v165, v44
	v_exp_f32_e32 v167, v45
	v_exp_f32_e32 v168, v46
	v_exp_f32_e32 v169, v53
	v_lshl_add_u64 v[180:181], s[26:27], 0, v[16:17]
	v_lshl_add_u64 v[16:17], s[28:29], 0, v[48:49]
	s_waitcnt vmcnt(4)
	v_or_b32_e32 v16, v16, v18
	v_mov_b64_e32 v[12:13], s[48:49]
	v_pk_fma_f32 v[154:155], v[30:31], s[8:9], v[52:53] op_sel_hi:[1,0,0]
	v_pk_fma_f32 v[156:157], v[28:29], s[8:9], v[52:53] op_sel_hi:[1,0,0]
	v_pk_fma_f32 v[158:159], v[26:27], s[8:9], v[52:53] op_sel_hi:[1,0,0]
	v_pk_fma_f32 v[144:145], v[24:25], s[8:9], v[52:53] op_sel_hi:[1,0,0]
	v_pk_fma_f32 v[146:147], v[22:23], s[8:9], v[52:53] op_sel_hi:[1,0,0]
	v_pk_fma_f32 v[148:149], v[20:21], s[8:9], v[52:53] op_sel_hi:[1,0,0]
	s_waitcnt vmcnt(7)
	ds_write_b128 v193, v[56:59] offset:16384
	s_waitcnt vmcnt(6)
	ds_write_b128 v194, v[60:63] offset:16384
	s_waitcnt vmcnt(5)
	ds_write_b128 v195, v[64:67] offset:49152
	s_waitcnt vmcnt(4)
	ds_write_b128 v196, v[68:71] offset:49152
	s_addk_i32 s61, 0x4000
	v_lshl_add_u64 v[182:183], s[26:27], 0, v[16:17]
	v_mov_b64_e32 v[62:63], v[14:15]
	v_mov_b64_e32 v[30:31], v[14:15]
	v_mov_b64_e32 v[46:47], v[14:15]
	v_cmp_gt_u32_e64 s[2:3], 32, v79
	v_add_u32_e32 v191, s61, v80
	v_mov_b64_e32 v[60:61], v[12:13]
	v_mov_b64_e32 v[58:59], v[10:11]
	v_mov_b64_e32 v[56:57], v[8:9]
	v_mov_b64_e32 v[54:55], v[6:7]
	v_mov_b64_e32 v[52:53], v[4:5]
	v_mov_b64_e32 v[50:51], v[2:3]
	v_mov_b64_e32 v[48:49], v[0:1]
	v_mov_b64_e32 v[28:29], v[12:13]
	v_mov_b64_e32 v[26:27], v[10:11]
	v_mov_b64_e32 v[24:25], v[8:9]
	v_mov_b64_e32 v[22:23], v[6:7]
	v_mov_b64_e32 v[20:21], v[4:5]
	v_mov_b64_e32 v[18:19], v[2:3]
	v_mov_b64_e32 v[16:17], v[0:1]
	v_mov_b64_e32 v[44:45], v[12:13]
	v_mov_b64_e32 v[42:43], v[10:11]
	v_mov_b64_e32 v[40:41], v[8:9]
	v_mov_b64_e32 v[38:39], v[6:7]
	v_mov_b64_e32 v[36:37], v[4:5]
	v_mov_b64_e32 v[34:35], v[2:3]
	v_mov_b64_e32 v[32:33], v[0:1]
	s_waitcnt lgkmcnt(0)
	s_barrier
.LBB0_2190:
	ds_read_b128 v[64:67], v197 offset:49152
	ds_read_b128 v[68:71], v197 offset:57344
	ds_read_b128 v[206:209], v198 offset:49152
	ds_read_b128 v[210:213], v198 offset:57344
	ds_read_b128 v[214:217], v199 offset:49152
	ds_read_b128 v[218:221], v199 offset:57344
	v_add_f32_e32 v161, 0, v170
	v_add_f32_e32 v161, v171, v161
	s_waitcnt lgkmcnt(5)
	v_mfma_f32_32x32x16_bf16 v[80:95], v[64:67], v[124:127], 0
	v_add_f32_e32 v161, v172, v161
	v_add_f32_e32 v161, v173, v161
	v_add_f32_e32 v161, v174, v161
	v_add_f32_e32 v161, v184, v161
	v_add_f32_e32 v161, v175, v161
	v_add_f32_e32 v161, v185, v161
	v_add_f32_e32 v161, v162, v161
	s_waitcnt lgkmcnt(4)
	v_mfma_f32_32x32x16_bf16 v[64:79], v[68:71], v[124:127], 0
	v_add_f32_e32 v161, v163, v161
	v_add_f32_e32 v161, v164, v161
	v_add_f32_e32 v161, v166, v161
	v_exp_f32_e32 v152, v152
	v_add_f32_e32 v161, v165, v161
	v_exp_f32_e32 v153, v153
	v_add_f32_e32 v161, v167, v161
	s_waitcnt lgkmcnt(3)
	v_mfma_f32_32x32x16_bf16 v[80:95], v[206:209], v[120:123], v[80:95]
	ds_read_b128 v[206:209], v200 offset:49152
	ds_read_b128 v[222:225], v200 offset:57344
	ds_read_b128 v[226:229], v201 offset:49152
	ds_read_b128 v[230:233], v201 offset:57344
	ds_read_b128 v[234:237], v202 offset:49152
	ds_read_b128 v[238:241], v202 offset:57344
	ds_read_b128 v[242:245], v203 offset:49152
	ds_read_b128 v[246:249], v203 offset:57344
	v_exp_f32_e32 v150, v150
	v_add_f32_e32 v161, v168, v161
	v_exp_f32_e32 v151, v151
	v_add_f32_e32 v161, v169, v161
	v_exp_f32_e32 v148, v148
	v_add_f32_e32 v161, v152, v161
	s_waitcnt lgkmcnt(10)
	v_mfma_f32_32x32x16_bf16 v[64:79], v[210:213], v[120:123], v[64:79]
	v_exp_f32_e32 v149, v149
	v_add_f32_e32 v161, v153, v161
	v_exp_f32_e32 v146, v146
	v_add_f32_e32 v161, v150, v161
	v_exp_f32_e32 v147, v147
	v_add_f32_e32 v161, v151, v161
	v_exp_f32_e32 v144, v144
	s_waitcnt lgkmcnt(9)
	v_mfma_f32_32x32x16_bf16 v[80:95], v[214:217], v[116:119], v[80:95]
	v_add_f32_e32 v161, v148, v161
	ds_read_b128 v[210:213], v204 offset:49152
	ds_read_b128 v[250:253], v204 offset:57344
	v_exp_f32_e32 v145, v145
	v_add_f32_e32 v161, v149, v161
	v_exp_f32_e32 v158, v158
	v_add_f32_e32 v161, v146, v161
	v_exp_f32_e32 v159, v159
	s_waitcnt lgkmcnt(10)
	v_mfma_f32_32x32x16_bf16 v[64:79], v[218:221], v[116:119], v[64:79]
	v_add_f32_e32 v161, v147, v161
	v_exp_f32_e32 v156, v156
	v_add_f32_e32 v161, v144, v161
	v_exp_f32_e32 v157, v157
	v_add_f32_e32 v161, v145, v161
	v_exp_f32_e32 v154, v154
	v_add_f32_e32 v161, v158, v161
	s_waitcnt lgkmcnt(9)
	v_mfma_f32_32x32x16_bf16 v[80:95], v[206:209], v[112:115], v[80:95]
	v_exp_f32_e32 v155, v155
	v_add_f32_e32 v161, v159, v161
	v_add_f32_e32 v161, v156, v161
	v_add_f32_e32 v161, v157, v161
	v_add_f32_e32 v161, v154, v161
	v_add_f32_e32 v206, v155, v161
	v_mov_b32_e32 v207, v206
	s_waitcnt lgkmcnt(8)
	v_mfma_f32_32x32x16_bf16 v[64:79], v[222:225], v[112:115], v[64:79]
	v_cvt_pk_bf16_f32 v208, v144, v145
	v_permlane32_swap_b32_e32 v206, v207
	v_cvt_pk_bf16_f32 v170, v170, v171
	v_cvt_pk_bf16_f32 v171, v172, v173
	v_cvt_pk_bf16_f32 v172, v174, v184
	v_cvt_pk_bf16_f32 v173, v175, v185
	s_waitcnt lgkmcnt(7)
	v_mfma_f32_32x32x16_bf16 v[80:95], v[226:229], v[108:111], v[80:95]
	v_cvt_pk_bf16_f32 v162, v162, v163
	v_cvt_pk_bf16_f32 v163, v164, v166
	v_cvt_pk_bf16_f32 v164, v165, v167
	v_cvt_pk_bf16_f32 v165, v168, v169
	v_cvt_pk_bf16_f32 v166, v152, v153
	v_cvt_pk_bf16_f32 v167, v150, v151
	v_cvt_pk_bf16_f32 v168, v148, v149
	s_waitcnt lgkmcnt(6)
	v_mfma_f32_32x32x16_bf16 v[64:79], v[230:233], v[108:111], v[64:79]
	v_cvt_pk_bf16_f32 v169, v146, v147
	v_cvt_pk_bf16_f32 v209, v158, v159
	s_waitcnt lgkmcnt(5)
	v_mfma_f32_32x32x16_bf16 v[80:95], v[234:237], v[104:107], v[80:95]
	s_waitcnt lgkmcnt(4)
	v_mfma_f32_32x32x16_bf16 v[64:79], v[238:241], v[104:107], v[64:79]
	s_waitcnt lgkmcnt(3)
	v_mfma_f32_32x32x16_bf16 v[80:95], v[242:245], v[100:103], v[80:95]
	s_waitcnt lgkmcnt(2)
	v_mfma_f32_32x32x16_bf16 v[64:79], v[246:249], v[100:103], v[64:79]
	s_waitcnt lgkmcnt(1)
	v_mfma_f32_32x32x16_bf16 v[80:95], v[210:213], v[96:99], v[80:95]
	v_cvt_pk_bf16_f32 v210, v156, v157
	v_cvt_pk_bf16_f32 v211, v154, v155
	s_waitcnt lgkmcnt(0)
	v_mfma_f32_32x32x16_bf16 v[64:79], v[250:253], v[96:99], v[64:79]
	v_lshl_add_u64 v[186:187], v[182:183], 0, s[52:53]
	v_add_co_u32_e32 v144, vcc, s16, v186
	v_lshl_add_u64 v[184:185], v[180:181], 0, s[52:53]
	s_nop 0
	v_addc_co_u32_e32 v145, vcc, 0, v187, vcc
	v_add_co_u32_e32 v148, vcc, s17, v186
	s_nop 1
	v_addc_co_u32_e32 v149, vcc, 0, v187, vcc
	v_add_co_u32_e32 v152, vcc, s21, v184
	global_load_dwordx4 v[144:147], v[144:145], off offset:2560
	s_nop 0
	global_load_dwordx4 v[148:151], v[148:149], off offset:2560
	v_addc_co_u32_e32 v153, vcc, 0, v185, vcc
	v_add_co_u32_e32 v156, vcc, s23, v184
	s_nop 1
	v_addc_co_u32_e32 v157, vcc, 0, v185, vcc
	global_load_dwordx4 v[152:155], v[152:153], off offset:512
	s_nop 0
	global_load_dwordx4 v[156:159], v[156:157], off offset:512
	ds_read_b64_tr_b16 v[212:213], v192 offset:0x0
	ds_read_b64_tr_b16 v[214:215], v192 offset:0x100
	ds_read_b64_tr_b16 v[216:217], v192 offset:0x1000
	ds_read_b64_tr_b16 v[218:219], v192 offset:0x1100
	ds_read_b64_tr_b16 v[220:221], v192 offset:0x2000
	ds_read_b64_tr_b16 v[222:223], v192 offset:0x2100
	ds_read_b64_tr_b16 v[224:225], v192 offset:0x3000
	ds_read_b64_tr_b16 v[226:227], v192 offset:0x3100
	s_waitcnt lgkmcnt(0)
	s_nop 0
	v_mfma_f32_32x32x16_bf16 v[0:15], v[170:173], v[212:215], v[0:15]
	ds_read_b64_tr_b16 v[212:213], v192 offset:0x200
	ds_read_b64_tr_b16 v[214:215], v192 offset:0x300
	v_mfma_f32_32x32x16_bf16 v[0:15], v[162:165], v[216:219], v[0:15]
	ds_read_b64_tr_b16 v[216:217], v192 offset:0x1200
	ds_read_b64_tr_b16 v[218:219], v192 offset:0x1300
	v_mfma_f32_32x32x16_bf16 v[0:15], v[166:169], v[220:223], v[0:15]
	ds_read_b64_tr_b16 v[220:221], v192 offset:0x2200
	ds_read_b64_tr_b16 v[222:223], v192 offset:0x2300
	ds_read_b64_tr_b16 v[228:229], v192 offset:0x3200
	ds_read_b64_tr_b16 v[230:231], v192 offset:0x3300
	s_waitcnt lgkmcnt(0)
	v_mfma_f32_32x32x16_bf16 v[0:15], v[208:211], v[224:227], v[0:15]
	v_mfma_f32_32x32x16_bf16 v[48:63], v[170:173], v[212:215], v[48:63]
	ds_read_b64_tr_b16 v[212:213], v192 offset:0x400
	ds_read_b64_tr_b16 v[214:215], v192 offset:0x500
	v_mfma_f32_32x32x16_bf16 v[48:63], v[162:165], v[216:219], v[48:63]
	ds_read_b64_tr_b16 v[216:217], v192 offset:0x1400
	ds_read_b64_tr_b16 v[218:219], v192 offset:0x1500
	v_mfma_f32_32x32x16_bf16 v[48:63], v[166:169], v[220:223], v[48:63]
	ds_read_b64_tr_b16 v[220:221], v192 offset:0x2400
	ds_read_b64_tr_b16 v[222:223], v192 offset:0x2500
	ds_read_b64_tr_b16 v[224:225], v192 offset:0x3400
	ds_read_b64_tr_b16 v[226:227], v192 offset:0x3500
	s_waitcnt lgkmcnt(0)
	v_mfma_f32_32x32x16_bf16 v[48:63], v[208:211], v[228:231], v[48:63]
	v_mfma_f32_32x32x16_bf16 v[16:31], v[170:173], v[212:215], v[16:31]
	ds_read_b64_tr_b16 v[212:213], v192 offset:0x600
	ds_read_b64_tr_b16 v[214:215], v192 offset:0x700
	v_mfma_f32_32x32x16_bf16 v[16:31], v[162:165], v[216:219], v[16:31]
	ds_read_b64_tr_b16 v[216:217], v192 offset:0x1600
	ds_read_b64_tr_b16 v[218:219], v192 offset:0x1700
	v_mfma_f32_32x32x16_bf16 v[16:31], v[166:169], v[220:223], v[16:31]
	ds_read_b64_tr_b16 v[220:221], v192 offset:0x2600
	ds_read_b64_tr_b16 v[222:223], v192 offset:0x2700
	ds_read_b64_tr_b16 v[228:229], v192 offset:0x3600
	ds_read_b64_tr_b16 v[230:231], v192 offset:0x3700
	s_waitcnt lgkmcnt(0)
	v_mfma_f32_32x32x16_bf16 v[16:31], v[208:211], v[224:227], v[16:31]
	v_mfma_f32_32x32x16_bf16 v[32:47], v[170:173], v[212:215], v[32:47]
	v_max_f32_e32 v161, v81, v81
	v_max_f32_e32 v174, v80, v80
	v_max_f32_e32 v161, v174, v161
	v_max3_f32 v161, v161, v82, v83
	v_max3_f32 v161, v161, v84, v85
	v_max3_f32 v161, v161, v86, v87
	v_max3_f32 v161, v161, v88, v89
	v_max3_f32 v161, v161, v90, v91
	v_mfma_f32_32x32x16_bf16 v[32:47], v[162:165], v[216:219], v[32:47]
	v_max3_f32 v161, v161, v92, v93
	v_max3_f32 v161, v161, v94, v95
	v_max3_f32 v161, v161, v64, v65
	v_max3_f32 v161, v161, v66, v67
	v_max3_f32 v161, v161, v68, v69
	v_max3_f32 v161, v161, v70, v71
	v_max3_f32 v161, v161, v72, v73
	v_max3_f32 v161, v161, v74, v75
	v_mfma_f32_32x32x16_bf16 v[32:47], v[166:169], v[220:223], v[32:47]
	v_max3_f32 v161, v161, v76, v77
	v_max3_f32 v161, v161, v78, v79
	v_mov_b32_e32 v162, v161
	s_nop 1
	v_permlane32_swap_b32_e32 v161, v162
	v_max_f32_e32 v162, v162, v162
	v_max_f32_e32 v161, v161, v161
	v_max_f32_e32 v161, v161, v162
	v_max_f32_e32 v163, v160, v160
	v_sub_f32_e32 v162, v161, v160
	v_max_f32_e32 v161, v163, v161
	v_mfma_f32_32x32x16_bf16 v[32:47], v[208:211], v[228:231], v[32:47]
	v_sub_f32_e32 v163, v160, v161
	v_mul_f32_e32 v163, 0x3e0293ee, v163
	v_exp_f32_e32 v163, v163
	v_cmp_ge_f32_e32 vcc, s9, v162
	s_cmp_eq_u64 vcc, exec
	s_cselect_b64 s[4:5], -1, 0
	s_barrier
	s_waitcnt vmcnt(4)
	v_cndmask_b32_e64 v208, v163, 1.0, s[4:5]
	v_cmp_gt_f32_e32 vcc, 1.0, v208
	s_waitcnt vmcnt(4)
	ds_write_b128 v193, v[128:131]
	ds_write_b128 v194, v[132:135]
	ds_write_b128 v195, v[136:139] offset:32768
	ds_write_b128 v196, v[140:143] offset:32768
	s_cbranch_vccz .LBB0_2194
	s_and_saveexec_b64 s[28:29], s[2:3]
	ds_write_b32 v179, v208 offset:128
	s_or_b64 exec, exec, s[28:29]
	s_waitcnt lgkmcnt(0)
	v_add_u32_e32 v174, s59, v176
	ds_read_b128 v[162:165], v174 offset:224
	ds_read_b128 v[166:169], v174 offset:192
	ds_read_b128 v[170:173], v174 offset:160
	ds_read_b128 v[210:213], v174 offset:128
	s_waitcnt lgkmcnt(3)
	v_pk_mul_f32 v[12:13], v[12:13], v[162:163]
	s_waitcnt lgkmcnt(2)
	v_pk_mul_f32 v[8:9], v[8:9], v[166:167]
	s_waitcnt lgkmcnt(1)
	v_pk_mul_f32 v[4:5], v[4:5], v[170:171]
	v_pk_mul_f32 v[14:15], v[14:15], v[164:165]
	v_pk_mul_f32 v[10:11], v[10:11], v[168:169]
	v_pk_mul_f32 v[6:7], v[6:7], v[172:173]
	s_waitcnt lgkmcnt(0)
	v_pk_mul_f32 v[2:3], v[2:3], v[212:213]
	v_pk_mul_f32 v[0:1], v[0:1], v[210:211]
	v_pk_mul_f32 v[60:61], v[60:61], v[162:163]
	v_pk_mul_f32 v[56:57], v[56:57], v[166:167]
	v_pk_mul_f32 v[52:53], v[52:53], v[170:171]
	v_pk_mul_f32 v[62:63], v[62:63], v[164:165]
	v_pk_mul_f32 v[58:59], v[58:59], v[168:169]
	v_pk_mul_f32 v[54:55], v[54:55], v[172:173]
	v_pk_mul_f32 v[50:51], v[50:51], v[212:213]
	v_pk_mul_f32 v[48:49], v[48:49], v[210:211]
	v_pk_mul_f32 v[28:29], v[28:29], v[162:163]
	v_pk_mul_f32 v[24:25], v[24:25], v[166:167]
	v_pk_mul_f32 v[20:21], v[20:21], v[170:171]
	v_pk_mul_f32 v[30:31], v[30:31], v[164:165]
	v_pk_mul_f32 v[26:27], v[26:27], v[168:169]
	v_pk_mul_f32 v[22:23], v[22:23], v[172:173]
	v_pk_mul_f32 v[18:19], v[18:19], v[212:213]
	v_pk_mul_f32 v[16:17], v[16:17], v[210:211]
	v_pk_mul_f32 v[44:45], v[44:45], v[162:163]
	v_pk_mul_f32 v[40:41], v[40:41], v[166:167]
	v_pk_mul_f32 v[36:37], v[36:37], v[170:171]
	v_pk_mul_f32 v[46:47], v[46:47], v[164:165]
	v_pk_mul_f32 v[42:43], v[42:43], v[168:169]
	v_pk_mul_f32 v[38:39], v[38:39], v[172:173]
	v_pk_mul_f32 v[34:35], v[34:35], v[212:213]
	v_pk_mul_f32 v[32:33], v[32:33], v[210:211]
.LBB0_2194:
	v_cndmask_b32_e64 v209, v161, v160, s[4:5]
	v_mul_f32_e32 v210, 0xbe0293ee, v209
	v_fmamk_f32 v80, v80, 0x3e0293ee, v210
	v_fmamk_f32 v81, v81, 0x3e0293ee, v210
	v_fmamk_f32 v82, v82, 0x3e0293ee, v210
	v_fmamk_f32 v83, v83, 0x3e0293ee, v210
	v_fmamk_f32 v84, v84, 0x3e0293ee, v210
	v_fmamk_f32 v85, v85, 0x3e0293ee, v210
	v_fmamk_f32 v86, v86, 0x3e0293ee, v210
	v_fmamk_f32 v87, v87, 0x3e0293ee, v210
	v_fmamk_f32 v88, v88, 0x3e0293ee, v210
	v_fmamk_f32 v89, v89, 0x3e0293ee, v210
	v_fmamk_f32 v90, v90, 0x3e0293ee, v210
	v_fmamk_f32 v91, v91, 0x3e0293ee, v210
	v_fmamk_f32 v92, v92, 0x3e0293ee, v210
	v_fmamk_f32 v93, v93, 0x3e0293ee, v210
	v_fmamk_f32 v94, v94, 0x3e0293ee, v210
	v_fmamk_f32 v95, v95, 0x3e0293ee, v210
	v_exp_f32_e32 v160, v80
	v_exp_f32_e32 v161, v81
	v_exp_f32_e32 v162, v82
	v_exp_f32_e32 v173, v83
	v_exp_f32_e32 v174, v84
	v_exp_f32_e32 v175, v85
	v_exp_f32_e32 v163, v86
	v_exp_f32_e32 v172, v87
	v_exp_f32_e32 v164, v88
	v_exp_f32_e32 v165, v89
	v_exp_f32_e32 v169, v90
	v_exp_f32_e32 v171, v91
	v_exp_f32_e32 v166, v92
	v_exp_f32_e32 v167, v93
	v_exp_f32_e32 v168, v94
	v_exp_f32_e32 v170, v95
	v_fmamk_f32 v220, v64, 0x3e0293ee, v210
	v_fmamk_f32 v221, v65, 0x3e0293ee, v210
	v_fmamk_f32 v222, v66, 0x3e0293ee, v210
	v_fmamk_f32 v223, v67, 0x3e0293ee, v210
	v_fmamk_f32 v224, v68, 0x3e0293ee, v210
	v_fmamk_f32 v212, v69, 0x3e0293ee, v210
	v_fmamk_f32 v213, v70, 0x3e0293ee, v210
	v_fmamk_f32 v214, v71, 0x3e0293ee, v210
	v_fmamk_f32 v215, v72, 0x3e0293ee, v210
	v_fmamk_f32 v217, v73, 0x3e0293ee, v210
	v_fmamk_f32 v218, v74, 0x3e0293ee, v210
	v_fmamk_f32 v219, v75, 0x3e0293ee, v210
	v_fmamk_f32 v211, v76, 0x3e0293ee, v210
	v_fmamk_f32 v225, v77, 0x3e0293ee, v210
	v_fmamk_f32 v226, v78, 0x3e0293ee, v210
	v_fmac_f32_e32 v210, 0x3e0293ee, v79
	s_waitcnt lgkmcnt(0)
	s_barrier
	ds_read_b128 v[64:67], v197 offset:32768
	ds_read_b128 v[68:71], v197 offset:40960
	ds_read_b128 v[228:231], v198 offset:32768
	ds_read_b128 v[232:235], v198 offset:40960
	v_exp_f32_e32 v227, v210
	v_add_f32_e32 v210, 0, v160
	s_waitcnt lgkmcnt(3)
	v_mfma_f32_32x32x16_bf16 v[80:95], v[64:67], v[124:127], 0
	v_add_f32_e32 v210, v161, v210
	v_add_f32_e32 v210, v162, v210
	v_add_f32_e32 v210, v173, v210
	v_add_f32_e32 v210, v174, v210
	v_add_f32_e32 v210, v175, v210
	v_add_f32_e32 v210, v163, v210
	v_add_f32_e32 v210, v172, v210
	s_waitcnt lgkmcnt(2)
	v_mfma_f32_32x32x16_bf16 v[64:79], v[68:71], v[124:127], 0
	v_add_f32_e32 v210, v164, v210
	v_add_f32_e32 v210, v165, v210
	v_add_f32_e32 v210, v169, v210
	v_add_f32_e32 v210, v171, v210
	v_exp_f32_e32 v216, v220
	v_add_f32_e32 v210, v166, v210
	v_exp_f32_e32 v220, v221
	s_waitcnt lgkmcnt(1)
	v_mfma_f32_32x32x16_bf16 v[80:95], v[228:231], v[120:123], v[80:95]
	v_add_f32_e32 v210, v167, v210
	v_exp_f32_e32 v221, v222
	v_add_f32_e32 v210, v168, v210
	v_exp_f32_e32 v222, v223
	v_add_f32_e32 v210, v170, v210
	v_exp_f32_e32 v223, v224
	v_add_f32_e32 v210, v216, v210
	s_waitcnt lgkmcnt(0)
	v_mfma_f32_32x32x16_bf16 v[64:79], v[232:235], v[120:123], v[64:79]
	ds_read_b128 v[228:231], v199 offset:32768
	ds_read_b128 v[232:235], v199 offset:40960
	v_exp_f32_e32 v212, v212
	v_add_f32_e32 v210, v220, v210
	v_exp_f32_e32 v213, v213
	v_add_f32_e32 v210, v221, v210
	v_exp_f32_e32 v214, v214
	v_add_f32_e32 v210, v222, v210
	s_waitcnt lgkmcnt(1)
	v_mfma_f32_32x32x16_bf16 v[80:95], v[228:231], v[116:119], v[80:95]
	v_exp_f32_e32 v215, v215
	v_add_f32_e32 v210, v223, v210
	v_exp_f32_e32 v217, v217
	v_add_f32_e32 v210, v212, v210
	v_exp_f32_e32 v218, v218
	v_add_f32_e32 v210, v213, v210
	v_exp_f32_e32 v219, v219
	s_waitcnt lgkmcnt(0)
	v_mfma_f32_32x32x16_bf16 v[64:79], v[232:235], v[116:119], v[64:79]
	ds_read_b128 v[228:231], v200 offset:32768
	ds_read_b128 v[232:235], v200 offset:40960
	v_add_f32_e32 v210, v214, v210
	v_exp_f32_e32 v224, v211
	v_add_f32_e32 v210, v215, v210
	v_exp_f32_e32 v225, v225
	v_add_f32_e32 v210, v217, v210
	v_exp_f32_e32 v226, v226
	s_waitcnt lgkmcnt(1)
	v_mfma_f32_32x32x16_bf16 v[80:95], v[228:231], v[112:115], v[80:95]
	v_add_f32_e32 v210, v218, v210
	v_add_f32_e32 v210, v219, v210
	v_add_f32_e32 v210, v224, v210
	v_add_f32_e32 v210, v225, v210
	v_add_f32_e32 v210, v226, v210
	v_add_f32_e32 v210, v227, v210
	v_mov_b32_e32 v211, v210
	s_waitcnt lgkmcnt(0)
	v_mfma_f32_32x32x16_bf16 v[64:79], v[232:235], v[112:115], v[64:79]
	ds_read_b128 v[228:231], v201 offset:32768
	ds_read_b128 v[232:235], v201 offset:40960
	v_cvt_pk_bf16_f32 v160, v160, v161
	v_cvt_pk_bf16_f32 v161, v162, v173
	v_cvt_pk_bf16_f32 v162, v174, v175
	v_cvt_pk_bf16_f32 v163, v163, v172
	v_cvt_pk_bf16_f32 v164, v164, v165
	v_cvt_pk_bf16_f32 v165, v169, v171
	s_waitcnt lgkmcnt(1)
	v_mfma_f32_32x32x16_bf16 v[80:95], v[228:231], v[108:111], v[80:95]
	v_cvt_pk_bf16_f32 v166, v166, v167
	v_cvt_pk_bf16_f32 v167, v168, v170
	v_cvt_pk_bf16_f32 v168, v216, v220
	v_cvt_pk_bf16_f32 v169, v221, v222
	v_cvt_pk_bf16_f32 v170, v223, v212
	v_cvt_pk_bf16_f32 v171, v213, v214
	v_cvt_pk_bf16_f32 v172, v215, v217
	s_waitcnt lgkmcnt(0)
	v_mfma_f32_32x32x16_bf16 v[64:79], v[232:235], v[108:111], v[64:79]
	ds_read_b128 v[228:231], v202 offset:32768
	ds_read_b128 v[232:235], v202 offset:40960
	v_cvt_pk_bf16_f32 v173, v218, v219
	v_cvt_pk_bf16_f32 v174, v224, v225
	v_cvt_pk_bf16_f32 v175, v226, v227
	v_permlane32_swap_b32_e32 v210, v211
	s_waitcnt lgkmcnt(1)
	v_mfma_f32_32x32x16_bf16 v[80:95], v[228:231], v[104:107], v[80:95]
	s_waitcnt lgkmcnt(0)
	v_mfma_f32_32x32x16_bf16 v[64:79], v[232:235], v[104:107], v[64:79]
	ds_read_b128 v[228:231], v203 offset:32768
	ds_read_b128 v[232:235], v203 offset:40960
	s_waitcnt lgkmcnt(1)
	v_mfma_f32_32x32x16_bf16 v[80:95], v[228:231], v[100:103], v[80:95]
	s_waitcnt lgkmcnt(0)
	v_mfma_f32_32x32x16_bf16 v[64:79], v[232:235], v[100:103], v[64:79]
	ds_read_b128 v[228:231], v204 offset:32768
	ds_read_b128 v[232:235], v204 offset:40960
	s_waitcnt lgkmcnt(1)
	v_mfma_f32_32x32x16_bf16 v[80:95], v[228:231], v[96:99], v[80:95]
	s_waitcnt lgkmcnt(0)
	v_mfma_f32_32x32x16_bf16 v[64:79], v[232:235], v[96:99], v[64:79]
	s_cmp_gt_u32 s60, 60
	s_cselect_b64 s[28:29], -1, 0
	s_and_b64 vcc, exec, s[28:29]
	s_cbranch_vccnz .LBB0_2196
	v_add_co_u32_e32 v128, vcc, 0x40760000, v186
	s_nop 1
	v_addc_co_u32_e32 v129, vcc, 0, v187, vcc
	v_add_co_u32_e32 v132, vcc, 0x407a0000, v186
	s_nop 1
	v_addc_co_u32_e32 v133, vcc, 0, v187, vcc
	v_add_co_u32_e32 v136, vcc, 0x49d80000, v184
	global_load_dwordx4 v[128:131], v[128:129], off offset:2560
	s_nop 0
	global_load_dwordx4 v[132:135], v[132:133], off offset:2560
	v_addc_co_u32_e32 v137, vcc, 0, v185, vcc
	v_add_co_u32_e32 v140, vcc, 0x49d84000, v184
	s_nop 1
	v_addc_co_u32_e32 v141, vcc, 0, v185, vcc
	global_load_dwordx4 v[136:139], v[136:137], off offset:512
	s_nop 0
	global_load_dwordx4 v[140:143], v[140:141], off offset:512
.LBB0_2196:
	ds_read_b64_tr_b16 v[184:185], v191 offset:0x0
	ds_read_b64_tr_b16 v[186:187], v191 offset:0x100
	ds_read_b64_tr_b16 v[212:213], v191 offset:0x1000
	ds_read_b64_tr_b16 v[214:215], v191 offset:0x1100
	ds_read_b64_tr_b16 v[216:217], v191 offset:0x2000
	ds_read_b64_tr_b16 v[218:219], v191 offset:0x2100
	ds_read_b64_tr_b16 v[220:221], v191 offset:0x3000
	ds_read_b64_tr_b16 v[222:223], v191 offset:0x3100
	s_waitcnt lgkmcnt(0)
	s_nop 0
	v_mfma_f32_32x32x16_bf16 v[0:15], v[160:163], v[184:187], v[0:15]
	ds_read_b64_tr_b16 v[184:185], v191 offset:0x200
	ds_read_b64_tr_b16 v[186:187], v191 offset:0x300
	v_mfma_f32_32x32x16_bf16 v[0:15], v[164:167], v[212:215], v[0:15]
	ds_read_b64_tr_b16 v[212:213], v191 offset:0x1200
	ds_read_b64_tr_b16 v[214:215], v191 offset:0x1300
	v_mfma_f32_32x32x16_bf16 v[0:15], v[168:171], v[216:219], v[0:15]
	ds_read_b64_tr_b16 v[216:217], v191 offset:0x2200
	ds_read_b64_tr_b16 v[218:219], v191 offset:0x2300
	ds_read_b64_tr_b16 v[224:225], v191 offset:0x3200
	ds_read_b64_tr_b16 v[226:227], v191 offset:0x3300
	s_waitcnt lgkmcnt(0)
	v_mfma_f32_32x32x16_bf16 v[0:15], v[172:175], v[220:223], v[0:15]
	v_mfma_f32_32x32x16_bf16 v[48:63], v[160:163], v[184:187], v[48:63]
	ds_read_b64_tr_b16 v[184:185], v191 offset:0x400
	ds_read_b64_tr_b16 v[186:187], v191 offset:0x500
	v_mfma_f32_32x32x16_bf16 v[48:63], v[164:167], v[212:215], v[48:63]
	ds_read_b64_tr_b16 v[212:213], v191 offset:0x1400
	ds_read_b64_tr_b16 v[214:215], v191 offset:0x1500
	v_mfma_f32_32x32x16_bf16 v[48:63], v[168:171], v[216:219], v[48:63]
	ds_read_b64_tr_b16 v[216:217], v191 offset:0x2400
	ds_read_b64_tr_b16 v[218:219], v191 offset:0x2500
	ds_read_b64_tr_b16 v[220:221], v191 offset:0x3400
	ds_read_b64_tr_b16 v[222:223], v191 offset:0x3500
	s_waitcnt lgkmcnt(0)
	v_mfma_f32_32x32x16_bf16 v[48:63], v[172:175], v[224:227], v[48:63]
	v_mfma_f32_32x32x16_bf16 v[16:31], v[160:163], v[184:187], v[16:31]
	ds_read_b64_tr_b16 v[184:185], v191 offset:0x600
	ds_read_b64_tr_b16 v[186:187], v191 offset:0x700
	v_mfma_f32_32x32x16_bf16 v[16:31], v[164:167], v[212:215], v[16:31]
	ds_read_b64_tr_b16 v[212:213], v191 offset:0x1600
	ds_read_b64_tr_b16 v[214:215], v191 offset:0x1700
	v_mfma_f32_32x32x16_bf16 v[16:31], v[168:171], v[216:219], v[16:31]
	ds_read_b64_tr_b16 v[216:217], v191 offset:0x2600
	ds_read_b64_tr_b16 v[218:219], v191 offset:0x2700
	ds_read_b64_tr_b16 v[224:225], v191 offset:0x3600
	ds_read_b64_tr_b16 v[226:227], v191 offset:0x3700
	s_waitcnt lgkmcnt(0)
	v_mfma_f32_32x32x16_bf16 v[16:31], v[172:175], v[220:223], v[16:31]
	v_mfma_f32_32x32x16_bf16 v[32:47], v[160:163], v[184:187], v[32:47]
	v_max_f32_e32 v220, v81, v81
	v_max_f32_e32 v221, v80, v80
	v_max_f32_e32 v220, v221, v220
	v_max3_f32 v220, v220, v82, v83
	v_max3_f32 v220, v220, v84, v85
	v_max3_f32 v160, v220, v86, v87
	v_max3_f32 v160, v160, v88, v89
	v_max3_f32 v160, v160, v90, v91
	v_mfma_f32_32x32x16_bf16 v[32:47], v[164:167], v[212:215], v[32:47]
	v_max3_f32 v160, v160, v92, v93
	v_max3_f32 v160, v160, v94, v95
	v_max3_f32 v160, v160, v64, v65
	v_max3_f32 v160, v160, v66, v67
	v_max3_f32 v160, v160, v68, v69
	v_max3_f32 v160, v160, v70, v71
	v_max3_f32 v160, v160, v72, v73
	v_max3_f32 v160, v160, v74, v75
	v_mfma_f32_32x32x16_bf16 v[32:47], v[168:171], v[216:219], v[32:47]
	v_max3_f32 v160, v160, v76, v77
	v_max3_f32 v160, v160, v78, v79
	v_mov_b32_e32 v161, v160
	s_nop 1
	v_permlane32_swap_b32_e32 v160, v161
	v_max_f32_e32 v161, v161, v161
	v_max_f32_e32 v160, v160, v160
	v_max_f32_e32 v160, v160, v161
	v_max_f32_e32 v162, v209, v209
	v_sub_f32_e32 v161, v160, v209
	v_max_f32_e32 v160, v162, v160
	v_mfma_f32_32x32x16_bf16 v[32:47], v[172:175], v[224:227], v[32:47]
	v_sub_f32_e32 v162, v209, v160
	v_mul_f32_e32 v162, 0x3e0293ee, v162
	v_exp_f32_e32 v162, v162
	v_cmp_ge_f32_e32 vcc, s9, v161
	s_cmp_eq_u64 vcc, exec
	s_cselect_b64 s[4:5], -1, 0
	s_barrier
	s_waitcnt vmcnt(4)
	v_cndmask_b32_e64 v161, v162, 1.0, s[4:5]
	v_cmp_gt_f32_e32 vcc, 1.0, v161
	s_waitcnt vmcnt(3)
	ds_write_b128 v193, v[144:147] offset:16384
	s_waitcnt vmcnt(2)
	ds_write_b128 v194, v[148:151] offset:16384
	s_waitcnt vmcnt(1)
	ds_write_b128 v195, v[152:155] offset:49152
	s_waitcnt vmcnt(0)
	ds_write_b128 v196, v[156:159] offset:49152
	s_cbranch_vccz .LBB0_2200
	s_and_saveexec_b64 s[38:39], s[2:3]
	ds_write_b32 v179, v161 offset:128
	s_or_b64 exec, exec, s[38:39]
	s_waitcnt lgkmcnt(0)
	v_add_u32_e32 v156, s59, v176
	ds_read_b128 v[144:147], v156 offset:224
	ds_read_b128 v[148:151], v156 offset:192
	ds_read_b128 v[152:155], v156 offset:160
	ds_read_b128 v[156:159], v156 offset:128
	s_waitcnt lgkmcnt(3)
	v_pk_mul_f32 v[12:13], v[12:13], v[144:145]
	s_waitcnt lgkmcnt(2)
	v_pk_mul_f32 v[8:9], v[8:9], v[148:149]
	s_waitcnt lgkmcnt(1)
	v_pk_mul_f32 v[4:5], v[4:5], v[152:153]
	v_pk_mul_f32 v[14:15], v[14:15], v[146:147]
	v_pk_mul_f32 v[10:11], v[10:11], v[150:151]
	v_pk_mul_f32 v[6:7], v[6:7], v[154:155]
	s_waitcnt lgkmcnt(0)
	v_pk_mul_f32 v[2:3], v[2:3], v[158:159]
	v_pk_mul_f32 v[0:1], v[0:1], v[156:157]
	v_pk_mul_f32 v[60:61], v[60:61], v[144:145]
	v_pk_mul_f32 v[56:57], v[56:57], v[148:149]
	v_pk_mul_f32 v[52:53], v[52:53], v[152:153]
	v_pk_mul_f32 v[62:63], v[62:63], v[146:147]
	v_pk_mul_f32 v[58:59], v[58:59], v[150:151]
	v_pk_mul_f32 v[54:55], v[54:55], v[154:155]
	v_pk_mul_f32 v[50:51], v[50:51], v[158:159]
	v_pk_mul_f32 v[48:49], v[48:49], v[156:157]
	v_pk_mul_f32 v[28:29], v[28:29], v[144:145]
	v_pk_mul_f32 v[24:25], v[24:25], v[148:149]
	v_pk_mul_f32 v[20:21], v[20:21], v[152:153]
	v_pk_mul_f32 v[30:31], v[30:31], v[146:147]
	v_pk_mul_f32 v[26:27], v[26:27], v[150:151]
	v_pk_mul_f32 v[22:23], v[22:23], v[154:155]
	v_pk_mul_f32 v[18:19], v[18:19], v[158:159]
	v_pk_mul_f32 v[16:17], v[16:17], v[156:157]
	v_pk_mul_f32 v[44:45], v[44:45], v[144:145]
	v_pk_mul_f32 v[40:41], v[40:41], v[148:149]
	v_pk_mul_f32 v[36:37], v[36:37], v[152:153]
	v_pk_mul_f32 v[46:47], v[46:47], v[146:147]
	v_pk_mul_f32 v[42:43], v[42:43], v[150:151]
	v_pk_mul_f32 v[38:39], v[38:39], v[154:155]
	v_pk_mul_f32 v[34:35], v[34:35], v[158:159]
	v_pk_mul_f32 v[32:33], v[32:33], v[156:157]

.LBB0_2202:
	ds_read_b128 v[64:67], v197 offset:49152
	ds_read_b128 v[68:71], v197 offset:57344
	v_exp_f32_e32 v152, v152
	v_exp_f32_e32 v153, v153
	v_exp_f32_e32 v150, v150
	s_waitcnt lgkmcnt(1)
	v_mfma_f32_32x32x16_bf16 v[80:95], v[64:67], v[124:127], 0
	v_exp_f32_e32 v151, v151
	v_exp_f32_e32 v148, v148
	s_waitcnt lgkmcnt(0)
	v_mfma_f32_32x32x16_bf16 v[64:79], v[68:71], v[124:127], 0
	ds_read_b128 v[124:127], v198 offset:49152
	ds_read_b128 v[128:131], v198 offset:57344
	ds_read_b128 v[132:135], v199 offset:49152
	ds_read_b128 v[136:139], v199 offset:57344
	s_waitcnt lgkmcnt(3)
	v_mfma_f32_32x32x16_bf16 v[80:95], v[124:127], v[120:123], v[80:95]
	ds_read_b128 v[124:127], v200 offset:49152
	ds_read_b128 v[140:143], v200 offset:57344
	ds_read_b128 v[180:183], v201 offset:49152
	ds_read_b128 v[194:197], v201 offset:57344
	ds_read_b128 v[198:201], v202 offset:49152
	ds_read_b128 v[206:209], v202 offset:57344
	ds_read_b128 v[210:213], v203 offset:49152
	ds_read_b128 v[214:217], v203 offset:57344
	s_waitcnt lgkmcnt(10)
	v_mfma_f32_32x32x16_bf16 v[64:79], v[128:131], v[120:123], v[64:79]
	ds_read_b128 v[120:123], v204 offset:49152
	ds_read_b128 v[128:131], v204 offset:57344
	s_waitcnt lgkmcnt(11)
	v_mfma_f32_32x32x16_bf16 v[80:95], v[132:135], v[116:119], v[80:95]
	v_exp_f32_e32 v132, v149
	v_exp_f32_e32 v133, v146
	v_exp_f32_e32 v134, v147
	v_exp_f32_e32 v135, v144
	v_exp_f32_e32 v144, v145
	v_exp_f32_e32 v145, v158
	v_exp_f32_e32 v146, v159
	s_waitcnt lgkmcnt(10)
	v_mfma_f32_32x32x16_bf16 v[64:79], v[136:139], v[116:119], v[64:79]
	v_add_f32_e32 v116, 0, v170
	v_add_f32_e32 v116, v171, v116
	v_add_f32_e32 v116, v172, v116
	v_add_f32_e32 v116, v173, v116
	v_add_f32_e32 v116, v174, v116
	v_add_f32_e32 v116, v184, v116
	v_add_f32_e32 v116, v175, v116
	s_waitcnt lgkmcnt(9)
	v_mfma_f32_32x32x16_bf16 v[80:95], v[124:127], v[112:115], v[80:95]
	v_add_f32_e32 v116, v185, v116
	v_add_f32_e32 v116, v162, v116
	v_add_f32_e32 v116, v163, v116
	v_exp_f32_e32 v118, v156
	v_exp_f32_e32 v119, v157
	v_exp_f32_e32 v136, v154
	v_exp_f32_e32 v137, v155
	s_waitcnt lgkmcnt(8)
	v_mfma_f32_32x32x16_bf16 v[64:79], v[140:143], v[112:115], v[64:79]
	v_add_f32_e32 v112, v164, v116
	v_add_f32_e32 v112, v166, v112
	v_add_f32_e32 v112, v165, v112
	v_add_f32_e32 v112, v167, v112
	v_add_f32_e32 v112, v168, v112
	v_add_f32_e32 v112, v169, v112
	v_add_f32_e32 v112, v152, v112
	s_waitcnt lgkmcnt(7)
	v_mfma_f32_32x32x16_bf16 v[80:95], v[180:183], v[108:111], v[80:95]
	v_add_f32_e32 v112, v153, v112
	v_add_f32_e32 v112, v150, v112
	v_add_f32_e32 v112, v151, v112
	v_add_f32_e32 v112, v148, v112
	v_add_f32_e32 v112, v132, v112
	v_add_f32_e32 v112, v133, v112
	v_add_f32_e32 v112, v134, v112
	s_waitcnt lgkmcnt(6)
	v_mfma_f32_32x32x16_bf16 v[64:79], v[194:197], v[108:111], v[64:79]
	v_add_f32_e32 v108, v135, v112
	v_add_f32_e32 v108, v144, v108
	v_add_f32_e32 v108, v145, v108
	v_add_f32_e32 v108, v146, v108
	v_add_f32_e32 v108, v118, v108
	v_add_f32_e32 v108, v119, v108
	v_add_f32_e32 v108, v136, v108
	s_waitcnt lgkmcnt(5)
	v_mfma_f32_32x32x16_bf16 v[80:95], v[198:201], v[104:107], v[80:95]
	v_add_f32_e32 v108, v137, v108
	v_mov_b32_e32 v109, v108
	s_nop 1
	v_permlane32_swap_b32_e32 v108, v109
	v_cvt_pk_bf16_f32 v110, v170, v171
	v_cvt_pk_bf16_f32 v111, v172, v173
	v_cvt_pk_bf16_f32 v112, v174, v184
	s_waitcnt lgkmcnt(4)
	v_mfma_f32_32x32x16_bf16 v[64:79], v[206:209], v[104:107], v[64:79]
	v_cvt_pk_bf16_f32 v113, v175, v185
	v_cvt_pk_bf16_f32 v104, v162, v163
	v_cvt_pk_bf16_f32 v105, v164, v166
	v_cvt_pk_bf16_f32 v106, v165, v167
	v_cvt_pk_bf16_f32 v107, v168, v169
	v_cvt_pk_bf16_f32 v114, v152, v153
	v_cvt_pk_bf16_f32 v115, v150, v151
	s_waitcnt lgkmcnt(3)
	v_mfma_f32_32x32x16_bf16 v[80:95], v[210:213], v[100:103], v[80:95]
	v_cvt_pk_bf16_f32 v116, v148, v132
	v_cvt_pk_bf16_f32 v117, v133, v134
	s_waitcnt lgkmcnt(2)
	v_mfma_f32_32x32x16_bf16 v[64:79], v[214:217], v[100:103], v[64:79]
	v_cvt_pk_bf16_f32 v100, v135, v144
	v_cvt_pk_bf16_f32 v101, v145, v146
	v_cvt_pk_bf16_f32 v102, v118, v119
	v_cvt_pk_bf16_f32 v103, v136, v137
	s_waitcnt lgkmcnt(1)
	v_mfma_f32_32x32x16_bf16 v[80:95], v[120:123], v[96:99], v[80:95]
	s_waitcnt lgkmcnt(0)
	v_mfma_f32_32x32x16_bf16 v[64:79], v[128:131], v[96:99], v[64:79]
	ds_read_b64_tr_b16 v[96:97], v192 offset:0x0
	ds_read_b64_tr_b16 v[98:99], v192 offset:0x100
	ds_read_b64_tr_b16 v[118:119], v192 offset:0x1000
	ds_read_b64_tr_b16 v[120:121], v192 offset:0x1100
	ds_read_b64_tr_b16 v[122:123], v192 offset:0x2000
	ds_read_b64_tr_b16 v[124:125], v192 offset:0x2100
	ds_read_b64_tr_b16 v[126:127], v192 offset:0x3000
	ds_read_b64_tr_b16 v[128:129], v192 offset:0x3100
	s_waitcnt lgkmcnt(0)
	s_nop 0
	v_mfma_f32_32x32x16_bf16 v[0:15], v[110:113], v[96:99], v[0:15]
	ds_read_b64_tr_b16 v[96:97], v192 offset:0x200
	ds_read_b64_tr_b16 v[98:99], v192 offset:0x300
	v_mfma_f32_32x32x16_bf16 v[0:15], v[104:107], v[118:121], v[0:15]
	ds_read_b64_tr_b16 v[118:119], v192 offset:0x1200
	ds_read_b64_tr_b16 v[120:121], v192 offset:0x1300
	v_mfma_f32_32x32x16_bf16 v[0:15], v[114:117], v[122:125], v[0:15]
	ds_read_b64_tr_b16 v[122:123], v192 offset:0x2200
	ds_read_b64_tr_b16 v[124:125], v192 offset:0x2300
	ds_read_b64_tr_b16 v[130:131], v192 offset:0x3200
	ds_read_b64_tr_b16 v[132:133], v192 offset:0x3300
	s_waitcnt lgkmcnt(0)
	v_mfma_f32_32x32x16_bf16 v[0:15], v[100:103], v[126:129], v[0:15]
	v_mfma_f32_32x32x16_bf16 v[48:63], v[110:113], v[96:99], v[48:63]
	ds_read_b64_tr_b16 v[96:97], v192 offset:0x400
	ds_read_b64_tr_b16 v[98:99], v192 offset:0x500
	v_mfma_f32_32x32x16_bf16 v[48:63], v[104:107], v[118:121], v[48:63]
	ds_read_b64_tr_b16 v[118:119], v192 offset:0x1400
	ds_read_b64_tr_b16 v[120:121], v192 offset:0x1500
	v_mfma_f32_32x32x16_bf16 v[48:63], v[114:117], v[122:125], v[48:63]
	ds_read_b64_tr_b16 v[122:123], v192 offset:0x2400
	ds_read_b64_tr_b16 v[124:125], v192 offset:0x2500
	ds_read_b64_tr_b16 v[126:127], v192 offset:0x3400
	ds_read_b64_tr_b16 v[128:129], v192 offset:0x3500
	s_waitcnt lgkmcnt(0)
	v_mfma_f32_32x32x16_bf16 v[48:63], v[100:103], v[130:133], v[48:63]
	v_mfma_f32_32x32x16_bf16 v[16:31], v[110:113], v[96:99], v[16:31]
	ds_read_b64_tr_b16 v[96:97], v192 offset:0x600
	ds_read_b64_tr_b16 v[98:99], v192 offset:0x700
	v_mfma_f32_32x32x16_bf16 v[16:31], v[104:107], v[118:121], v[16:31]
	ds_read_b64_tr_b16 v[118:119], v192 offset:0x1600
	ds_read_b64_tr_b16 v[120:121], v192 offset:0x1700
	v_mfma_f32_32x32x16_bf16 v[16:31], v[114:117], v[122:125], v[16:31]
	ds_read_b64_tr_b16 v[122:123], v192 offset:0x2600
	ds_read_b64_tr_b16 v[124:125], v192 offset:0x2700
	ds_read_b64_tr_b16 v[130:131], v192 offset:0x3600
	ds_read_b64_tr_b16 v[132:133], v192 offset:0x3700
	s_waitcnt lgkmcnt(0)
	v_mfma_f32_32x32x16_bf16 v[16:31], v[100:103], v[126:129], v[16:31]
	v_mfma_f32_32x32x16_bf16 v[32:47], v[110:113], v[96:99], v[32:47]
	v_max_f32_e32 v126, v81, v81
	v_max_f32_e32 v127, v80, v80
	v_max_f32_e32 v126, v127, v126
	v_max3_f32 v126, v126, v82, v83
	v_max3_f32 v126, v126, v84, v85
	v_max3_f32 v96, v126, v86, v87
	v_max3_f32 v96, v96, v88, v89
	v_max3_f32 v96, v96, v90, v91
	v_mfma_f32_32x32x16_bf16 v[32:47], v[104:107], v[118:121], v[32:47]
	v_max3_f32 v96, v96, v92, v93
	v_max3_f32 v96, v96, v94, v95
	v_max3_f32 v96, v96, v64, v65
	v_max3_f32 v96, v96, v66, v67
	v_max3_f32 v96, v96, v68, v69
	v_max3_f32 v96, v96, v70, v71
	v_max3_f32 v96, v96, v72, v73
	v_max3_f32 v96, v96, v74, v75
	v_mfma_f32_32x32x16_bf16 v[32:47], v[114:117], v[122:125], v[32:47]
	v_max3_f32 v96, v96, v76, v77
	v_max3_f32 v96, v96, v78, v79
	v_mov_b32_e32 v97, v96
	s_nop 1
	v_permlane32_swap_b32_e32 v96, v97
	v_max_f32_e32 v97, v97, v97
	v_max_f32_e32 v96, v96, v96
	v_max_f32_e32 v96, v96, v97
	v_max_f32_e32 v97, v160, v160
	v_max_f32_e32 v97, v97, v96
	v_sub_f32_e32 v98, v96, v160
	v_mfma_f32_32x32x16_bf16 v[32:47], v[100:103], v[130:133], v[32:47]
	v_sub_f32_e32 v96, v160, v97
	v_mul_f32_e32 v96, 0x3e0293ee, v96
	v_exp_f32_e32 v96, v96
	v_cmp_ge_f32_e32 vcc, s9, v98
	s_cmp_eq_u64 vcc, exec
	s_cselect_b64 s[4:5], -1, 0
	v_cndmask_b32_e64 v96, v96, 1.0, s[4:5]
	v_cmp_gt_f32_e32 vcc, 1.0, v96
	s_barrier
	s_cbranch_vccz .LBB0_2206
	s_and_saveexec_b64 s[28:29], s[2:3]
	ds_write_b32 v179, v96 offset:128
	s_or_b64 exec, exec, s[28:29]
	s_waitcnt lgkmcnt(0)
	v_add_u32_e32 v106, s59, v176
	ds_read_b128 v[98:101], v106 offset:224
	ds_read_b128 v[102:105], v106 offset:192
	ds_read_b128 v[110:113], v106 offset:160
	ds_read_b128 v[114:117], v106 offset:128
	s_waitcnt lgkmcnt(3)
	v_pk_mul_f32 v[12:13], v[12:13], v[98:99]
	s_waitcnt lgkmcnt(2)
	v_pk_mul_f32 v[8:9], v[8:9], v[102:103]
	s_waitcnt lgkmcnt(1)
	v_pk_mul_f32 v[4:5], v[4:5], v[110:111]
	v_pk_mul_f32 v[14:15], v[14:15], v[100:101]
	v_pk_mul_f32 v[10:11], v[10:11], v[104:105]
	v_pk_mul_f32 v[6:7], v[6:7], v[112:113]
	s_waitcnt lgkmcnt(0)
	v_pk_mul_f32 v[2:3], v[2:3], v[116:117]
	v_pk_mul_f32 v[0:1], v[0:1], v[114:115]
	v_pk_mul_f32 v[60:61], v[60:61], v[98:99]
	v_pk_mul_f32 v[56:57], v[56:57], v[102:103]
	v_pk_mul_f32 v[52:53], v[52:53], v[110:111]
	v_pk_mul_f32 v[62:63], v[62:63], v[100:101]
	v_pk_mul_f32 v[58:59], v[58:59], v[104:105]
	v_pk_mul_f32 v[54:55], v[54:55], v[112:113]
	v_pk_mul_f32 v[50:51], v[50:51], v[116:117]
	v_pk_mul_f32 v[48:49], v[48:49], v[114:115]
	v_pk_mul_f32 v[28:29], v[28:29], v[98:99]
	v_pk_mul_f32 v[24:25], v[24:25], v[102:103]
	v_pk_mul_f32 v[20:21], v[20:21], v[110:111]
	v_pk_mul_f32 v[30:31], v[30:31], v[100:101]
	v_pk_mul_f32 v[26:27], v[26:27], v[104:105]
	v_pk_mul_f32 v[22:23], v[22:23], v[112:113]
	v_pk_mul_f32 v[18:19], v[18:19], v[116:117]
	v_pk_mul_f32 v[16:17], v[16:17], v[114:115]
	v_pk_mul_f32 v[44:45], v[44:45], v[98:99]
	v_pk_mul_f32 v[40:41], v[40:41], v[102:103]
	v_pk_mul_f32 v[36:37], v[36:37], v[110:111]
	v_pk_mul_f32 v[46:47], v[46:47], v[100:101]
	v_pk_mul_f32 v[42:43], v[42:43], v[104:105]
	v_pk_mul_f32 v[38:39], v[38:39], v[112:113]
	v_pk_mul_f32 v[34:35], v[34:35], v[116:117]
	v_pk_mul_f32 v[32:33], v[32:33], v[114:115]

.LBB0_2221:
	s_and_b64 vcc, exec, s[26:27]
	s_cbranch_vccz .LBB0_2210
	s_ashr_i32 s2, s69, 4
	s_mul_hi_i32 s3, s2, 0x2aaaaaab
	s_load_dwordx2 s[26:27], s[4:5], 0x78
	s_lshr_b32 s4, s3, 31
	s_add_i32 s3, s3, s4
	s_mul_i32 s3, s3, 6
	s_sub_i32 s70, s2, s3
	s_mul_hi_i32 s2, s69, 0x2aaaaaab
	s_lshr_b32 s3, s2, 31
	s_ashr_i32 s2, s2, 4
	s_add_i32 s4, s2, s3
	s_ashr_i32 s5, s4, 31
	s_lshl_b32 s2, s69, 8
	s_lshl_b64 s[30:31], s[4:5], 12
	s_and_b32 s2, s2, 0xf00
	s_or_b32 s30, s30, s2
	s_mul_i32 s2, s31, 0xa00
	s_mul_hi_u32 s3, s30, 0xa00
	s_add_i32 s3, s3, s2
	s_mul_i32 s2, s30, 0xa00
	s_add_u32 s28, s24, s2
	s_mul_i32 s2, s70, 0xc0
	s_addc_u32 s29, s25, s3
	s_ashr_i32 s3, s2, 31
	s_lshl_b64 s[2:3], s[2:3], 1
	s_add_u32 s2, s28, s2
	s_addc_u32 s3, s29, s3
	s_add_u32 s38, s2, 0x4bb60200
	s_addc_u32 s39, s3, 0
	s_mul_i32 s3, s4, 0xc00000
	s_mul_hi_i32 s2, s4, 0xc00000
	s_add_u32 s34, s24, s3
	s_addc_u32 s35, s25, s2
	s_lshl_b32 s2, s70, 8
	s_ashr_i32 s3, s2, 31
	s_lshl_b64 s[28:29], s[2:3], 1
	s_add_u32 s2, s34, s28
	s_addc_u32 s3, s35, s29
	s_waitcnt lgkmcnt(0)
	s_add_u32 s2, s2, 0x4e360200
	s_addc_u32 s3, s3, 0
	v_ashrrev_i32_e32 v53, 4, v52
	v_lshlrev_b32_e32 v24, 3, v52
	s_lshl_b64 s[34:35], s[4:5], 19
	v_and_b32_e32 v62, 0x78, v24
	v_ashrrev_i32_e32 v20, 3, v52
	v_mad_i64_i32 v[0:1], s[42:43], v53, s21, 0
	s_add_u32 s40, s24, s34
	v_add_u32_e32 v25, 32, v53
	v_or_b32_e32 v0, v0, v62
	v_ashrrev_i32_e32 v21, 31, v20
	s_addc_u32 s41, s25, s35
	v_lshlrev_b32_e32 v54, 4, v52
	v_lshl_add_u64 v[4:5], v[0:1], 1, s[2:3]
	v_mad_i64_i32 v[0:1], s[42:43], v25, s21, 0
	v_lshlrev_b64 v[48:49], 7, v[20:21]
	v_or_b32_e32 v0, v0, v62
	v_lshl_add_u64 v[16:17], s[40:41], 0, v[48:49]
	v_and_b32_e32 v58, 0x70, v54
	v_mov_b32_e32 v59, v145
	v_lshl_add_u64 v[12:13], v[0:1], 1, s[2:3]
	v_lshl_add_u64 v[50:51], v[16:17], 0, v[58:59]
	global_load_dwordx4 v[0:3], v[4:5], off offset:256
	s_nop 0
	global_load_dwordx4 v[4:7], v[4:5], off
	s_nop 0
	global_load_dwordx4 v[8:11], v[12:13], off offset:256
	s_nop 0
	global_load_dwordx4 v[12:15], v[12:13], off
	v_add_co_u32_e32 v16, vcc, s33, v50
	v_readfirstlane_b32 s5, v52
	s_nop 0
	v_addc_co_u32_e32 v17, vcc, 0, v51, vcc
	s_ashr_i32 s37, s5, 1
	global_load_dwordx4 v[16:19], v[16:17], off offset:512
	v_mov_b32_e32 v21, s37
	v_bfe_u32 v171, v52, 5, 1
	v_bfi_b32 v21, s17, v21, v52
	v_mov_b64_e32 v[22:23], s[38:39]
	v_mad_i64_i32 v[22:23], s[38:39], v21, s9, v[22:23]
	v_lshlrev_b32_e32 v144, 4, v171
	v_lshl_add_u64 v[22:23], v[22:23], 0, v[144:145]
	global_load_dwordx4 v[140:143], v[22:23], off
	global_load_dwordx4 v[136:139], v[22:23], off offset:32
	global_load_dwordx4 v[132:135], v[22:23], off offset:64
	global_load_dwordx4 v[128:131], v[22:23], off offset:96
	global_load_dwordx4 v[124:127], v[22:23], off offset:128
	global_load_dwordx4 v[120:123], v[22:23], off offset:160
	global_load_dwordx4 v[116:119], v[22:23], off offset:192
	global_load_dwordx4 v[112:115], v[22:23], off offset:224
	global_load_dwordx4 v[108:111], v[22:23], off offset:256
	global_load_dwordx4 v[104:107], v[22:23], off offset:288
	global_load_dwordx4 v[100:103], v[22:23], off offset:320
	global_load_dwordx4 v[96:99], v[22:23], off offset:352
	v_and_b32_e32 v21, 0xfffff0, v53
	v_lshlrev_b32_e32 v22, 1, v53
	v_and_or_b32 v21, v22, 8, v21
	v_lshrrev_b32_e32 v22, 1, v53
	v_lshrrev_b32_e32 v21, 1, v21
	v_bfe_u32 v23, v24, 5, 2
	v_and_b32_e32 v24, 3, v53
	v_and_b32_e32 v27, 0xfffff0, v25
	v_lshlrev_b32_e32 v25, 1, v25
	v_or_b32_e32 v21, v21, v23
	v_and_or_b32 v22, v22, 4, v24
	v_lshlrev_b32_e32 v24, 1, v62
	v_and_or_b32 v25, v25, 8, v27
	v_lshlrev_b32_e32 v21, 9, v21
	v_lshlrev_b32_e32 v22, 6, v22
	v_and_b32_e32 v26, 48, v24
	v_lshrrev_b32_e32 v25, 1, v25
	v_or3_b32 v21, v21, v22, v26
	v_or_b32_e32 v23, v25, v23
	v_lshlrev_b32_e32 v23, 9, v23
	v_add_u32_e32 v175, 0, v21
	v_or3_b32 v22, v23, v22, v26
	s_waitcnt vmcnt(0)
	v_and_b32_e32 v146, 31, v52
	v_add_u32_e32 v176, 0, v22
	v_or_b32_e32 v59, 32, v144
	v_or_b32_e32 v60, 64, v144
	v_or_b32_e32 v61, 0x60, v144
	v_bitop3_b32 v63, v144, v58, s52 bitop3:0x36
	v_bitop3_b32 v64, v144, v58, s53 bitop3:0x36
	v_bitop3_b32 v65, v144, v58, s16 bitop3:0x36
	v_bitop3_b32 v66, v144, v58, s54 bitop3:0x36
	v_bitop3_b32 v67, v144, v58, s0 bitop3:0x36
	v_and_b32_e32 v74, 63, v52
	v_bitop3_b32 v68, v144, v58, s55 bitop3:0x36
	v_bitop3_b32 v70, v144, v58, s56 bitop3:0x36
	v_bitop3_b32 v71, v144, v58, s57 bitop3:0x36
	s_and_b32 s71, s37, 0xffffffe0
	s_mov_b32 s37, s36
	s_mov_b32 s38, s36
	s_mov_b32 s39, s36
	s_mov_b32 s40, s36
	s_mov_b32 s41, s36
	s_mov_b32 s42, s36
	s_mov_b32 s43, s36
	s_mov_b32 s44, s36
	s_mov_b32 s45, s36
	s_mov_b32 s46, s36
	s_mov_b32 s47, s36
	s_mov_b32 s48, s36
	s_mov_b32 s49, s36
	s_mov_b32 s50, s36
	s_mov_b32 s51, s36
	v_add_co_u32_e32 v50, vcc, s59, v50
	s_and_b32 s5, s5, 0x3fffffc0
	s_nop 0
	v_addc_co_u32_e32 v51, vcc, 0, v51, vcc
	s_lshl_b32 s5, s5, 2
	s_waitcnt vmcnt(16)
	ds_write_b128 v175, v[0:3]
	v_mul_lo_u32 v0, v53, s1
	v_bitop3_b32 v1, v24, v52, s23 bitop3:0x78
	v_lshlrev_b32_e32 v2, 4, v20
	v_add3_u32 v177, v1, v0, 0
	v_mul_lo_u32 v0, v20, s1
	v_or_b32_e32 v1, 0x100, v58
	v_and_b32_e32 v2, 0x70, v2
	s_waitcnt vmcnt(14)
	ds_write_b128 v176, v[8:11]
	v_xad_u32 v0, v1, v2, v0
	v_mul_u32_u24_e32 v8, 0x180, v146
	v_add_u32_e32 v178, 0, v0
	v_bitop3_b32 v0, v144, v8, v58 bitop3:0xde
	v_add_u32_e32 v179, 0, v0
	ds_write_b128 v177, v[4:7] offset:32768
	s_waitcnt vmcnt(13)
	ds_write_b128 v177, v[12:15] offset:45056
	s_waitcnt vmcnt(12)
	ds_write_b128 v178, v[16:19] offset:32768
	s_waitcnt lgkmcnt(0)
	s_barrier
	ds_read_b128 v[0:3], v179 offset:32768
	ds_read_b128 v[4:7], v179 offset:45056
	s_waitcnt vmcnt(11) lgkmcnt(1)
	v_mfma_f32_32x32x16_bf16 v[32:47], v[0:3], v[140:143], 0
	v_bitop3_b32 v0, v59, v8, v58 bitop3:0xde
	v_add_u32_e32 v180, 0, v0
	s_add_i32 s72, s5, 0
	s_add_i32 s72, s72, 0x14000
	s_cmp_lg_u32 0, -1
	s_cselect_b32 s5, 0, 0
	v_lshl_add_u64 v[150:151], s[34:35], 0, v[48:49]
	s_waitcnt lgkmcnt(0)
	v_mfma_f32_32x32x16_bf16 v[16:31], v[4:7], v[140:143], 0
	ds_read_b128 v[0:3], v180 offset:32768
	ds_read_b128 v[4:7], v180 offset:45056
	v_add_u32_e32 v191, 0x3000, v177
	s_mov_b32 s73, -1
	v_lshl_add_u32 v147, v146, 2, s72
	v_mov_b32_e32 v172, 0
	s_waitcnt vmcnt(10) lgkmcnt(1)
	v_mfma_f32_32x32x16_bf16 v[32:47], v[0:3], v[136:139], v[32:47]
	v_bitop3_b32 v0, v60, v8, v58 bitop3:0xde
	v_add_u32_e32 v181, 0, v0
	s_waitcnt lgkmcnt(0)
	v_mfma_f32_32x32x16_bf16 v[16:31], v[4:7], v[136:139], v[16:31]
	ds_read_b128 v[0:3], v181 offset:32768
	ds_read_b128 v[4:7], v181 offset:45056
	s_waitcnt vmcnt(9) lgkmcnt(1)
	v_mfma_f32_32x32x16_bf16 v[32:47], v[0:3], v[132:135], v[32:47]
	v_bitop3_b32 v0, v61, v8, v58 bitop3:0xde
	v_add_u32_e32 v182, 0, v0
	v_lshlrev_b32_e32 v8, 3, v74
	s_waitcnt lgkmcnt(0)
	v_mfma_f32_32x32x16_bf16 v[16:31], v[4:7], v[132:135], v[16:31]
	ds_read_b128 v[0:3], v182 offset:32768
	ds_read_b128 v[4:7], v182 offset:45056
	s_waitcnt vmcnt(8) lgkmcnt(1)
	v_mfma_f32_32x32x16_bf16 v[32:47], v[0:3], v[128:131], v[32:47]
	v_mad_u32_u24 v0, v146, s1, v63
	v_add_u32_e32 v183, 0, v0
	s_waitcnt lgkmcnt(0)
	v_mfma_f32_32x32x16_bf16 v[16:31], v[4:7], v[128:131], v[16:31]
	ds_read_b128 v[0:3], v183 offset:32768
	ds_read_b128 v[4:7], v183 offset:45056
	s_waitcnt vmcnt(7) lgkmcnt(1)
	v_mfma_f32_32x32x16_bf16 v[32:47], v[0:3], v[124:127], v[32:47]
	v_mad_u32_u24 v0, v146, s1, v64
	v_add_u32_e32 v184, 0, v0
	s_waitcnt lgkmcnt(0)
	v_mfma_f32_32x32x16_bf16 v[16:31], v[4:7], v[124:127], v[16:31]
	ds_read_b128 v[0:3], v184 offset:32768
	ds_read_b128 v[4:7], v184 offset:45056
	s_waitcnt vmcnt(6) lgkmcnt(1)
	v_mfma_f32_32x32x16_bf16 v[32:47], v[0:3], v[120:123], v[32:47]
	v_mad_u32_u24 v0, v146, s1, v65
	v_add_u32_e32 v185, 0, v0
	s_waitcnt lgkmcnt(0)
	v_mfma_f32_32x32x16_bf16 v[16:31], v[4:7], v[120:123], v[16:31]
	ds_read_b128 v[0:3], v185 offset:32768
	ds_read_b128 v[4:7], v185 offset:45056
	s_waitcnt vmcnt(5) lgkmcnt(1)
	v_mfma_f32_32x32x16_bf16 v[32:47], v[0:3], v[116:119], v[32:47]
	v_mad_u32_u24 v0, v146, s1, v66
	v_add_u32_e32 v186, 0, v0
	ds_read_b128 v[0:3], v186 offset:32768
	s_waitcnt lgkmcnt(1)
	v_mfma_f32_32x32x16_bf16 v[16:31], v[4:7], v[116:119], v[16:31]
	ds_read_b128 v[4:7], v186 offset:45056
	s_waitcnt vmcnt(4) lgkmcnt(1)
	v_mfma_f32_32x32x16_bf16 v[32:47], v[0:3], v[112:115], v[32:47]
	v_mad_u32_u24 v0, v146, s1, v67
	v_add_u32_e32 v187, 0, v0
	ds_read_b128 v[0:3], v187 offset:32768
	s_waitcnt lgkmcnt(1)
	v_mfma_f32_32x32x16_bf16 v[16:31], v[4:7], v[112:115], v[16:31]
	v_and_b32_e32 v4, 0xc0, v54
	v_lshlrev_b32_e32 v5, 1, v52
	v_and_or_b32 v4, v8, 24, v4
	v_and_b32_e32 v5, 32, v5
	v_lshlrev_b32_e32 v6, 3, v8
	v_and_b32_e32 v6, 0x800, v6
	v_or3_b32 v75, v4, v5, v6
	ds_read_b128 v[4:7], v187 offset:45056
	s_waitcnt vmcnt(3) lgkmcnt(1)
	v_mfma_f32_32x32x16_bf16 v[32:47], v[0:3], v[108:111], v[32:47]
	v_mad_u32_u24 v0, v146, s1, v68
	v_add_u32_e32 v188, 0, v0
	ds_read_b128 v[0:3], v188 offset:32768
	v_add_u32_e32 v174, s5, v75
	s_waitcnt lgkmcnt(1)
	v_mfma_f32_32x32x16_bf16 v[16:31], v[4:7], v[108:111], v[16:31]
	v_mov_b32_e32 v4, 0x3000
	v_mad_u32_u24 v69, v146, s1, v4
	ds_read_b128 v[4:7], v188 offset:45056
	v_bitop3_b32 v76, v144, v69, v58 bitop3:0xde
	v_bitop3_b32 v77, v59, v69, v58 bitop3:0xde
	v_bitop3_b32 v78, v60, v69, v58 bitop3:0xde
	v_bitop3_b32 v79, v61, v69, v58 bitop3:0xde
	s_waitcnt vmcnt(2) lgkmcnt(1)
	v_mfma_f32_32x32x16_bf16 v[32:47], v[0:3], v[104:107], v[32:47]
	v_mad_u32_u24 v0, v146, s1, v70
	v_add_u32_e32 v189, 0, v0
	ds_read_b128 v[0:3], v189 offset:32768
	v_add_u32_e32 v83, v66, v69
	v_add_u32_e32 v84, v67, v69
	v_add_u32_e32 v80, v63, v69
	v_add_u32_e32 v81, v64, v69
	s_waitcnt lgkmcnt(1)
	v_mfma_f32_32x32x16_bf16 v[16:31], v[4:7], v[104:107], v[16:31]
	ds_read_b128 v[4:7], v189 offset:45056
	v_add_u32_e32 v82, v65, v69
	v_add_u32_e32 v85, v68, v69
	v_add_u32_e32 v86, v70, v69
	v_add_u32_e32 v87, v71, v69
	v_add_u32_e32 v203, 0, v76
	v_add_u32_e32 v204, 0, v77
	s_waitcnt vmcnt(1) lgkmcnt(1)
	v_mfma_f32_32x32x16_bf16 v[32:47], v[0:3], v[100:103], v[32:47]
	v_mad_u32_u24 v0, v146, s1, v71
	v_add_u32_e32 v190, 0, v0
	ds_read_b128 v[54:57], v190 offset:32768
	ds_read_b128 v[58:61], v190 offset:45056
	v_add_u32_e32 v201, 0, v78
	v_add_u32_e32 v202, 0, v79
	v_add_u32_e32 v199, 0, v80
	s_waitcnt lgkmcnt(2)
	v_mfma_f32_32x32x16_bf16 v[16:31], v[4:7], v[100:103], v[16:31]
	v_mov_b64_e32 v[0:1], s[36:37]
	v_mov_b64_e32 v[2:3], s[38:39]
	v_mov_b64_e32 v[4:5], s[40:41]
	v_mov_b64_e32 v[6:7], s[42:43]
	v_mov_b64_e32 v[8:9], s[44:45]
	v_mov_b64_e32 v[10:11], s[46:47]
	v_mov_b64_e32 v[12:13], s[48:49]
	s_waitcnt vmcnt(0) lgkmcnt(1)
	v_mfma_f32_32x32x16_bf16 v[32:47], v[54:57], v[96:99], v[32:47]
	v_add_u32_e32 v54, 64, v53
	v_mov_b64_e32 v[14:15], s[50:51]
	v_mad_i64_i32 v[54:55], s[38:39], v54, s21, 0
	v_or_b32_e32 v54, v54, v62
	v_add_u32_e32 v200, 0, v81
	v_add_u32_e32 v197, 0, v82
	s_waitcnt lgkmcnt(0)
	v_mfma_f32_32x32x16_bf16 v[16:31], v[58:61], v[96:99], v[16:31]
	v_lshl_add_u64 v[58:59], v[54:55], 1, s[2:3]
	v_add_u32_e32 v54, 0x60, v53
	v_mad_i64_i32 v[54:55], s[38:39], v54, s21, 0
	v_or_b32_e32 v54, v54, v62
	v_lshl_add_u64 v[66:67], v[54:55], 1, s[2:3]
	global_load_dwordx4 v[54:57], v[58:59], off offset:256
	s_nop 0
	global_load_dwordx4 v[58:61], v[58:59], off
	s_nop 0
	global_load_dwordx4 v[62:65], v[66:67], off offset:256
	s_nop 0
	global_load_dwordx4 v[66:69], v[66:67], off
	v_max_f32_e32 v88, v33, v33
	global_load_dwordx4 v[70:73], v[50:51], off offset:512
	v_max_f32_e32 v89, v32, v32
	v_max_f32_e32 v50, v89, v88
	v_max3_f32 v50, v50, v34, v35
	v_max3_f32 v50, v50, v36, v37
	v_max3_f32 v50, v50, v38, v39
	v_max3_f32 v50, v50, v40, v41
	v_max3_f32 v50, v50, v42, v43
	v_max3_f32 v50, v50, v44, v45
	v_max3_f32 v50, v50, v46, v47
	v_max3_f32 v50, v50, v16, v17
	v_max3_f32 v50, v50, v18, v19
	v_max3_f32 v50, v50, v20, v21
	v_max3_f32 v50, v50, v22, v23
	v_max3_f32 v50, v50, v24, v25
	v_max3_f32 v50, v50, v26, v27
	v_max3_f32 v50, v50, v28, v29
	v_max3_f32 v50, v50, v30, v31
	v_mov_b32_e32 v51, v50
	s_nop 1
	v_permlane32_swap_b32_e32 v50, v51
	v_max_f32_e32 v51, v51, v51
	v_max_f32_e32 v50, v50, v50
	v_max_f32_e32 v50, v50, v51
	v_add_f32_e32 v51, 0x7149f2ca, v50
	v_max_f32_e32 v50, 0xf149f2ca, v50
	v_cmp_ge_f32_e32 vcc, s58, v51
	v_sub_f32_e32 v51, 0xf149f2ca, v50
	v_mul_f32_e32 v51, 0x3dd53b94, v51
	v_exp_f32_e32 v51, v51
	s_cmp_eq_u64 vcc, exec
	s_cselect_b64 vcc, -1, 0
	v_mov_b32_e32 v88, 0xf149f2ca
	v_cndmask_b32_e32 v205, v50, v88, vcc
	v_mul_f32_e32 v50, 0xbdd53b94, v205
	v_cndmask_b32_e64 v196, v51, 1.0, vcc
	v_mov_b32_e32 v51, v50
	v_fmac_f32_e32 v51, 0x3dd53b94, v47
	v_pk_fma_f32 v[162:163], v[16:17], s[8:9], v[50:51] op_sel_hi:[1,0,0]
	s_addk_i32 s5, 0x4000
	v_mad_i64_i32 v[16:17], s[38:39], v53, s60, 0
	v_fmamk_f32 v32, v32, 0x3dd53b94, v50
	v_fmamk_f32 v33, v33, 0x3dd53b94, v50
	v_fmamk_f32 v34, v34, 0x3dd53b94, v50
	v_fmamk_f32 v35, v35, 0x3dd53b94, v50
	v_fmamk_f32 v36, v36, 0x3dd53b94, v50
	v_fmamk_f32 v37, v37, 0x3dd53b94, v50
	v_fmamk_f32 v38, v38, 0x3dd53b94, v50
	v_fmamk_f32 v39, v39, 0x3dd53b94, v50
	v_fmamk_f32 v40, v40, 0x3dd53b94, v50
	v_fmamk_f32 v41, v41, 0x3dd53b94, v50
	v_fmamk_f32 v42, v42, 0x3dd53b94, v50
	v_fmamk_f32 v43, v43, 0x3dd53b94, v50
	v_fmamk_f32 v44, v44, 0x3dd53b94, v50
	v_fmamk_f32 v45, v45, 0x3dd53b94, v50
	v_fmamk_f32 v46, v46, 0x3dd53b94, v50
	v_pk_fma_f32 v[160:161], v[18:19], s[8:9], v[50:51] op_sel_hi:[1,0,0]
	v_add_u32_e32 v173, s5, v75
	v_mad_i64_i32 v[16:17], s[4:5], s4, v170, v[16:17]
	v_and_b32_e32 v18, 15, v52
	v_exp_f32_e32 v219, v32
	v_exp_f32_e32 v220, v33
	v_exp_f32_e32 v221, v34
	v_exp_f32_e32 v223, v35
	v_exp_f32_e32 v224, v36
	v_exp_f32_e32 v226, v37
	v_exp_f32_e32 v222, v38
	v_exp_f32_e32 v225, v39
	v_exp_f32_e32 v210, v40
	v_exp_f32_e32 v212, v41
	v_exp_f32_e32 v213, v42
	v_exp_f32_e32 v217, v43
	v_exp_f32_e32 v211, v44
	v_exp_f32_e32 v214, v45
	v_exp_f32_e32 v215, v46
	v_exp_f32_e32 v218, v51
	v_lshl_or_b32 v16, v18, 4, v16
	s_waitcnt vmcnt(0)
	v_lshl_add_u64 v[148:149], v[16:17], 0, s[28:29]
	v_and_b32_e32 v16, 7, v52
	v_pk_fma_f32 v[158:159], v[30:31], s[8:9], v[50:51] op_sel_hi:[1,0,0]
	v_pk_fma_f32 v[164:165], v[28:29], s[8:9], v[50:51] op_sel_hi:[1,0,0]
	v_pk_fma_f32 v[166:167], v[26:27], s[8:9], v[50:51] op_sel_hi:[1,0,0]
	v_pk_fma_f32 v[152:153], v[24:25], s[8:9], v[50:51] op_sel_hi:[1,0,0]
	v_pk_fma_f32 v[154:155], v[22:23], s[8:9], v[50:51] op_sel_hi:[1,0,0]
	v_pk_fma_f32 v[156:157], v[20:21], s[8:9], v[50:51] op_sel_hi:[1,0,0]
	s_waitcnt vmcnt(4)
	ds_write_b128 v175, v[54:57] offset:16384
	s_waitcnt vmcnt(2)
	ds_write_b128 v176, v[62:65] offset:16384
	ds_write_b128 v177, v[58:61] offset:57344
	s_waitcnt vmcnt(1)
	ds_write_b128 v191, v[66:69] offset:57344
	s_waitcnt vmcnt(0)
	ds_write_b128 v178, v[70:73] offset:57344
	v_lshl_or_b32 v150, v16, 4, v150
	v_mov_b64_e32 v[62:63], v[14:15]
	v_mov_b64_e32 v[30:31], v[14:15]
	v_mov_b64_e32 v[46:47], v[14:15]
	v_cmp_gt_u32_e64 s[2:3], 32, v74
	v_add_u32_e32 v198, 0, v83
	v_add_u32_e32 v194, 0, v84
	v_add_u32_e32 v195, 0, v85
	v_add_u32_e32 v192, 0, v86
	v_add_u32_e32 v193, 0, v87
	v_mov_b64_e32 v[60:61], v[12:13]
	v_mov_b64_e32 v[58:59], v[10:11]
	v_mov_b64_e32 v[56:57], v[8:9]
	v_mov_b64_e32 v[54:55], v[6:7]
	v_mov_b64_e32 v[52:53], v[4:5]
	v_mov_b64_e32 v[50:51], v[2:3]
	v_mov_b64_e32 v[48:49], v[0:1]
	v_mov_b64_e32 v[28:29], v[12:13]
	v_mov_b64_e32 v[26:27], v[10:11]
	v_mov_b64_e32 v[24:25], v[8:9]
	v_mov_b64_e32 v[22:23], v[6:7]
	v_mov_b64_e32 v[20:21], v[4:5]
	v_mov_b64_e32 v[18:19], v[2:3]
	v_mov_b64_e32 v[16:17], v[0:1]
	v_mov_b64_e32 v[44:45], v[12:13]
	v_mov_b64_e32 v[42:43], v[10:11]
	v_mov_b64_e32 v[40:41], v[8:9]
	v_mov_b64_e32 v[38:39], v[6:7]
	v_mov_b64_e32 v[36:37], v[4:5]
	v_mov_b64_e32 v[34:35], v[2:3]
	v_mov_b64_e32 v[32:33], v[0:1]
	s_waitcnt lgkmcnt(0)
	s_barrier
.LBB0_2223:
	ds_read_b128 v[64:67], v179 offset:57344
	ds_read_b128 v[68:71], v203 offset:57344
	ds_read_b128 v[206:209], v180 offset:57344
	ds_read_b128 v[228:231], v204 offset:57344
	v_exp_f32_e32 v216, v156
	v_add_f32_e32 v156, 0, v219
	s_waitcnt lgkmcnt(3)
	v_mfma_f32_32x32x16_bf16 v[80:95], v[64:67], v[140:143], 0
	v_add_f32_e32 v156, v220, v156
	v_add_f32_e32 v156, v221, v156
	v_add_f32_e32 v156, v223, v156
	v_add_f32_e32 v156, v224, v156
	v_add_f32_e32 v156, v226, v156
	v_add_f32_e32 v156, v222, v156
	v_add_f32_e32 v156, v225, v156
	s_waitcnt lgkmcnt(2)
	v_mfma_f32_32x32x16_bf16 v[64:79], v[68:71], v[140:143], 0
	v_add_f32_e32 v156, v210, v156
	v_add_f32_e32 v156, v212, v156
	v_add_f32_e32 v156, v213, v156
	v_add_f32_e32 v156, v217, v156
	v_exp_f32_e32 v168, v162
	v_add_f32_e32 v156, v211, v156
	v_exp_f32_e32 v169, v163
	s_waitcnt lgkmcnt(1)
	v_mfma_f32_32x32x16_bf16 v[80:95], v[206:209], v[136:139], v[80:95]
	v_add_f32_e32 v156, v214, v156
	v_add_f32_e32 v156, v215, v156
	v_add_f32_e32 v156, v218, v156
	v_add_f32_e32 v156, v168, v156
	v_exp_f32_e32 v227, v157
	v_add_f32_e32 v156, v169, v156
	v_exp_f32_e32 v154, v154
	s_waitcnt lgkmcnt(0)
	v_mfma_f32_32x32x16_bf16 v[64:79], v[228:231], v[136:139], v[64:79]
	ds_read_b128 v[206:209], v181 offset:57344
	ds_read_b128 v[228:231], v201 offset:57344
	v_exp_f32_e32 v155, v155
	v_exp_f32_e32 v152, v152
	v_exp_f32_e32 v153, v153
	v_exp_f32_e32 v232, v158
	v_exp_f32_e32 v233, v159
	v_cvt_pk_bf16_f32 v158, v224, v226
	s_waitcnt lgkmcnt(1)
	v_mfma_f32_32x32x16_bf16 v[80:95], v[206:209], v[132:135], v[80:95]
	v_cvt_pk_bf16_f32 v162, v211, v214
	v_cvt_pk_bf16_f32 v211, v232, v233
	v_cvt_pk_bf16_f32 v157, v221, v223
	v_cvt_pk_bf16_f32 v159, v222, v225
	v_cvt_pk_bf16_f32 v163, v215, v218
	s_waitcnt lgkmcnt(0)
	v_mfma_f32_32x32x16_bf16 v[64:79], v[228:231], v[132:135], v[64:79]
	ds_read_b128 v[206:209], v182 offset:57344
	ds_read_b128 v[228:231], v202 offset:57344
	s_waitcnt lgkmcnt(1)
	v_mfma_f32_32x32x16_bf16 v[80:95], v[206:209], v[128:131], v[80:95]
	s_waitcnt lgkmcnt(0)
	v_mfma_f32_32x32x16_bf16 v[64:79], v[228:231], v[128:131], v[64:79]
	ds_read_b128 v[206:209], v183 offset:57344
	ds_read_b128 v[228:231], v199 offset:57344
	s_waitcnt lgkmcnt(1)
	v_mfma_f32_32x32x16_bf16 v[80:95], v[206:209], v[124:127], v[80:95]
	s_waitcnt lgkmcnt(0)
	v_mfma_f32_32x32x16_bf16 v[64:79], v[228:231], v[124:127], v[64:79]
	ds_read_b128 v[206:209], v184 offset:57344
	ds_read_b128 v[228:231], v200 offset:57344
	s_waitcnt lgkmcnt(1)
	v_mfma_f32_32x32x16_bf16 v[80:95], v[206:209], v[120:123], v[80:95]
	s_waitcnt lgkmcnt(0)
	v_mfma_f32_32x32x16_bf16 v[64:79], v[228:231], v[120:123], v[64:79]
	ds_read_b128 v[206:209], v185 offset:57344
	ds_read_b128 v[228:231], v197 offset:57344
	s_waitcnt lgkmcnt(1)
	v_mfma_f32_32x32x16_bf16 v[80:95], v[206:209], v[116:119], v[80:95]
	s_waitcnt lgkmcnt(0)
	v_mfma_f32_32x32x16_bf16 v[64:79], v[228:231], v[116:119], v[64:79]
	ds_read_b128 v[206:209], v186 offset:57344
	ds_read_b128 v[228:231], v198 offset:57344
	s_waitcnt lgkmcnt(1)
	v_mfma_f32_32x32x16_bf16 v[80:95], v[206:209], v[112:115], v[80:95]
	s_waitcnt lgkmcnt(0)
	v_mfma_f32_32x32x16_bf16 v[64:79], v[228:231], v[112:115], v[64:79]
	ds_read_b128 v[206:209], v187 offset:57344
	ds_read_b128 v[228:231], v194 offset:57344
	s_waitcnt lgkmcnt(1)
	v_mfma_f32_32x32x16_bf16 v[80:95], v[206:209], v[108:111], v[80:95]
	s_waitcnt lgkmcnt(0)
	v_mfma_f32_32x32x16_bf16 v[64:79], v[228:231], v[108:111], v[64:79]
	ds_read_b128 v[206:209], v188 offset:57344
	ds_read_b128 v[228:231], v195 offset:57344
	s_waitcnt lgkmcnt(1)
	v_mfma_f32_32x32x16_bf16 v[80:95], v[206:209], v[104:107], v[80:95]
	s_waitcnt lgkmcnt(0)
	v_mfma_f32_32x32x16_bf16 v[64:79], v[228:231], v[104:107], v[64:79]
	ds_read_b128 v[206:209], v189 offset:57344
	ds_read_b128 v[228:231], v192 offset:57344
	s_waitcnt lgkmcnt(1)
	v_mfma_f32_32x32x16_bf16 v[80:95], v[206:209], v[100:103], v[80:95]
	s_waitcnt lgkmcnt(0)
	v_mfma_f32_32x32x16_bf16 v[64:79], v[228:231], v[100:103], v[64:79]
	ds_read_b128 v[206:209], v190 offset:57344
	ds_read_b128 v[228:231], v193 offset:57344
	s_waitcnt lgkmcnt(1)
	v_mfma_f32_32x32x16_bf16 v[80:95], v[206:209], v[96:99], v[80:95]
	v_exp_f32_e32 v208, v160
	v_exp_f32_e32 v209, v161
	v_cvt_pk_bf16_f32 v160, v210, v212
	v_cvt_pk_bf16_f32 v161, v213, v217
	v_add_f32_e32 v156, v208, v156
	v_add_f32_e32 v156, v209, v156
	v_add_f32_e32 v156, v216, v156
	v_add_f32_e32 v156, v227, v156
	s_waitcnt lgkmcnt(0)
	v_mfma_f32_32x32x16_bf16 v[64:79], v[228:231], v[96:99], v[64:79]
	v_exp_f32_e32 v228, v166
	v_add_f32_e32 v156, v154, v156
	v_exp_f32_e32 v229, v167
	v_add_f32_e32 v156, v155, v156
	v_exp_f32_e32 v230, v164
	v_add_f32_e32 v156, v152, v156
	v_exp_f32_e32 v231, v165
	v_add_f32_e32 v156, v153, v156
	v_add_f32_e32 v156, v228, v156
	v_add_f32_e32 v156, v229, v156
	v_add_f32_e32 v156, v230, v156
	v_add_f32_e32 v156, v231, v156
	v_add_f32_e32 v156, v232, v156
	v_add_f32_e32 v206, v233, v156
	v_mov_b32_e32 v207, v206
	v_cvt_pk_bf16_f32 v156, v219, v220
	v_cvt_pk_bf16_f32 v165, v208, v209
	v_cvt_pk_bf16_f32 v209, v228, v229
	v_permlane32_swap_b32_e32 v206, v207
	v_cvt_pk_bf16_f32 v164, v168, v169
	v_cvt_pk_bf16_f32 v166, v216, v227
	v_cvt_pk_bf16_f32 v167, v154, v155
	v_cvt_pk_bf16_f32 v208, v152, v153
	v_cvt_pk_bf16_f32 v210, v230, v231
	v_lshl_add_u64 v[152:153], s[24:25], 0, v[148:149]
	v_add_co_u32_e32 v154, vcc, s61, v152
	s_nop 1
	v_addc_co_u32_e32 v155, vcc, 0, v153, vcc
	v_add_co_u32_e32 v168, vcc, s62, v152
	s_nop 1
	v_addc_co_u32_e32 v169, vcc, 0, v153, vcc
	global_load_dwordx4 v[212:215], v[154:155], off offset:768
	global_load_dwordx4 v[216:219], v[154:155], off offset:512
	global_load_dwordx4 v[220:223], v[168:169], off offset:768
	global_load_dwordx4 v[224:227], v[168:169], off offset:512
	v_lshl_add_u64 v[154:155], s[24:25], 0, v[150:151]
	v_add_co_u32_e32 v168, vcc, s63, v154
	s_nop 1
	v_addc_co_u32_e32 v169, vcc, 0, v155, vcc
	global_load_dwordx4 v[228:231], v[168:169], off offset:512
	ds_read_b64_tr_b16 v[232:233], v174 offset:0x0
	ds_read_b64_tr_b16 v[234:235], v174 offset:0x100
	ds_read_b64_tr_b16 v[236:237], v174 offset:0x1000
	ds_read_b64_tr_b16 v[238:239], v174 offset:0x1100
	ds_read_b64_tr_b16 v[240:241], v174 offset:0x2000
	ds_read_b64_tr_b16 v[242:243], v174 offset:0x2100
	ds_read_b64_tr_b16 v[244:245], v174 offset:0x3000
	ds_read_b64_tr_b16 v[246:247], v174 offset:0x3100
	s_waitcnt lgkmcnt(0)
	s_nop 0
	v_mfma_f32_32x32x16_bf16 v[0:15], v[156:159], v[232:235], v[0:15]
	ds_read_b64_tr_b16 v[232:233], v174 offset:0x200
	ds_read_b64_tr_b16 v[234:235], v174 offset:0x300
	v_mfma_f32_32x32x16_bf16 v[0:15], v[160:163], v[236:239], v[0:15]
	ds_read_b64_tr_b16 v[236:237], v174 offset:0x1200
	ds_read_b64_tr_b16 v[238:239], v174 offset:0x1300
	v_mfma_f32_32x32x16_bf16 v[0:15], v[164:167], v[240:243], v[0:15]
	ds_read_b64_tr_b16 v[240:241], v174 offset:0x2200
	ds_read_b64_tr_b16 v[242:243], v174 offset:0x2300
	ds_read_b64_tr_b16 v[248:249], v174 offset:0x3200
	ds_read_b64_tr_b16 v[250:251], v174 offset:0x3300
	s_waitcnt lgkmcnt(0)
	v_mfma_f32_32x32x16_bf16 v[0:15], v[208:211], v[244:247], v[0:15]
	v_mfma_f32_32x32x16_bf16 v[48:63], v[156:159], v[232:235], v[48:63]
	ds_read_b64_tr_b16 v[232:233], v174 offset:0x400
	ds_read_b64_tr_b16 v[234:235], v174 offset:0x500
	v_mfma_f32_32x32x16_bf16 v[48:63], v[160:163], v[236:239], v[48:63]
	ds_read_b64_tr_b16 v[236:237], v174 offset:0x1400
	ds_read_b64_tr_b16 v[238:239], v174 offset:0x1500
	v_mfma_f32_32x32x16_bf16 v[48:63], v[164:167], v[240:243], v[48:63]
	ds_read_b64_tr_b16 v[240:241], v174 offset:0x2400
	ds_read_b64_tr_b16 v[242:243], v174 offset:0x2500
	ds_read_b64_tr_b16 v[244:245], v174 offset:0x3400
	ds_read_b64_tr_b16 v[246:247], v174 offset:0x3500
	s_waitcnt lgkmcnt(0)
	v_mfma_f32_32x32x16_bf16 v[48:63], v[208:211], v[248:251], v[48:63]
	v_mfma_f32_32x32x16_bf16 v[16:31], v[156:159], v[232:235], v[16:31]
	ds_read_b64_tr_b16 v[232:233], v174 offset:0x600
	ds_read_b64_tr_b16 v[234:235], v174 offset:0x700
	v_mfma_f32_32x32x16_bf16 v[16:31], v[160:163], v[236:239], v[16:31]
	ds_read_b64_tr_b16 v[236:237], v174 offset:0x1600
	ds_read_b64_tr_b16 v[238:239], v174 offset:0x1700
	v_mfma_f32_32x32x16_bf16 v[16:31], v[164:167], v[240:243], v[16:31]
	ds_read_b64_tr_b16 v[240:241], v174 offset:0x2600
	ds_read_b64_tr_b16 v[242:243], v174 offset:0x2700
	ds_read_b64_tr_b16 v[248:249], v174 offset:0x3600
	ds_read_b64_tr_b16 v[250:251], v174 offset:0x3700
	s_waitcnt lgkmcnt(0)
	v_mfma_f32_32x32x16_bf16 v[16:31], v[208:211], v[244:247], v[16:31]
	v_mfma_f32_32x32x16_bf16 v[32:47], v[156:159], v[232:235], v[32:47]
	v_max_f32_e32 v168, v81, v81
	v_max_f32_e32 v169, v80, v80
	v_max_f32_e32 v168, v169, v168
	v_max3_f32 v168, v168, v82, v83
	v_max3_f32 v168, v168, v84, v85
	v_max3_f32 v156, v168, v86, v87
	v_max3_f32 v156, v156, v88, v89
	v_max3_f32 v156, v156, v90, v91
	v_mfma_f32_32x32x16_bf16 v[32:47], v[160:163], v[236:239], v[32:47]
	v_max3_f32 v156, v156, v92, v93
	v_max3_f32 v156, v156, v94, v95
	v_max3_f32 v156, v156, v64, v65
	v_max3_f32 v156, v156, v66, v67
	v_max3_f32 v156, v156, v68, v69
	v_max3_f32 v156, v156, v70, v71
	v_max3_f32 v156, v156, v72, v73
	v_max3_f32 v156, v156, v74, v75
	v_mfma_f32_32x32x16_bf16 v[32:47], v[164:167], v[240:243], v[32:47]
	v_max3_f32 v156, v156, v76, v77
	v_max3_f32 v156, v156, v78, v79
	v_mov_b32_e32 v157, v156
	s_nop 1
	v_permlane32_swap_b32_e32 v156, v157
	v_max_f32_e32 v157, v157, v157
	v_max_f32_e32 v156, v156, v156
	v_max_f32_e32 v156, v156, v157
	v_max_f32_e32 v158, v205, v205
	v_sub_f32_e32 v157, v156, v205
	v_max_f32_e32 v156, v158, v156
	v_mfma_f32_32x32x16_bf16 v[32:47], v[208:211], v[248:251], v[32:47]
	v_sub_f32_e32 v158, v205, v156
	v_mul_f32_e32 v158, 0x3dd53b94, v158
	v_exp_f32_e32 v158, v158
	v_cmp_ge_f32_e32 vcc, s58, v157
	s_cmp_eq_u64 vcc, exec
	s_cselect_b64 s[4:5], -1, 0
	s_barrier
	s_waitcnt vmcnt(0)
	v_cndmask_b32_e64 v209, v158, 1.0, s[4:5]
	v_cmp_gt_f32_e32 vcc, 1.0, v209
	s_waitcnt vmcnt(4)
	ds_write_b128 v175, v[212:215]
	s_waitcnt vmcnt(2)
	ds_write_b128 v176, v[220:223]
	ds_write_b128 v177, v[216:219] offset:32768
	s_waitcnt vmcnt(1)
	ds_write_b128 v177, v[224:227] offset:45056
	s_waitcnt vmcnt(0)
	ds_write_b128 v178, v[228:231] offset:32768
	s_cbranch_vccz .LBB0_2227
	s_and_saveexec_b64 s[28:29], s[2:3]
	ds_write_b32 v147, v209 offset:128
	s_or_b64 exec, exec, s[28:29]
	s_waitcnt lgkmcnt(0)
	v_add_u32_e32 v157, s72, v144
	ds_read_b128 v[158:161], v157 offset:224
	ds_read_b128 v[162:165], v157 offset:192
	ds_read_b128 v[210:213], v157 offset:160
	ds_read_b128 v[214:217], v157 offset:128
	s_waitcnt lgkmcnt(3)
	v_pk_mul_f32 v[12:13], v[12:13], v[158:159]
	s_waitcnt lgkmcnt(2)
	v_pk_mul_f32 v[8:9], v[8:9], v[162:163]
	s_waitcnt lgkmcnt(1)
	v_pk_mul_f32 v[4:5], v[4:5], v[210:211]
	v_pk_mul_f32 v[14:15], v[14:15], v[160:161]
	v_pk_mul_f32 v[10:11], v[10:11], v[164:165]
	v_pk_mul_f32 v[6:7], v[6:7], v[212:213]
	s_waitcnt lgkmcnt(0)
	v_pk_mul_f32 v[2:3], v[2:3], v[216:217]
	v_pk_mul_f32 v[0:1], v[0:1], v[214:215]
	v_pk_mul_f32 v[60:61], v[60:61], v[158:159]
	v_pk_mul_f32 v[56:57], v[56:57], v[162:163]
	v_pk_mul_f32 v[52:53], v[52:53], v[210:211]
	v_pk_mul_f32 v[62:63], v[62:63], v[160:161]
	v_pk_mul_f32 v[58:59], v[58:59], v[164:165]
	v_pk_mul_f32 v[54:55], v[54:55], v[212:213]
	v_pk_mul_f32 v[50:51], v[50:51], v[216:217]
	v_pk_mul_f32 v[48:49], v[48:49], v[214:215]
	v_pk_mul_f32 v[28:29], v[28:29], v[158:159]
	v_pk_mul_f32 v[24:25], v[24:25], v[162:163]
	v_pk_mul_f32 v[20:21], v[20:21], v[210:211]
	v_pk_mul_f32 v[30:31], v[30:31], v[160:161]
	v_pk_mul_f32 v[26:27], v[26:27], v[164:165]
	v_pk_mul_f32 v[22:23], v[22:23], v[212:213]
	v_pk_mul_f32 v[18:19], v[18:19], v[216:217]
	v_pk_mul_f32 v[16:17], v[16:17], v[214:215]
	v_pk_mul_f32 v[44:45], v[44:45], v[158:159]
	v_pk_mul_f32 v[40:41], v[40:41], v[162:163]
	v_pk_mul_f32 v[36:37], v[36:37], v[210:211]
	v_pk_mul_f32 v[46:47], v[46:47], v[160:161]
	v_pk_mul_f32 v[42:43], v[42:43], v[164:165]
	v_pk_mul_f32 v[38:39], v[38:39], v[212:213]
	v_pk_mul_f32 v[34:35], v[34:35], v[216:217]
	v_pk_mul_f32 v[32:33], v[32:33], v[214:215]
.LBB0_2227:
	v_cndmask_b32_e64 v156, v156, v205, s[4:5]
	v_mul_f32_e32 v213, 0xbdd53b94, v156
	v_fmamk_f32 v87, v87, 0x3dd53b94, v213
	v_exp_f32_e32 v208, v87
	v_fmamk_f32 v80, v80, 0x3dd53b94, v213
	v_fmamk_f32 v81, v81, 0x3dd53b94, v213
	v_fmamk_f32 v82, v82, 0x3dd53b94, v213
	v_fmamk_f32 v83, v83, 0x3dd53b94, v213
	v_fmamk_f32 v84, v84, 0x3dd53b94, v213
	v_fmamk_f32 v85, v85, 0x3dd53b94, v213
	v_fmamk_f32 v86, v86, 0x3dd53b94, v213
	v_fmamk_f32 v88, v88, 0x3dd53b94, v213
	v_fmamk_f32 v89, v89, 0x3dd53b94, v213
	v_fmamk_f32 v90, v90, 0x3dd53b94, v213
	v_fmamk_f32 v91, v91, 0x3dd53b94, v213
	v_fmamk_f32 v92, v92, 0x3dd53b94, v213
	v_fmamk_f32 v93, v93, 0x3dd53b94, v213
	v_fmamk_f32 v94, v94, 0x3dd53b94, v213
	v_fmamk_f32 v95, v95, 0x3dd53b94, v213
	v_fmamk_f32 v227, v68, 0x3dd53b94, v213
	v_fmamk_f32 v228, v77, 0x3dd53b94, v213
	v_fmamk_f32 v223, v64, 0x3dd53b94, v213
	v_fmamk_f32 v224, v65, 0x3dd53b94, v213
	v_fmamk_f32 v225, v66, 0x3dd53b94, v213
	v_fmamk_f32 v226, v67, 0x3dd53b94, v213
	v_fmamk_f32 v215, v69, 0x3dd53b94, v213
	v_fmamk_f32 v217, v70, 0x3dd53b94, v213
	v_fmamk_f32 v218, v71, 0x3dd53b94, v213
	v_fmamk_f32 v219, v72, 0x3dd53b94, v213
	v_fmamk_f32 v220, v73, 0x3dd53b94, v213
	v_fmamk_f32 v221, v74, 0x3dd53b94, v213
	v_fmamk_f32 v222, v75, 0x3dd53b94, v213
	v_fmamk_f32 v214, v76, 0x3dd53b94, v213
	v_exp_f32_e32 v165, v80
	v_exp_f32_e32 v167, v81
	v_exp_f32_e32 v205, v82
	v_exp_f32_e32 v210, v83
	v_exp_f32_e32 v211, v84
	v_exp_f32_e32 v212, v85
	v_exp_f32_e32 v166, v86
	v_exp_f32_e32 v158, v88
	v_exp_f32_e32 v161, v89
	v_exp_f32_e32 v162, v90
	v_exp_f32_e32 v164, v91
	v_exp_f32_e32 v157, v92
	v_exp_f32_e32 v159, v93
	v_exp_f32_e32 v160, v94
	v_exp_f32_e32 v163, v95
	v_fmamk_f32 v229, v78, 0x3dd53b94, v213
	v_fmac_f32_e32 v213, 0x3dd53b94, v79
	s_waitcnt lgkmcnt(0)
	s_barrier
	ds_read_b128 v[64:67], v179 offset:32768
	ds_read_b128 v[68:71], v179 offset:45056
	ds_read_b128 v[230:233], v180 offset:32768
	ds_read_b128 v[234:237], v180 offset:45056
	v_exp_f32_e32 v168, v223
	v_exp_f32_e32 v169, v224
	s_waitcnt lgkmcnt(3)
	v_mfma_f32_32x32x16_bf16 v[80:95], v[64:67], v[140:143], 0
	v_exp_f32_e32 v223, v225
	v_exp_f32_e32 v224, v226
	v_exp_f32_e32 v225, v227
	v_exp_f32_e32 v226, v215
	v_exp_f32_e32 v218, v218
	v_exp_f32_e32 v219, v219
	v_exp_f32_e32 v220, v220
	s_waitcnt lgkmcnt(2)
	v_mfma_f32_32x32x16_bf16 v[64:79], v[68:71], v[140:143], 0
	v_exp_f32_e32 v221, v221
	v_exp_f32_e32 v222, v222
	v_exp_f32_e32 v229, v229
	v_cvt_pk_bf16_f32 v215, v205, v210
	v_cvt_pk_bf16_f32 v216, v211, v212
	s_waitcnt lgkmcnt(1)
	v_mfma_f32_32x32x16_bf16 v[80:95], v[230:233], v[136:139], v[80:95]
	s_waitcnt lgkmcnt(0)
	v_mfma_f32_32x32x16_bf16 v[64:79], v[234:237], v[136:139], v[64:79]
	ds_read_b128 v[230:233], v181 offset:32768
	ds_read_b128 v[234:237], v181 offset:45056
	s_waitcnt lgkmcnt(1)
	v_mfma_f32_32x32x16_bf16 v[80:95], v[230:233], v[132:135], v[80:95]
	s_waitcnt lgkmcnt(0)
	v_mfma_f32_32x32x16_bf16 v[64:79], v[234:237], v[132:135], v[64:79]
	ds_read_b128 v[230:233], v182 offset:32768
	ds_read_b128 v[234:237], v182 offset:45056
	s_waitcnt lgkmcnt(1)
	v_mfma_f32_32x32x16_bf16 v[80:95], v[230:233], v[128:131], v[80:95]
	s_waitcnt lgkmcnt(0)
	v_mfma_f32_32x32x16_bf16 v[64:79], v[234:237], v[128:131], v[64:79]
	ds_read_b128 v[230:233], v183 offset:32768
	ds_read_b128 v[234:237], v183 offset:45056
	s_waitcnt lgkmcnt(1)
	v_mfma_f32_32x32x16_bf16 v[80:95], v[230:233], v[124:127], v[80:95]
	s_waitcnt lgkmcnt(0)
	v_mfma_f32_32x32x16_bf16 v[64:79], v[234:237], v[124:127], v[64:79]
	ds_read_b128 v[230:233], v184 offset:32768
	ds_read_b128 v[234:237], v184 offset:45056
	s_waitcnt lgkmcnt(1)
	v_mfma_f32_32x32x16_bf16 v[80:95], v[230:233], v[120:123], v[80:95]
	s_waitcnt lgkmcnt(0)
	v_mfma_f32_32x32x16_bf16 v[64:79], v[234:237], v[120:123], v[64:79]
	ds_read_b128 v[230:233], v185 offset:32768
	ds_read_b128 v[234:237], v185 offset:45056
	s_waitcnt lgkmcnt(1)
	v_mfma_f32_32x32x16_bf16 v[80:95], v[230:233], v[116:119], v[80:95]
	s_waitcnt lgkmcnt(0)
	v_mfma_f32_32x32x16_bf16 v[64:79], v[234:237], v[116:119], v[64:79]
	ds_read_b128 v[230:233], v186 offset:32768
	ds_read_b128 v[234:237], v186 offset:45056
	s_waitcnt lgkmcnt(1)
	v_mfma_f32_32x32x16_bf16 v[80:95], v[230:233], v[112:115], v[80:95]
	s_waitcnt lgkmcnt(0)
	v_mfma_f32_32x32x16_bf16 v[64:79], v[234:237], v[112:115], v[64:79]
	ds_read_b128 v[230:233], v187 offset:32768
	ds_read_b128 v[234:237], v187 offset:45056
	s_waitcnt lgkmcnt(1)
	v_mfma_f32_32x32x16_bf16 v[80:95], v[230:233], v[108:111], v[80:95]
	s_waitcnt lgkmcnt(0)
	v_mfma_f32_32x32x16_bf16 v[64:79], v[234:237], v[108:111], v[64:79]
	ds_read_b128 v[230:233], v188 offset:32768
	ds_read_b128 v[234:237], v188 offset:45056
	s_waitcnt lgkmcnt(1)
	v_mfma_f32_32x32x16_bf16 v[80:95], v[230:233], v[104:107], v[80:95]
	s_waitcnt lgkmcnt(0)
	v_mfma_f32_32x32x16_bf16 v[64:79], v[234:237], v[104:107], v[64:79]
	ds_read_b128 v[230:233], v189 offset:32768
	ds_read_b128 v[234:237], v189 offset:45056
	s_waitcnt lgkmcnt(1)
	v_mfma_f32_32x32x16_bf16 v[80:95], v[230:233], v[100:103], v[80:95]
	s_waitcnt lgkmcnt(0)
	v_mfma_f32_32x32x16_bf16 v[64:79], v[234:237], v[100:103], v[64:79]
	ds_read_b128 v[230:233], v190 offset:32768
	ds_read_b128 v[234:237], v190 offset:45056
	s_waitcnt lgkmcnt(1)
	v_mfma_f32_32x32x16_bf16 v[80:95], v[230:233], v[96:99], v[80:95]
	v_exp_f32_e32 v233, v213
	v_add_f32_e32 v213, 0, v165
	v_add_f32_e32 v213, v167, v213
	v_add_f32_e32 v213, v205, v213
	v_add_f32_e32 v213, v210, v213
	v_add_f32_e32 v213, v211, v213
	v_add_f32_e32 v213, v212, v213
	v_add_f32_e32 v213, v166, v213
	v_add_f32_e32 v213, v208, v213
	v_add_f32_e32 v213, v158, v213
	v_add_f32_e32 v213, v161, v213
	v_add_f32_e32 v213, v162, v213
	v_add_f32_e32 v213, v164, v213
	v_add_f32_e32 v213, v157, v213
	v_add_f32_e32 v213, v159, v213
	v_add_f32_e32 v213, v160, v213
	v_add_f32_e32 v213, v163, v213
	v_add_f32_e32 v213, v168, v213
	v_add_f32_e32 v213, v169, v213
	v_exp_f32_e32 v230, v217
	v_add_f32_e32 v213, v223, v213
	v_add_f32_e32 v213, v224, v213
	v_add_f32_e32 v213, v225, v213
	v_add_f32_e32 v213, v226, v213
	v_add_f32_e32 v213, v230, v213
	v_add_f32_e32 v213, v218, v213
	v_exp_f32_e32 v231, v214
	v_add_f32_e32 v213, v219, v213
	v_exp_f32_e32 v232, v228
	v_add_f32_e32 v213, v220, v213
	s_waitcnt lgkmcnt(0)
	v_mfma_f32_32x32x16_bf16 v[64:79], v[234:237], v[96:99], v[64:79]
	v_add_f32_e32 v213, v221, v213
	v_add_f32_e32 v213, v222, v213
	v_add_f32_e32 v213, v231, v213
	v_add_f32_e32 v213, v232, v213
	v_add_f32_e32 v213, v229, v213
	v_add_f32_e32 v227, v233, v213
	v_mov_b32_e32 v228, v227
	s_nop 1
	v_permlane32_swap_b32_e32 v227, v228
	v_cvt_pk_bf16_f32 v214, v165, v167
	v_cvt_pk_bf16_f32 v217, v166, v208
	v_cvt_pk_bf16_f32 v210, v158, v161
	v_cvt_pk_bf16_f32 v211, v162, v164
	v_cvt_pk_bf16_f32 v212, v157, v159
	v_cvt_pk_bf16_f32 v213, v160, v163
	v_cvt_pk_bf16_f32 v158, v168, v169
	v_cvt_pk_bf16_f32 v159, v223, v224
	v_cvt_pk_bf16_f32 v160, v225, v226
	v_cvt_pk_bf16_f32 v161, v230, v218
	v_cvt_pk_bf16_f32 v162, v219, v220
	v_cvt_pk_bf16_f32 v163, v221, v222
	v_cvt_pk_bf16_f32 v164, v231, v232
	v_cvt_pk_bf16_f32 v165, v229, v233
	v_add_co_u32_e32 v166, vcc, s64, v152
	s_nop 1
	v_addc_co_u32_e32 v167, vcc, 0, v153, vcc
	v_add_co_u32_e32 v152, vcc, s65, v152
	s_nop 1
	v_addc_co_u32_e32 v153, vcc, 0, v153, vcc
	global_load_dwordx4 v[218:221], v[166:167], off offset:768
	global_load_dwordx4 v[222:225], v[166:167], off offset:512
	global_load_dwordx4 v[230:233], v[152:153], off offset:768
	global_load_dwordx4 v[234:237], v[152:153], off offset:512
	v_add_co_u32_e32 v152, vcc, s66, v154
	s_nop 1
	v_addc_co_u32_e32 v153, vcc, 0, v155, vcc
	global_load_dwordx4 v[238:241], v[152:153], off offset:512
	ds_read_b64_tr_b16 v[152:153], v173 offset:0x0
	ds_read_b64_tr_b16 v[154:155], v173 offset:0x100
	ds_read_b64_tr_b16 v[242:243], v173 offset:0x1000
	ds_read_b64_tr_b16 v[244:245], v173 offset:0x1100
	ds_read_b64_tr_b16 v[246:247], v173 offset:0x2000
	ds_read_b64_tr_b16 v[248:249], v173 offset:0x2100
	ds_read_b64_tr_b16 v[250:251], v173 offset:0x3000
	ds_read_b64_tr_b16 v[252:253], v173 offset:0x3100
	s_waitcnt lgkmcnt(0)
	s_nop 0
	v_mfma_f32_32x32x16_bf16 v[0:15], v[214:217], v[152:155], v[0:15]
	ds_read_b64_tr_b16 v[152:153], v173 offset:0x200
	ds_read_b64_tr_b16 v[154:155], v173 offset:0x300
	v_mfma_f32_32x32x16_bf16 v[0:15], v[210:213], v[242:245], v[0:15]
	ds_read_b64_tr_b16 v[242:243], v173 offset:0x1200
	ds_read_b64_tr_b16 v[244:245], v173 offset:0x1300
	v_mfma_f32_32x32x16_bf16 v[0:15], v[158:161], v[246:249], v[0:15]
	ds_read_b64_tr_b16 v[246:247], v173 offset:0x2200
	ds_read_b64_tr_b16 v[248:249], v173 offset:0x2300
	ds_read_b64_tr_b16 v[166:167], v173 offset:0x3200
	ds_read_b64_tr_b16 v[168:169], v173 offset:0x3300
	s_waitcnt lgkmcnt(0)
	v_mfma_f32_32x32x16_bf16 v[0:15], v[162:165], v[250:253], v[0:15]
	v_mfma_f32_32x32x16_bf16 v[48:63], v[214:217], v[152:155], v[48:63]
	ds_read_b64_tr_b16 v[152:153], v173 offset:0x400
	ds_read_b64_tr_b16 v[154:155], v173 offset:0x500
	v_mfma_f32_32x32x16_bf16 v[48:63], v[210:213], v[242:245], v[48:63]
	ds_read_b64_tr_b16 v[242:243], v173 offset:0x1400
	ds_read_b64_tr_b16 v[244:245], v173 offset:0x1500
	v_mfma_f32_32x32x16_bf16 v[48:63], v[158:161], v[246:249], v[48:63]
	ds_read_b64_tr_b16 v[246:247], v173 offset:0x2400
	ds_read_b64_tr_b16 v[248:249], v173 offset:0x2500
	ds_read_b64_tr_b16 v[250:251], v173 offset:0x3400
	ds_read_b64_tr_b16 v[252:253], v173 offset:0x3500
	s_waitcnt lgkmcnt(0)
	v_mfma_f32_32x32x16_bf16 v[48:63], v[162:165], v[166:169], v[48:63]
	v_mfma_f32_32x32x16_bf16 v[16:31], v[214:217], v[152:155], v[16:31]
	ds_read_b64_tr_b16 v[152:153], v173 offset:0x600
	ds_read_b64_tr_b16 v[154:155], v173 offset:0x700
	ds_read_b64_tr_b16 v[166:167], v173 offset:0x1600
	ds_read_b64_tr_b16 v[168:169], v173 offset:0x1700
	v_mfma_f32_32x32x16_bf16 v[16:31], v[210:213], v[242:245], v[16:31]
	ds_read_b64_tr_b16 v[242:243], v173 offset:0x2600
	ds_read_b64_tr_b16 v[244:245], v173 offset:0x2700
	v_mfma_f32_32x32x16_bf16 v[16:31], v[158:161], v[246:249], v[16:31]
	ds_read_b64_tr_b16 v[246:247], v173 offset:0x3600
	ds_read_b64_tr_b16 v[248:249], v173 offset:0x3700
	s_waitcnt lgkmcnt(0)
	v_mfma_f32_32x32x16_bf16 v[16:31], v[162:165], v[250:253], v[16:31]
	v_mfma_f32_32x32x16_bf16 v[32:47], v[214:217], v[152:155], v[32:47]
	v_max_f32_e32 v157, v81, v81
	v_max_f32_e32 v205, v80, v80
	v_max_f32_e32 v157, v205, v157
	v_max3_f32 v157, v157, v82, v83
	v_max3_f32 v157, v157, v84, v85
	v_max3_f32 v152, v157, v86, v87
	v_max3_f32 v152, v152, v88, v89
	v_max3_f32 v152, v152, v90, v91
	v_mfma_f32_32x32x16_bf16 v[32:47], v[210:213], v[166:169], v[32:47]
	v_max3_f32 v152, v152, v92, v93
	v_max3_f32 v152, v152, v94, v95
	v_max3_f32 v152, v152, v64, v65
	v_max3_f32 v152, v152, v66, v67
	v_max3_f32 v152, v152, v68, v69
	v_max3_f32 v152, v152, v70, v71
	v_max3_f32 v152, v152, v72, v73
	v_max3_f32 v152, v152, v74, v75
	v_mfma_f32_32x32x16_bf16 v[32:47], v[158:161], v[242:245], v[32:47]
	v_max3_f32 v152, v152, v76, v77
	v_max3_f32 v152, v152, v78, v79
	v_mov_b32_e32 v153, v152
	s_nop 1
	v_permlane32_swap_b32_e32 v152, v153
	v_max_f32_e32 v153, v153, v153
	v_max_f32_e32 v152, v152, v152
	v_max_f32_e32 v152, v152, v153
	v_max_f32_e32 v154, v156, v156
	v_sub_f32_e32 v153, v152, v156
	v_max_f32_e32 v152, v154, v152
	v_mfma_f32_32x32x16_bf16 v[32:47], v[162:165], v[246:249], v[32:47]
	v_sub_f32_e32 v154, v156, v152
	v_mul_f32_e32 v154, 0x3dd53b94, v154
	v_exp_f32_e32 v154, v154
	v_cmp_ge_f32_e32 vcc, s58, v153
	s_cmp_eq_u64 vcc, exec
	s_cselect_b64 s[4:5], -1, 0
	s_barrier
	s_waitcnt vmcnt(0)
	v_cndmask_b32_e64 v208, v154, 1.0, s[4:5]
	v_cmp_gt_f32_e32 vcc, 1.0, v208
	s_waitcnt vmcnt(4)
	ds_write_b128 v175, v[218:221] offset:16384
	s_waitcnt vmcnt(2)
	ds_write_b128 v176, v[230:233] offset:16384
	ds_write_b128 v177, v[222:225] offset:57344
	s_waitcnt vmcnt(1)
	ds_write_b128 v191, v[234:237] offset:57344
	s_waitcnt vmcnt(0)
	ds_write_b128 v178, v[238:241] offset:57344
	s_cbranch_vccz .LBB0_2231
	s_and_saveexec_b64 s[28:29], s[2:3]
	ds_write_b32 v147, v208 offset:128
	s_or_b64 exec, exec, s[28:29]
	s_waitcnt lgkmcnt(0)
	v_add_u32_e32 v153, s72, v144
	ds_read_b128 v[158:161], v153 offset:224
	ds_read_b128 v[162:165], v153 offset:192
	ds_read_b128 v[166:169], v153 offset:160
	ds_read_b128 v[210:213], v153 offset:128
	s_waitcnt lgkmcnt(3)
	v_pk_mul_f32 v[12:13], v[12:13], v[158:159]
	s_waitcnt lgkmcnt(2)
	v_pk_mul_f32 v[8:9], v[8:9], v[162:163]
	s_waitcnt lgkmcnt(1)
	v_pk_mul_f32 v[4:5], v[4:5], v[166:167]
	v_pk_mul_f32 v[14:15], v[14:15], v[160:161]
	v_pk_mul_f32 v[10:11], v[10:11], v[164:165]
	v_pk_mul_f32 v[6:7], v[6:7], v[168:169]
	s_waitcnt lgkmcnt(0)
	v_pk_mul_f32 v[2:3], v[2:3], v[212:213]
	v_pk_mul_f32 v[0:1], v[0:1], v[210:211]
	v_pk_mul_f32 v[60:61], v[60:61], v[158:159]
	v_pk_mul_f32 v[56:57], v[56:57], v[162:163]
	v_pk_mul_f32 v[52:53], v[52:53], v[166:167]
	v_pk_mul_f32 v[62:63], v[62:63], v[160:161]
	v_pk_mul_f32 v[58:59], v[58:59], v[164:165]
	v_pk_mul_f32 v[54:55], v[54:55], v[168:169]
	v_pk_mul_f32 v[50:51], v[50:51], v[212:213]
	v_pk_mul_f32 v[48:49], v[48:49], v[210:211]
	v_pk_mul_f32 v[28:29], v[28:29], v[158:159]
	v_pk_mul_f32 v[24:25], v[24:25], v[162:163]
	v_pk_mul_f32 v[20:21], v[20:21], v[166:167]
	v_pk_mul_f32 v[30:31], v[30:31], v[160:161]
	v_pk_mul_f32 v[26:27], v[26:27], v[164:165]
	v_pk_mul_f32 v[22:23], v[22:23], v[168:169]
	v_pk_mul_f32 v[18:19], v[18:19], v[212:213]
	v_pk_mul_f32 v[16:17], v[16:17], v[210:211]
	v_pk_mul_f32 v[44:45], v[44:45], v[158:159]
	v_pk_mul_f32 v[40:41], v[40:41], v[162:163]
	v_pk_mul_f32 v[36:37], v[36:37], v[166:167]
	v_pk_mul_f32 v[46:47], v[46:47], v[160:161]
	v_pk_mul_f32 v[42:43], v[42:43], v[164:165]
	v_pk_mul_f32 v[38:39], v[38:39], v[168:169]
	v_pk_mul_f32 v[34:35], v[34:35], v[212:213]
	v_pk_mul_f32 v[32:33], v[32:33], v[210:211]

.LBB0_2233:
	ds_read_b128 v[64:67], v179 offset:57344
	ds_read_b128 v[148:151], v180 offset:57344
	v_exp_f32_e32 v162, v162
	v_exp_f32_e32 v163, v163
	v_exp_f32_e32 v160, v160
	s_waitcnt lgkmcnt(1)
	v_mfma_f32_32x32x16_bf16 v[80:95], v[64:67], v[140:143], 0
	ds_read_b128 v[64:67], v203 offset:57344
	ds_read_b128 v[176:179], v204 offset:57344
	v_exp_f32_e32 v161, v161
	v_exp_f32_e32 v156, v156
	s_waitcnt lgkmcnt(1)
	v_mfma_f32_32x32x16_bf16 v[64:79], v[64:67], v[140:143], 0
	v_mfma_f32_32x32x16_bf16 v[80:95], v[148:151], v[136:139], v[80:95]
	s_waitcnt lgkmcnt(0)
	v_mfma_f32_32x32x16_bf16 v[64:79], v[176:179], v[136:139], v[64:79]
	ds_read_b128 v[136:139], v181 offset:57344
	ds_read_b128 v[140:143], v182 offset:57344
	s_waitcnt lgkmcnt(1)
	v_mfma_f32_32x32x16_bf16 v[80:95], v[136:139], v[132:135], v[80:95]
	ds_read_b128 v[136:139], v201 offset:57344
	ds_read_b128 v[148:151], v202 offset:57344
	s_waitcnt lgkmcnt(1)
	v_mfma_f32_32x32x16_bf16 v[64:79], v[136:139], v[132:135], v[64:79]
	v_mfma_f32_32x32x16_bf16 v[80:95], v[140:143], v[128:131], v[80:95]
	s_waitcnt lgkmcnt(0)
	v_mfma_f32_32x32x16_bf16 v[64:79], v[148:151], v[128:131], v[64:79]
	ds_read_b128 v[128:131], v183 offset:57344
	ds_read_b128 v[132:135], v184 offset:57344
	s_waitcnt lgkmcnt(1)
	v_mfma_f32_32x32x16_bf16 v[80:95], v[128:131], v[124:127], v[80:95]
	ds_read_b128 v[128:131], v199 offset:57344
	ds_read_b128 v[136:139], v200 offset:57344
	s_waitcnt lgkmcnt(1)
	v_mfma_f32_32x32x16_bf16 v[64:79], v[128:131], v[124:127], v[64:79]
	ds_read_b128 v[124:127], v185 offset:57344
	ds_read_b128 v[128:131], v186 offset:57344
	v_mfma_f32_32x32x16_bf16 v[80:95], v[132:135], v[120:123], v[80:95]
	ds_read_b128 v[132:135], v197 offset:57344
	ds_read_b128 v[140:143], v198 offset:57344
	ds_read_b128 v[148:151], v187 offset:57344
	ds_read_b128 v[176:179], v188 offset:57344
	ds_read_b128 v[180:183], v194 offset:57344
	ds_read_b128 v[184:187], v195 offset:57344
	ds_read_b128 v[194:197], v189 offset:57344
	ds_read_b128 v[188:191], v190 offset:57344
	s_waitcnt lgkmcnt(10)
	v_mfma_f32_32x32x16_bf16 v[64:79], v[136:139], v[120:123], v[64:79]
	ds_read_b128 v[120:123], v192 offset:57344
	ds_read_b128 v[136:139], v193 offset:57344
	s_waitcnt lgkmcnt(11)
	v_mfma_f32_32x32x16_bf16 v[80:95], v[124:127], v[116:119], v[80:95]
	v_exp_f32_e32 v124, v157
	v_exp_f32_e32 v125, v154
	v_exp_f32_e32 v126, v155
	v_exp_f32_e32 v127, v152
	v_exp_f32_e32 v152, v153
	v_exp_f32_e32 v153, v166
	v_exp_f32_e32 v154, v167
	s_waitcnt lgkmcnt(9)
	v_mfma_f32_32x32x16_bf16 v[64:79], v[132:135], v[116:119], v[64:79]
	v_add_f32_e32 v116, 0, v219
	v_add_f32_e32 v116, v220, v116
	v_add_f32_e32 v116, v221, v116
	v_add_f32_e32 v116, v223, v116
	v_add_f32_e32 v116, v224, v116
	v_add_f32_e32 v116, v226, v116
	v_add_f32_e32 v116, v222, v116
	v_mfma_f32_32x32x16_bf16 v[80:95], v[128:131], v[112:115], v[80:95]
	v_add_f32_e32 v116, v225, v116
	v_add_f32_e32 v116, v210, v116
	v_add_f32_e32 v116, v212, v116
	v_exp_f32_e32 v118, v164
	v_exp_f32_e32 v119, v165
	v_exp_f32_e32 v132, v158
	v_exp_f32_e32 v133, v159
	s_waitcnt lgkmcnt(8)
	v_mfma_f32_32x32x16_bf16 v[64:79], v[140:143], v[112:115], v[64:79]
	v_add_f32_e32 v112, v213, v116
	v_add_f32_e32 v112, v217, v112
	v_add_f32_e32 v112, v211, v112
	v_add_f32_e32 v112, v214, v112
	v_add_f32_e32 v112, v215, v112
	v_add_f32_e32 v112, v218, v112
	v_add_f32_e32 v112, v162, v112
	s_waitcnt lgkmcnt(7)
	v_mfma_f32_32x32x16_bf16 v[80:95], v[148:151], v[108:111], v[80:95]
	v_add_f32_e32 v112, v163, v112
	v_add_f32_e32 v112, v160, v112
	v_add_f32_e32 v112, v161, v112
	v_add_f32_e32 v112, v156, v112
	v_add_f32_e32 v112, v124, v112
	v_add_f32_e32 v112, v125, v112
	v_add_f32_e32 v112, v126, v112
	s_waitcnt lgkmcnt(5)
	v_mfma_f32_32x32x16_bf16 v[64:79], v[180:183], v[108:111], v[64:79]
	v_add_f32_e32 v108, v127, v112
	v_add_f32_e32 v108, v152, v108
	v_add_f32_e32 v108, v153, v108
	v_add_f32_e32 v108, v154, v108
	v_add_f32_e32 v108, v118, v108
	v_add_f32_e32 v108, v119, v108
	v_add_f32_e32 v108, v132, v108
	v_mfma_f32_32x32x16_bf16 v[80:95], v[176:179], v[104:107], v[80:95]
	v_add_f32_e32 v108, v133, v108
	v_mov_b32_e32 v109, v108
	s_nop 1
	v_permlane32_swap_b32_e32 v108, v109
	v_cvt_pk_bf16_f32 v110, v219, v220
	v_cvt_pk_bf16_f32 v111, v221, v223
	v_cvt_pk_bf16_f32 v112, v224, v226
	s_waitcnt lgkmcnt(4)
	v_mfma_f32_32x32x16_bf16 v[64:79], v[184:187], v[104:107], v[64:79]
	v_cvt_pk_bf16_f32 v113, v222, v225
	v_cvt_pk_bf16_f32 v104, v210, v212
	v_cvt_pk_bf16_f32 v105, v213, v217
	v_cvt_pk_bf16_f32 v106, v211, v214
	v_cvt_pk_bf16_f32 v107, v215, v218
	v_cvt_pk_bf16_f32 v114, v162, v163
	v_cvt_pk_bf16_f32 v115, v160, v161
	s_waitcnt lgkmcnt(3)
	v_mfma_f32_32x32x16_bf16 v[80:95], v[194:197], v[100:103], v[80:95]
	v_cvt_pk_bf16_f32 v116, v156, v124
	v_cvt_pk_bf16_f32 v117, v125, v126
	s_waitcnt lgkmcnt(1)
	v_mfma_f32_32x32x16_bf16 v[64:79], v[120:123], v[100:103], v[64:79]
	v_cvt_pk_bf16_f32 v100, v127, v152
	v_cvt_pk_bf16_f32 v101, v153, v154
	v_cvt_pk_bf16_f32 v102, v118, v119
	v_cvt_pk_bf16_f32 v103, v132, v133
	v_mfma_f32_32x32x16_bf16 v[80:95], v[188:191], v[96:99], v[80:95]
	s_waitcnt lgkmcnt(0)
	v_mfma_f32_32x32x16_bf16 v[64:79], v[136:139], v[96:99], v[64:79]
	ds_read_b64_tr_b16 v[96:97], v174 offset:0x0
	ds_read_b64_tr_b16 v[98:99], v174 offset:0x100
	ds_read_b64_tr_b16 v[118:119], v174 offset:0x1000
	ds_read_b64_tr_b16 v[120:121], v174 offset:0x1100
	ds_read_b64_tr_b16 v[122:123], v174 offset:0x2000
	ds_read_b64_tr_b16 v[124:125], v174 offset:0x2100
	ds_read_b64_tr_b16 v[126:127], v174 offset:0x3000
	ds_read_b64_tr_b16 v[128:129], v174 offset:0x3100
	s_waitcnt lgkmcnt(0)
	s_nop 0
	v_mfma_f32_32x32x16_bf16 v[0:15], v[110:113], v[96:99], v[0:15]
	ds_read_b64_tr_b16 v[96:97], v174 offset:0x200
	ds_read_b64_tr_b16 v[98:99], v174 offset:0x300
	v_mfma_f32_32x32x16_bf16 v[0:15], v[104:107], v[118:121], v[0:15]
	ds_read_b64_tr_b16 v[118:119], v174 offset:0x1200
	ds_read_b64_tr_b16 v[120:121], v174 offset:0x1300
	v_mfma_f32_32x32x16_bf16 v[0:15], v[114:117], v[122:125], v[0:15]
	ds_read_b64_tr_b16 v[122:123], v174 offset:0x2200
	ds_read_b64_tr_b16 v[124:125], v174 offset:0x2300
	ds_read_b64_tr_b16 v[130:131], v174 offset:0x3200
	ds_read_b64_tr_b16 v[132:133], v174 offset:0x3300
	s_waitcnt lgkmcnt(0)
	v_mfma_f32_32x32x16_bf16 v[0:15], v[100:103], v[126:129], v[0:15]
	v_mfma_f32_32x32x16_bf16 v[48:63], v[110:113], v[96:99], v[48:63]
	ds_read_b64_tr_b16 v[96:97], v174 offset:0x400
	ds_read_b64_tr_b16 v[98:99], v174 offset:0x500
	v_mfma_f32_32x32x16_bf16 v[48:63], v[104:107], v[118:121], v[48:63]
	ds_read_b64_tr_b16 v[118:119], v174 offset:0x1400
	ds_read_b64_tr_b16 v[120:121], v174 offset:0x1500
	v_mfma_f32_32x32x16_bf16 v[48:63], v[114:117], v[122:125], v[48:63]
	ds_read_b64_tr_b16 v[122:123], v174 offset:0x2400
	ds_read_b64_tr_b16 v[124:125], v174 offset:0x2500
	ds_read_b64_tr_b16 v[126:127], v174 offset:0x3400
	ds_read_b64_tr_b16 v[128:129], v174 offset:0x3500
	s_waitcnt lgkmcnt(0)
	v_mfma_f32_32x32x16_bf16 v[48:63], v[100:103], v[130:133], v[48:63]
	v_mfma_f32_32x32x16_bf16 v[16:31], v[110:113], v[96:99], v[16:31]
	ds_read_b64_tr_b16 v[96:97], v174 offset:0x600
	ds_read_b64_tr_b16 v[98:99], v174 offset:0x700
	v_mfma_f32_32x32x16_bf16 v[16:31], v[104:107], v[118:121], v[16:31]
	ds_read_b64_tr_b16 v[118:119], v174 offset:0x1600
	ds_read_b64_tr_b16 v[120:121], v174 offset:0x1700
	v_mfma_f32_32x32x16_bf16 v[16:31], v[114:117], v[122:125], v[16:31]
	ds_read_b64_tr_b16 v[122:123], v174 offset:0x2600
	ds_read_b64_tr_b16 v[124:125], v174 offset:0x2700
	ds_read_b64_tr_b16 v[130:131], v174 offset:0x3600
	ds_read_b64_tr_b16 v[132:133], v174 offset:0x3700
	s_waitcnt lgkmcnt(0)
	v_mfma_f32_32x32x16_bf16 v[16:31], v[100:103], v[126:129], v[16:31]
	v_mfma_f32_32x32x16_bf16 v[32:47], v[110:113], v[96:99], v[32:47]
	v_max_f32_e32 v126, v81, v81
	v_max_f32_e32 v127, v80, v80
	v_max_f32_e32 v126, v127, v126
	v_max3_f32 v126, v126, v82, v83
	v_max3_f32 v126, v126, v84, v85
	v_max3_f32 v96, v126, v86, v87
	v_max3_f32 v96, v96, v88, v89
	v_max3_f32 v96, v96, v90, v91
	v_mfma_f32_32x32x16_bf16 v[32:47], v[104:107], v[118:121], v[32:47]
	v_max3_f32 v96, v96, v92, v93
	v_max3_f32 v96, v96, v94, v95
	v_max3_f32 v96, v96, v64, v65
	v_max3_f32 v96, v96, v66, v67
	v_max3_f32 v96, v96, v68, v69
	v_max3_f32 v96, v96, v70, v71
	v_max3_f32 v96, v96, v72, v73
	v_max3_f32 v96, v96, v74, v75
	v_mfma_f32_32x32x16_bf16 v[32:47], v[114:117], v[122:125], v[32:47]
	v_max3_f32 v96, v96, v76, v77
	v_max3_f32 v96, v96, v78, v79
	v_mov_b32_e32 v97, v96
	s_nop 1
	v_permlane32_swap_b32_e32 v96, v97
	v_max_f32_e32 v97, v97, v97
	v_max_f32_e32 v96, v96, v96
	v_max_f32_e32 v96, v96, v97
	v_max_f32_e32 v97, v205, v205
	v_max_f32_e32 v97, v97, v96
	v_sub_f32_e32 v98, v96, v205
	v_mfma_f32_32x32x16_bf16 v[32:47], v[100:103], v[130:133], v[32:47]
	v_sub_f32_e32 v96, v205, v97
	v_mul_f32_e32 v96, 0x3dd53b94, v96
	v_exp_f32_e32 v96, v96
	v_cmp_ge_f32_e32 vcc, s58, v98
	s_cmp_eq_u64 vcc, exec
	s_cselect_b64 s[4:5], -1, 0
	v_cndmask_b32_e64 v96, v96, 1.0, s[4:5]
	v_cmp_gt_f32_e32 vcc, 1.0, v96
	s_barrier
	s_cbranch_vccz .LBB0_2237
	s_and_saveexec_b64 s[28:29], s[2:3]
	ds_write_b32 v147, v96 offset:128
	s_or_b64 exec, exec, s[28:29]
	s_waitcnt lgkmcnt(0)
	v_add_u32_e32 v106, s72, v144
	ds_read_b128 v[98:101], v106 offset:224
	ds_read_b128 v[102:105], v106 offset:192
	ds_read_b128 v[110:113], v106 offset:160
	ds_read_b128 v[114:117], v106 offset:128
	s_waitcnt lgkmcnt(3)
	v_pk_mul_f32 v[12:13], v[12:13], v[98:99]
	s_waitcnt lgkmcnt(2)
	v_pk_mul_f32 v[8:9], v[8:9], v[102:103]
	s_waitcnt lgkmcnt(1)
	v_pk_mul_f32 v[4:5], v[4:5], v[110:111]
	v_pk_mul_f32 v[14:15], v[14:15], v[100:101]
	v_pk_mul_f32 v[10:11], v[10:11], v[104:105]
	v_pk_mul_f32 v[6:7], v[6:7], v[112:113]
	s_waitcnt lgkmcnt(0)
	v_pk_mul_f32 v[2:3], v[2:3], v[116:117]
	v_pk_mul_f32 v[0:1], v[0:1], v[114:115]
	v_pk_mul_f32 v[60:61], v[60:61], v[98:99]
	v_pk_mul_f32 v[56:57], v[56:57], v[102:103]
	v_pk_mul_f32 v[52:53], v[52:53], v[110:111]
	v_pk_mul_f32 v[62:63], v[62:63], v[100:101]
	v_pk_mul_f32 v[58:59], v[58:59], v[104:105]
	v_pk_mul_f32 v[54:55], v[54:55], v[112:113]
	v_pk_mul_f32 v[50:51], v[50:51], v[116:117]
	v_pk_mul_f32 v[48:49], v[48:49], v[114:115]
	v_pk_mul_f32 v[28:29], v[28:29], v[98:99]
	v_pk_mul_f32 v[24:25], v[24:25], v[102:103]
	v_pk_mul_f32 v[20:21], v[20:21], v[110:111]
	v_pk_mul_f32 v[30:31], v[30:31], v[100:101]
	v_pk_mul_f32 v[26:27], v[26:27], v[104:105]
	v_pk_mul_f32 v[22:23], v[22:23], v[112:113]
	v_pk_mul_f32 v[18:19], v[18:19], v[116:117]
	v_pk_mul_f32 v[16:17], v[16:17], v[114:115]
	v_pk_mul_f32 v[44:45], v[44:45], v[98:99]
	v_pk_mul_f32 v[40:41], v[40:41], v[102:103]
	v_pk_mul_f32 v[36:37], v[36:37], v[110:111]
	v_pk_mul_f32 v[46:47], v[46:47], v[100:101]
	v_pk_mul_f32 v[42:43], v[42:43], v[104:105]
	v_pk_mul_f32 v[38:39], v[38:39], v[112:113]
	v_pk_mul_f32 v[34:35], v[34:35], v[116:117]
	v_pk_mul_f32 v[32:33], v[32:33], v[114:115]
